# P0: gain vector loaded once before the row loop (was one round trip per piece per row); P12 expert weights: a token's 16 ids, gates and row scales fetched together
# speedup vs baseline: 1.0484x; 1.0061x over previous
; __device__ __forceinline__ float wave_sum(float v) { v = dpp_add16(v); return (rdlane(v, 0) + rdlane(v, 16)) + (rdlane(v, 32) + rdlane(v, 48)); }
; __device__ __forceinline__ void rms_row_to_both(const float* xrow, const float* g, bf16* orow, unsigned char* orow8, int lane) {
;     const f32x4* xr = (const f32x4*)xrow + lane; const f32x4* gr = (const f32x4*)g + lane;
;     f32x4 v[16]; float s = 0.f;
; #pragma unroll
;     for (int j = 0; j < 16; ++j) { v[j] = xr[64 * j]; s += (v[j].x * v[j].x + v[j].y * v[j].y) + (v[j].z * v[j].z + v[j].w * v[j].w); }
;     const float rs = 1.0f / sqrtf(wave_sum(s) * (1.f / D_) + 1e-6f);
;     unsigned* o4 = (unsigned*)orow8 + lane; (void)orow;
; #pragma unroll
;     for (int j = 0; j < 16; ++j) { const f32x4 y = v[j] * rs * gr[64 * j]; o4[64 * j] = pk4_i8(y.x * I8_SA, y.y * I8_SA, y.z * I8_SA, y.w * I8_SA); }
; __device__ __forceinline__ void p0_prologue(Frame& F) {
;     ...
;     for (int m = F.gw; m < S_; m += F.NGW) rms_row_to_both(F.in[0] + (size_t)m * D_, F.in[1], (bf16*)(F.ws + WS_XN) + (size_t)m * D_, F.ws + WS_XN8 + (size_t)m * D_, F.lane);
.LBB0_47:
	s_or_b64 exec, exec, s[6:7]
	s_cmpk_gt_i32 s94, 0x1fff
	s_cbranch_scc1 .LBB0_51
	v_ashrrev_i32_e32 v7, 31, v6
	v_lshlrev_b64 v[2:3], 4, v[6:7]
	v_lshl_add_u64 v[70:71], s[38:39], 0, v[2:3]
	s_mov_b64 s[0:1], 0x1000
	v_lshl_add_u64 v[72:73], v[70:71], 0, s[0:1]
	s_mov_b64 s[0:1], 0x1400
	v_lshl_add_u64 v[74:75], v[70:71], 0, s[0:1]
	s_mov_b64 s[0:1], 0x1800
	v_lshl_add_u64 v[76:77], v[70:71], 0, s[0:1]
	s_mov_b64 s[0:1], 0x1c00
	v_lshl_add_u64 v[78:79], v[70:71], 0, s[0:1]
	s_mov_b64 s[0:1], 0x2000
	v_lshl_add_u64 v[80:81], v[70:71], 0, s[0:1]
	s_mov_b64 s[0:1], 0x2400
	v_lshl_add_u64 v[82:83], v[70:71], 0, s[0:1]
	s_mov_b64 s[0:1], 0x2800
	v_lshl_add_u64 v[84:85], v[70:71], 0, s[0:1]
	s_mov_b64 s[0:1], 0x2c00
	v_lshl_add_u64 v[86:87], v[70:71], 0, s[0:1]
	s_mov_b64 s[0:1], 0x3000
	v_lshl_add_u64 v[88:89], v[70:71], 0, s[0:1]
	s_mov_b64 s[0:1], 0x3400
	v_lshl_add_u64 v[90:91], v[70:71], 0, s[0:1]
	s_mov_b64 s[0:1], 0x3800
	s_mov_b32 s33, s95
	v_lshl_add_u64 v[92:93], v[70:71], 0, s[0:1]
	s_mov_b64 s[0:1], 0x3c00
	s_ashr_i32 s95, s94, 31
	v_lshl_add_u64 v[94:95], v[70:71], 0, s[0:1]
	s_lshl_b64 s[0:1], s[94:95], 14
	s_add_u32 s0, s36, s0
	s_addc_u32 s1, s37, s1
	s_ashr_i32 s35, s34, 31
	v_lshl_add_u64 v[96:97], s[0:1], 0, v[2:3]
	s_lshl_b64 s[4:5], s[34:35], 14
	s_lshl_b64 s[0:1], s[94:95], 12
	s_add_u32 s0, s68, s0
	s_addc_u32 s1, s69, s1
	v_lshl_add_u64 v[2:3], v[6:7], 2, s[0:1]
	s_mov_b64 s[0:1], 0x1dc00000
	v_lshl_add_u64 v[98:99], v[2:3], 0, s[0:1]
	s_lshl_b64 s[6:7], s[34:35], 12
	s_movk_i32 s3, 0x1000
	s_movk_i32 s8, 0x2000
	s_movk_i32 s9, 0x3000
	v_mov_b32_e32 v1, 0x358637bd
	s_mov_b32 s10, 0xf800000
	v_mov_b32_e32 v101, 0x260
	s_mov_b32 s11, 0xc2fe0000
	v_mov_b32_e32 v102, 0x42fe0000
	s_mov_b32 s28, 0x40c0c00
	s_mov_b32 s29, s94
	global_load_dwordx4 v[164:167], v[70:71], off offset:1024
	global_load_dwordx4 v[168:171], v[70:71], off offset:2048
	global_load_dwordx4 v[172:175], v[70:71], off offset:3072
	global_load_dwordx4 v[176:179], v[72:73], off
	global_load_dwordx4 v[180:183], v[74:75], off
	global_load_dwordx4 v[184:187], v[76:77], off
	global_load_dwordx4 v[188:191], v[78:79], off
	global_load_dwordx4 v[192:195], v[80:81], off
	global_load_dwordx4 v[196:199], v[82:83], off
	global_load_dwordx4 v[200:203], v[84:85], off
	global_load_dwordx4 v[204:207], v[86:87], off
	global_load_dwordx4 v[208:211], v[88:89], off
	global_load_dwordx4 v[212:215], v[90:91], off
	global_load_dwordx4 v[216:219], v[92:93], off
	global_load_dwordx4 v[220:223], v[94:95], off
.LBB0_49:
	global_load_dwordx4 v[26:29], v[96:97], off
	global_load_dwordx4 v[22:25], v[96:97], off offset:1024
	global_load_dwordx4 v[54:57], v[96:97], off offset:2048
	global_load_dwordx4 v[42:45], v[96:97], off offset:3072
	v_add_co_u32_e32 v2, vcc, s3, v96
	s_add_i32 s29, s29, s34
	s_nop 0
	v_addc_co_u32_e32 v3, vcc, 0, v97, vcc
	v_add_co_u32_e32 v4, vcc, s8, v96
	s_cmpk_lt_i32 s29, 0x2000
	s_nop 0
	v_addc_co_u32_e32 v5, vcc, 0, v97, vcc
	v_add_co_u32_e32 v104, vcc, s9, v96
	s_waitcnt vmcnt(3)
	v_pk_mul_f32 v[106:107], v[26:27], v[26:27]
	v_addc_co_u32_e32 v105, vcc, 0, v97, vcc
	global_load_dwordx4 v[30:33], v[70:71], off
	global_load_dwordx4 v[66:69], v[4:5], off offset:-4096
	global_load_dwordx4 v[50:53], v[2:3], off offset:3072
	global_load_dwordx4 v[34:37], v[4:5], off offset:2048
	global_load_dwordx4 v[10:13], v[104:105], off offset:1024
	global_load_dwordx4 v[62:65], v[2:3], off offset:1024
	global_load_dwordx4 v[58:61], v[2:3], off offset:2048
	global_load_dwordx4 v[46:49], v[4:5], off
	global_load_dwordx4 v[38:41], v[4:5], off offset:1024
	global_load_dwordx4 v[18:21], v[4:5], off offset:3072
	global_load_dwordx4 v[14:17], v[104:105], off
	global_load_dwordx4 v[6:9], v[104:105], off offset:2048
	s_nop 0
	global_load_dwordx4 v[2:5], v[104:105], off offset:3072
	v_pk_mul_f32 v[104:105], v[28:29], v[28:29]
	s_waitcnt vmcnt(15)
	v_pk_mul_f32 v[108:109], v[24:25], v[24:25]
	v_pk_mul_f32 v[110:111], v[22:23], v[22:23]
	v_pk_mov_b32 v[114:115], v[106:107], v[104:105] op_sel:[1,0]
	v_mov_b32_e32 v107, v105
	v_pk_mov_b32 v[104:105], v[110:111], v[108:109] op_sel:[1,0]
	v_mov_b32_e32 v111, v109
	s_waitcnt vmcnt(14)
	v_mul_f32_e32 v100, v55, v55
	v_mul_f32_e32 v112, v57, v57
	v_pk_add_f32 v[106:107], v[114:115], v[106:107]
	v_pk_add_f32 v[104:105], v[104:105], v[110:111]
	s_waitcnt vmcnt(13)
	v_mul_f32_e32 v103, v44, v44
	v_mul_f32_e32 v133, v45, v45
	v_mul_f32_e32 v145, v42, v42
	v_mul_f32_e32 v146, v43, v43
	v_pk_fma_f32 v[130:131], v[54:55], v[54:55], v[100:101] op_sel_hi:[1,1,0]
	v_pk_fma_f32 v[112:113], v[56:57], v[56:57], v[112:113] op_sel_hi:[1,1,0]
	v_pk_add_f32 v[106:107], v[106:107], v[106:107] op_sel:[0,1] op_sel_hi:[1,0]
	v_pk_add_f32 v[104:105], v[104:105], v[104:105] op_sel:[0,1] op_sel_hi:[1,0]
	v_mov_b32_e32 v131, v103
	v_mov_b32_e32 v113, v133
	v_mov_b32_e32 v107, v145
	v_mov_b32_e32 v105, v146
	v_pk_add_f32 v[112:113], v[130:131], v[112:113]
	v_pk_add_f32 v[104:105], v[106:107], v[104:105]
	v_lshl_add_u64 v[96:97], v[96:97], 0, s[4:5]
	v_pk_add_f32 v[104:105], v[104:105], v[112:113]
	s_waitcnt vmcnt(11)
	v_pk_mul_f32 v[108:109], v[68:69], v[68:69]
	v_pk_mul_f32 v[116:117], v[66:67], v[66:67]
	s_waitcnt vmcnt(10)
	v_pk_mul_f32 v[118:119], v[52:53], v[52:53]
	v_pk_mov_b32 v[110:111], v[116:117], v[108:109] op_sel:[1,0]
	v_mov_b32_e32 v117, v109
	v_pk_mul_f32 v[120:121], v[50:51], v[50:51]
	s_waitcnt vmcnt(9)
	v_pk_mul_f32 v[122:123], v[36:37], v[36:37]
	v_pk_mul_f32 v[124:125], v[34:35], v[34:35]
	s_waitcnt vmcnt(8)
	v_pk_mul_f32 v[126:127], v[12:13], v[12:13]
	v_pk_mul_f32 v[128:129], v[10:11], v[10:11]
	s_waitcnt vmcnt(7)
; __device__ __forceinline__ float rdlane(float v, int l) { return __builtin_bit_cast(float, __builtin_amdgcn_readlane(__builtin_bit_cast(int, v), l)); }
; __device__ __forceinline__ float wave_sum(float v) { v = dpp_add16(v); return (rdlane(v, 0) + rdlane(v, 16)) + (rdlane(v, 32) + rdlane(v, 48)); }
; __device__ __forceinline__ void rms_row_to_both(const float* xrow, const float* g, bf16* orow, unsigned char* orow8, int lane) {
;     const f32x4* xr = (const f32x4*)xrow + lane; const f32x4* gr = (const f32x4*)g + lane;
;     f32x4 v[16]; float s = 0.f;
; #pragma unroll
;     for (int j = 0; j < 16; ++j) { v[j] = xr[64 * j]; s += (v[j].x * v[j].x + v[j].y * v[j].y) + (v[j].z * v[j].z + v[j].w * v[j].w); }
;     const float rs = 1.0f / sqrtf(wave_sum(s) * (1.f / D_) + 1e-6f);
	v_mul_f32_e32 v100, v63, v63
	v_mul_f32_e32 v132, v65, v65
	v_pk_add_f32 v[110:111], v[110:111], v[116:117]
	s_waitcnt vmcnt(6)
	v_mul_f32_e32 v147, v60, v60
	v_mul_f32_e32 v148, v61, v61
	v_mul_f32_e32 v155, v59, v59
	v_mul_f32_e32 v156, v58, v58
	v_pk_mov_b32 v[108:109], v[120:121], v[118:119] op_sel:[1,0]
	v_mov_b32_e32 v121, v119
	v_pk_mov_b32 v[114:115], v[124:125], v[122:123] op_sel:[1,0]
	v_mov_b32_e32 v125, v123
	v_pk_mov_b32 v[118:119], v[128:129], v[126:127] op_sel:[1,0]
	v_mov_b32_e32 v129, v127
	v_pk_fma_f32 v[122:123], v[62:63], v[62:63], v[100:101] op_sel_hi:[1,1,0]
	v_pk_fma_f32 v[126:127], v[64:65], v[64:65], v[132:133] op_sel_hi:[1,1,0]
	v_pk_add_f32 v[110:111], v[110:111], v[110:111] op_sel:[0,1] op_sel_hi:[1,0]
	v_pk_add_f32 v[104:105], v[104:105], v[104:105] op_sel:[0,1] op_sel_hi:[1,0]
	v_mov_b32_e32 v123, v147
	v_mov_b32_e32 v127, v148
	v_mov_b32_e32 v111, v155
	v_mov_b32_e32 v105, v156
	v_pk_add_f32 v[116:117], v[118:119], v[128:129]
	v_pk_add_f32 v[118:119], v[122:123], v[126:127]
	v_pk_add_f32 v[104:105], v[104:105], v[110:111]
	s_waitcnt vmcnt(5)
	v_mul_f32_e32 v134, v47, v47
	v_mul_f32_e32 v136, v49, v49
	v_pk_add_f32 v[108:109], v[108:109], v[120:121]
	v_pk_add_f32 v[104:105], v[104:105], v[118:119]
	s_waitcnt vmcnt(4)
	v_mul_f32_e32 v149, v40, v40
	v_mul_f32_e32 v150, v41, v41
	v_mul_f32_e32 v157, v39, v39
	v_mul_f32_e32 v158, v38, v38
	v_pk_fma_f32 v[132:133], v[46:47], v[46:47], v[134:135] op_sel_hi:[1,1,0]
	v_pk_fma_f32 v[134:135], v[48:49], v[48:49], v[136:137] op_sel_hi:[1,1,0]
	v_pk_add_f32 v[108:109], v[108:109], v[108:109] op_sel:[0,1] op_sel_hi:[1,0]
	v_pk_add_f32 v[104:105], v[104:105], v[104:105] op_sel:[0,1] op_sel_hi:[1,0]
	v_mov_b32_e32 v133, v149
	v_mov_b32_e32 v135, v150
	v_mov_b32_e32 v109, v157
	v_mov_b32_e32 v105, v158
	v_pk_add_f32 v[120:121], v[132:133], v[134:135]
	v_pk_add_f32 v[104:105], v[104:105], v[108:109]
	s_waitcnt vmcnt(3)
	v_mul_f32_e32 v138, v19, v19
	v_mul_f32_e32 v140, v21, v21
	v_pk_add_f32 v[114:115], v[114:115], v[124:125]
	v_pk_add_f32 v[104:105], v[104:105], v[120:121]
	s_waitcnt vmcnt(2)
	v_mul_f32_e32 v151, v16, v16
	v_mul_f32_e32 v152, v17, v17
	v_mul_f32_e32 v159, v15, v15
	v_mul_f32_e32 v160, v14, v14
	v_pk_fma_f32 v[136:137], v[18:19], v[18:19], v[138:139] op_sel_hi:[1,1,0]
	v_pk_fma_f32 v[138:139], v[20:21], v[20:21], v[140:141] op_sel_hi:[1,1,0]
	v_pk_add_f32 v[114:115], v[114:115], v[114:115] op_sel:[0,1] op_sel_hi:[1,0]
	v_pk_add_f32 v[104:105], v[104:105], v[104:105] op_sel:[0,1] op_sel_hi:[1,0]
	v_mov_b32_e32 v137, v151
	v_mov_b32_e32 v139, v152
	v_mov_b32_e32 v115, v159
	v_mov_b32_e32 v105, v160
	v_pk_add_f32 v[122:123], v[136:137], v[138:139]
	v_pk_add_f32 v[104:105], v[104:105], v[114:115]
	s_waitcnt vmcnt(1)
	v_mul_f32_e32 v142, v7, v7
	v_mul_f32_e32 v144, v9, v9
	v_pk_add_f32 v[104:105], v[104:105], v[122:123]
	s_waitcnt vmcnt(0)
	v_mul_f32_e32 v153, v4, v4
	v_mul_f32_e32 v154, v5, v5
	v_mul_f32_e32 v161, v3, v3
	v_mul_f32_e32 v162, v2, v2
	v_pk_fma_f32 v[140:141], v[6:7], v[6:7], v[142:143] op_sel_hi:[1,1,0]
	v_pk_fma_f32 v[142:143], v[8:9], v[8:9], v[144:145] op_sel_hi:[1,1,0]
	v_pk_add_f32 v[116:117], v[116:117], v[116:117] op_sel:[0,1] op_sel_hi:[1,0]
	v_pk_add_f32 v[104:105], v[104:105], v[104:105] op_sel:[0,1] op_sel_hi:[1,0]
	v_mov_b32_e32 v141, v153
	v_mov_b32_e32 v143, v154
	v_mov_b32_e32 v117, v161
	v_mov_b32_e32 v105, v162
	v_pk_add_f32 v[124:125], v[140:141], v[142:143]
	v_pk_add_f32 v[104:105], v[104:105], v[116:117]
	s_nop 0
	v_pk_add_f32 v[104:105], v[104:105], v[124:125]
	s_nop 0
	v_add_f32_e32 v100, v104, v105
	s_nop 1
	v_add_f32_dpp v100, v100, v100 quad_perm:[1,0,3,2] row_mask:0xf bank_mask:0xf bound_ctrl:1
	s_nop 1
	v_add_f32_dpp v100, v100, v100 quad_perm:[2,3,0,1] row_mask:0xf bank_mask:0xf bound_ctrl:1
	s_nop 1
	v_add_f32_dpp v100, v100, v100 row_half_mirror row_mask:0xf bank_mask:0xf bound_ctrl:1
	s_nop 1
	v_add_f32_dpp v100, v100, v100 row_mirror row_mask:0xf bank_mask:0xf bound_ctrl:1
	s_nop 0
	v_readlane_b32 s30, v100, 16
	v_readlane_b32 s31, v100, 48
	v_readlane_b32 s0, v100, 0
	v_readlane_b32 s1, v100, 32
	v_mov_b32_e32 v104, s30
	v_mov_b32_e32 v105, s31
	v_pk_add_f32 v[104:105], s[0:1], v[104:105]
	s_nop 0
	v_add_f32_e32 v100, v104, v105
	v_fmamk_f32 v100, v100, 0x39800000, v1
	v_mul_f32_e32 v103, 0x4f800000, v100
	v_cmp_gt_f32_e32 vcc, s10, v100
	s_nop 1
	v_cndmask_b32_e32 v100, v100, v103, vcc
	v_sqrt_f32_e32 v103, v100
	s_nop 0
	v_add_u32_e32 v104, -1, v103
	v_add_u32_e32 v105, 1, v103
	v_fma_f32 v106, -v104, v103, v100
	v_fma_f32 v107, -v105, v103, v100
	v_cmp_ge_f32_e64 s[0:1], 0, v106
	s_nop 1
	v_cndmask_b32_e64 v103, v103, v104, s[0:1]
	v_cmp_lt_f32_e64 s[0:1], 0, v107
	s_nop 1
	v_cndmask_b32_e64 v103, v103, v105, s[0:1]
	v_mul_f32_e32 v104, 0x37800000, v103
	v_cndmask_b32_e32 v103, v103, v104, vcc
	v_cmp_class_f32_e32 vcc, v100, v101
	s_nop 1
	v_cndmask_b32_e32 v100, v103, v100, vcc
	v_div_scale_f32 v103, s[0:1], v100, v100, 1.0
	v_rcp_f32_e32 v105, v103
	v_div_scale_f32 v104, vcc, 1.0, v100, 1.0
	v_fma_f32 v106, -v103, v105, 1.0
	v_fmac_f32_e32 v105, v106, v105
	v_mul_f32_e32 v106, v104, v105
	v_fma_f32 v107, -v103, v106, v104
	v_fmac_f32_e32 v106, v107, v105
	v_fma_f32 v103, -v103, v106, v104
	v_div_fmas_f32 v103, v103, v105, v106
	v_div_fixup_f32 v100, v103, v100, 1.0
	v_pk_mul_f32 v[26:27], v[26:27], v[100:101] op_sel_hi:[1,0]
	v_pk_mul_f32 v[28:29], v[28:29], v[100:101] op_sel_hi:[1,0]
	v_pk_mul_f32 v[26:27], v[30:31], v[26:27]
	v_pk_mul_f32 v[28:29], v[32:33], v[28:29]
	v_mul_f32_e32 v27, 0x41c80000, v27
	v_mul_f32_e32 v26, 0x41c80000, v26
	v_mul_f32_e32 v28, 0x41c80000, v28
	v_mul_f32_e32 v29, 0x41c80000, v29
; __device__ __forceinline__ unsigned pk4_i8(float a, float b, float c, float d) {
;     const int q0 = (int)rintf(fminf(fmaxf(a, -127.f), 127.f)), q1 = (int)rintf(fminf(fmaxf(b, -127.f), 127.f)), q2 = (int)rintf(fminf(fmaxf(c, -127.f), 127.f)), q3 = (int)rintf(fminf(fmaxf(d, -127.f), 127.f));
;     return (unsigned)(q0 & 0xff) | ((unsigned)(q1 & 0xff) << 8) | ((unsigned)(q2 & 0xff) << 16) | ((unsigned)q3 << 24);
; __device__ __forceinline__ void rms_row_to_both(const float* xrow, const float* g, bf16* orow, unsigned char* orow8, int lane) {
;     ...
;     unsigned* o4 = (unsigned*)orow8 + lane; (void)orow;
; #pragma unroll
;     for (int j = 0; j < 16; ++j) { const f32x4 y = v[j] * rs * gr[64 * j]; o4[64 * j] = pk4_i8(y.x * I8_SA, y.y * I8_SA, y.z * I8_SA, y.w * I8_SA); }
	v_med3_f32 v27, v27, s11, v102
	v_med3_f32 v26, v26, s11, v102
	v_med3_f32 v29, v29, s11, v102
	v_med3_f32 v28, v28, s11, v102
	v_rndne_f32_e32 v27, v27
	v_rndne_f32_e32 v26, v26
	v_rndne_f32_e32 v29, v29
	v_rndne_f32_e32 v28, v28
	v_cvt_i32_f32_e32 v27, v27
	v_cvt_i32_f32_e32 v26, v26
	v_cvt_i32_f32_e32 v29, v29
	v_cvt_i32_f32_sdwa v28, v28 dst_sel:WORD_1 dst_unused:UNUSED_PAD src0_sel:DWORD
	v_lshlrev_b32_e32 v27, 8, v27
	v_and_b32_e32 v27, 0xff00, v27
	v_perm_b32 v26, v29, v26, s28
	v_and_b32_e32 v28, 0xff0000, v28
	v_or3_b32 v26, v26, v27, v28
	global_store_dword v[98:99], v26, off
	v_mov_b64_e32 v[26:27], v[164:165]
	v_mov_b64_e32 v[28:29], v[166:167]
	v_pk_mul_f32 v[22:23], v[22:23], v[100:101] op_sel_hi:[1,0]
	v_pk_mul_f32 v[24:25], v[24:25], v[100:101] op_sel_hi:[1,0]
	v_pk_mul_f32 v[54:55], v[54:55], v[100:101] op_sel_hi:[1,0]
	v_pk_mul_f32 v[56:57], v[56:57], v[100:101] op_sel_hi:[1,0]
	v_pk_mul_f32 v[42:43], v[42:43], v[100:101] op_sel_hi:[1,0]
	v_pk_mul_f32 v[44:45], v[44:45], v[100:101] op_sel_hi:[1,0]
	v_pk_mul_f32 v[66:67], v[66:67], v[100:101] op_sel_hi:[1,0]
	v_pk_mul_f32 v[68:69], v[68:69], v[100:101] op_sel_hi:[1,0]
	v_pk_mul_f32 v[62:63], v[62:63], v[100:101] op_sel_hi:[1,0]
	v_pk_mul_f32 v[64:65], v[64:65], v[100:101] op_sel_hi:[1,0]
	v_pk_mul_f32 v[58:59], v[58:59], v[100:101] op_sel_hi:[1,0]
	v_pk_mul_f32 v[60:61], v[60:61], v[100:101] op_sel_hi:[1,0]
	v_pk_mul_f32 v[50:51], v[50:51], v[100:101] op_sel_hi:[1,0]
	v_pk_mul_f32 v[52:53], v[52:53], v[100:101] op_sel_hi:[1,0]
	v_pk_mul_f32 v[46:47], v[46:47], v[100:101] op_sel_hi:[1,0]
	v_pk_mul_f32 v[48:49], v[48:49], v[100:101] op_sel_hi:[1,0]
	v_pk_mul_f32 v[38:39], v[38:39], v[100:101] op_sel_hi:[1,0]
	v_pk_mul_f32 v[40:41], v[40:41], v[100:101] op_sel_hi:[1,0]
	v_pk_mul_f32 v[34:35], v[34:35], v[100:101] op_sel_hi:[1,0]
	v_pk_mul_f32 v[36:37], v[36:37], v[100:101] op_sel_hi:[1,0]
	v_pk_mul_f32 v[18:19], v[18:19], v[100:101] op_sel_hi:[1,0]
	v_pk_mul_f32 v[20:21], v[20:21], v[100:101] op_sel_hi:[1,0]
	v_pk_mul_f32 v[14:15], v[14:15], v[100:101] op_sel_hi:[1,0]
	v_pk_mul_f32 v[16:17], v[16:17], v[100:101] op_sel_hi:[1,0]
	v_pk_mul_f32 v[10:11], v[10:11], v[100:101] op_sel_hi:[1,0]
	v_pk_mul_f32 v[12:13], v[12:13], v[100:101] op_sel_hi:[1,0]
	v_pk_mul_f32 v[6:7], v[6:7], v[100:101] op_sel_hi:[1,0]
	v_pk_mul_f32 v[8:9], v[8:9], v[100:101] op_sel_hi:[1,0]
	v_pk_mul_f32 v[2:3], v[2:3], v[100:101] op_sel_hi:[1,0]
	v_pk_mul_f32 v[4:5], v[4:5], v[100:101] op_sel_hi:[1,0]
	v_pk_mul_f32 v[22:23], v[26:27], v[22:23]
	v_pk_mul_f32 v[24:25], v[28:29], v[24:25]
	v_mul_f32_e32 v23, 0x41c80000, v23
	v_mul_f32_e32 v22, 0x41c80000, v22
	v_mul_f32_e32 v24, 0x41c80000, v24
	v_mul_f32_e32 v25, 0x41c80000, v25
	v_med3_f32 v23, v23, s11, v102
	v_med3_f32 v22, v22, s11, v102
	v_med3_f32 v25, v25, s11, v102
	v_med3_f32 v24, v24, s11, v102
	v_rndne_f32_e32 v23, v23
	v_rndne_f32_e32 v22, v22
	v_rndne_f32_e32 v25, v25
	v_rndne_f32_e32 v24, v24
	v_cvt_i32_f32_e32 v23, v23
	v_cvt_i32_f32_e32 v22, v22
	v_cvt_i32_f32_e32 v25, v25
	v_cvt_i32_f32_sdwa v24, v24 dst_sel:WORD_1 dst_unused:UNUSED_PAD src0_sel:DWORD
	v_lshlrev_b32_e32 v23, 8, v23
	v_and_b32_e32 v23, 0xff00, v23
	v_perm_b32 v22, v25, v22, s28
	v_and_b32_e32 v24, 0xff0000, v24
	v_or3_b32 v22, v22, v23, v24
	global_store_dword v[98:99], v22, off offset:256
	v_mov_b64_e32 v[22:23], v[168:169]
	v_mov_b64_e32 v[24:25], v[170:171]
	v_pk_mul_f32 v[22:23], v[22:23], v[54:55]
	v_pk_mul_f32 v[24:25], v[24:25], v[56:57]
	v_mul_f32_e32 v23, 0x41c80000, v23
	v_mul_f32_e32 v22, 0x41c80000, v22
	v_mul_f32_e32 v24, 0x41c80000, v24
	v_mul_f32_e32 v25, 0x41c80000, v25
	v_med3_f32 v23, v23, s11, v102
	v_med3_f32 v22, v22, s11, v102
	v_med3_f32 v24, v24, s11, v102
	v_med3_f32 v25, v25, s11, v102
	v_rndne_f32_e32 v23, v23
	v_rndne_f32_e32 v22, v22
	v_rndne_f32_e32 v24, v24
	v_rndne_f32_e32 v25, v25
	v_cvt_i32_f32_e32 v23, v23
	v_cvt_i32_f32_e32 v22, v22
	v_cvt_i32_f32_sdwa v24, v24 dst_sel:WORD_1 dst_unused:UNUSED_PAD src0_sel:DWORD
	v_cvt_i32_f32_e32 v25, v25
	v_lshlrev_b32_e32 v23, 8, v23
	v_and_b32_e32 v23, 0xff00, v23
	v_and_b32_e32 v24, 0xff0000, v24
	v_perm_b32 v22, v25, v22, s28
	v_or3_b32 v22, v22, v23, v24
	global_store_dword v[98:99], v22, off offset:512
	v_mov_b64_e32 v[22:23], v[172:173]
	v_mov_b64_e32 v[24:25], v[174:175]
	v_pk_mul_f32 v[22:23], v[22:23], v[42:43]
	v_pk_mul_f32 v[24:25], v[24:25], v[44:45]
	v_mul_f32_e32 v23, 0x41c80000, v23
	v_mul_f32_e32 v22, 0x41c80000, v22
	v_mul_f32_e32 v24, 0x41c80000, v24
	v_mul_f32_e32 v25, 0x41c80000, v25
	v_med3_f32 v23, v23, s11, v102
	v_med3_f32 v22, v22, s11, v102
	v_med3_f32 v24, v24, s11, v102
	v_med3_f32 v25, v25, s11, v102
	v_rndne_f32_e32 v23, v23
	v_rndne_f32_e32 v22, v22
	v_rndne_f32_e32 v24, v24
	v_rndne_f32_e32 v25, v25
	v_cvt_i32_f32_e32 v23, v23
	v_cvt_i32_f32_e32 v22, v22
	v_cvt_i32_f32_sdwa v24, v24 dst_sel:WORD_1 dst_unused:UNUSED_PAD src0_sel:DWORD
	v_cvt_i32_f32_e32 v25, v25
	v_lshlrev_b32_e32 v23, 8, v23
	v_and_b32_e32 v23, 0xff00, v23
	v_and_b32_e32 v24, 0xff0000, v24
	v_perm_b32 v22, v25, v22, s28
	v_or3_b32 v22, v22, v23, v24
	global_store_dword v[98:99], v22, off offset:768
	v_mov_b64_e32 v[22:23], v[176:177]
	v_mov_b64_e32 v[24:25], v[178:179]
	v_pk_mul_f32 v[22:23], v[66:67], v[22:23]
	v_pk_mul_f32 v[24:25], v[68:69], v[24:25]
	v_mul_f32_e32 v23, 0x41c80000, v23
	v_mul_f32_e32 v22, 0x41c80000, v22
	v_mul_f32_e32 v24, 0x41c80000, v24
	v_mul_f32_e32 v25, 0x41c80000, v25
	v_med3_f32 v23, v23, s11, v102
	v_med3_f32 v22, v22, s11, v102
	v_med3_f32 v24, v24, s11, v102
	v_med3_f32 v25, v25, s11, v102
	v_rndne_f32_e32 v23, v23
	v_rndne_f32_e32 v22, v22
	v_rndne_f32_e32 v24, v24
; __device__ __forceinline__ unsigned pk4_i8(float a, float b, float c, float d) {
;     const int q0 = (int)rintf(fminf(fmaxf(a, -127.f), 127.f)), q1 = (int)rintf(fminf(fmaxf(b, -127.f), 127.f)), q2 = (int)rintf(fminf(fmaxf(c, -127.f), 127.f)), q3 = (int)rintf(fminf(fmaxf(d, -127.f), 127.f));
;     return (unsigned)(q0 & 0xff) | ((unsigned)(q1 & 0xff) << 8) | ((unsigned)(q2 & 0xff) << 16) | ((unsigned)q3 << 24);
; __device__ __forceinline__ void rms_row_to_both(const float* xrow, const float* g, bf16* orow, unsigned char* orow8, int lane) {
;     ...
;     unsigned* o4 = (unsigned*)orow8 + lane; (void)orow;
; #pragma unroll
;     for (int j = 0; j < 16; ++j) { const f32x4 y = v[j] * rs * gr[64 * j]; o4[64 * j] = pk4_i8(y.x * I8_SA, y.y * I8_SA, y.z * I8_SA, y.w * I8_SA); }
	v_rndne_f32_e32 v25, v25
	v_cvt_i32_f32_e32 v23, v23
	v_cvt_i32_f32_e32 v22, v22
	v_cvt_i32_f32_sdwa v24, v24 dst_sel:WORD_1 dst_unused:UNUSED_PAD src0_sel:DWORD
	v_cvt_i32_f32_e32 v25, v25
	v_lshlrev_b32_e32 v23, 8, v23
	v_and_b32_e32 v23, 0xff00, v23
	v_and_b32_e32 v24, 0xff0000, v24
	v_perm_b32 v22, v25, v22, s28
	v_or3_b32 v22, v22, v23, v24
	global_store_dword v[98:99], v22, off offset:1024
	v_mov_b64_e32 v[22:23], v[180:181]
	v_mov_b64_e32 v[24:25], v[182:183]
	v_pk_mul_f32 v[22:23], v[62:63], v[22:23]
	v_pk_mul_f32 v[24:25], v[64:65], v[24:25]
	v_mul_f32_e32 v23, 0x41c80000, v23
	v_mul_f32_e32 v22, 0x41c80000, v22
	v_mul_f32_e32 v24, 0x41c80000, v24
	v_mul_f32_e32 v25, 0x41c80000, v25
	v_med3_f32 v23, v23, s11, v102
	v_med3_f32 v22, v22, s11, v102
	v_med3_f32 v24, v24, s11, v102
	v_med3_f32 v25, v25, s11, v102
	v_rndne_f32_e32 v23, v23
	v_rndne_f32_e32 v22, v22
	v_rndne_f32_e32 v24, v24
	v_rndne_f32_e32 v25, v25
	v_cvt_i32_f32_e32 v23, v23
	v_cvt_i32_f32_e32 v22, v22
	v_cvt_i32_f32_sdwa v24, v24 dst_sel:WORD_1 dst_unused:UNUSED_PAD src0_sel:DWORD
	v_cvt_i32_f32_e32 v25, v25
	v_lshlrev_b32_e32 v23, 8, v23
	v_and_b32_e32 v23, 0xff00, v23
	v_and_b32_e32 v24, 0xff0000, v24
	v_perm_b32 v22, v25, v22, s28
	v_or3_b32 v22, v22, v23, v24
	global_store_dword v[98:99], v22, off offset:1280
	v_mov_b64_e32 v[22:23], v[184:185]
	v_mov_b64_e32 v[24:25], v[186:187]
	v_pk_mul_f32 v[22:23], v[58:59], v[22:23]
	v_pk_mul_f32 v[24:25], v[60:61], v[24:25]
	v_mul_f32_e32 v23, 0x41c80000, v23
	v_mul_f32_e32 v22, 0x41c80000, v22
	v_mul_f32_e32 v24, 0x41c80000, v24
	v_mul_f32_e32 v25, 0x41c80000, v25
	v_med3_f32 v23, v23, s11, v102
	v_med3_f32 v22, v22, s11, v102
	v_med3_f32 v24, v24, s11, v102
	v_med3_f32 v25, v25, s11, v102
	v_rndne_f32_e32 v23, v23
	v_rndne_f32_e32 v22, v22
	v_rndne_f32_e32 v24, v24
	v_rndne_f32_e32 v25, v25
	v_cvt_i32_f32_e32 v23, v23
	v_cvt_i32_f32_e32 v22, v22
	v_cvt_i32_f32_sdwa v24, v24 dst_sel:WORD_1 dst_unused:UNUSED_PAD src0_sel:DWORD
	v_cvt_i32_f32_e32 v25, v25
	v_lshlrev_b32_e32 v23, 8, v23
	v_and_b32_e32 v23, 0xff00, v23
	v_and_b32_e32 v24, 0xff0000, v24
	v_perm_b32 v22, v25, v22, s28
	v_or3_b32 v22, v22, v23, v24
	global_store_dword v[98:99], v22, off offset:1536
	v_mov_b64_e32 v[22:23], v[188:189]
	v_mov_b64_e32 v[24:25], v[190:191]
	v_pk_mul_f32 v[22:23], v[50:51], v[22:23]
	v_pk_mul_f32 v[24:25], v[52:53], v[24:25]
	v_mul_f32_e32 v23, 0x41c80000, v23
	v_mul_f32_e32 v22, 0x41c80000, v22
	v_mul_f32_e32 v24, 0x41c80000, v24
	v_mul_f32_e32 v25, 0x41c80000, v25
	v_med3_f32 v23, v23, s11, v102
	v_med3_f32 v22, v22, s11, v102
	v_med3_f32 v24, v24, s11, v102
	v_med3_f32 v25, v25, s11, v102
	v_rndne_f32_e32 v23, v23
	v_rndne_f32_e32 v22, v22
	v_rndne_f32_e32 v24, v24
	v_rndne_f32_e32 v25, v25
	v_cvt_i32_f32_e32 v23, v23
	v_cvt_i32_f32_e32 v22, v22
	v_cvt_i32_f32_sdwa v24, v24 dst_sel:WORD_1 dst_unused:UNUSED_PAD src0_sel:DWORD
	v_cvt_i32_f32_e32 v25, v25
	v_lshlrev_b32_e32 v23, 8, v23
	v_and_b32_e32 v23, 0xff00, v23
	v_and_b32_e32 v24, 0xff0000, v24
	v_perm_b32 v22, v25, v22, s28
	v_or3_b32 v22, v22, v23, v24
	global_store_dword v[98:99], v22, off offset:1792
	v_mov_b64_e32 v[22:23], v[192:193]
	v_mov_b64_e32 v[24:25], v[194:195]
	v_pk_mul_f32 v[22:23], v[46:47], v[22:23]
	v_pk_mul_f32 v[24:25], v[48:49], v[24:25]
	v_mul_f32_e32 v23, 0x41c80000, v23
	v_mul_f32_e32 v22, 0x41c80000, v22
	v_mul_f32_e32 v24, 0x41c80000, v24
	v_mul_f32_e32 v25, 0x41c80000, v25
	v_med3_f32 v23, v23, s11, v102
	v_med3_f32 v22, v22, s11, v102
	v_med3_f32 v24, v24, s11, v102
	v_med3_f32 v25, v25, s11, v102
	v_rndne_f32_e32 v23, v23
	v_rndne_f32_e32 v22, v22
	v_rndne_f32_e32 v24, v24
	v_rndne_f32_e32 v25, v25
	v_cvt_i32_f32_e32 v23, v23
	v_cvt_i32_f32_e32 v22, v22
	v_cvt_i32_f32_sdwa v24, v24 dst_sel:WORD_1 dst_unused:UNUSED_PAD src0_sel:DWORD
	v_cvt_i32_f32_e32 v25, v25
	v_lshlrev_b32_e32 v23, 8, v23
	v_and_b32_e32 v23, 0xff00, v23
	v_and_b32_e32 v24, 0xff0000, v24
	v_perm_b32 v22, v25, v22, s28
	v_or3_b32 v22, v22, v23, v24
	global_store_dword v[98:99], v22, off offset:2048
	v_mov_b64_e32 v[22:23], v[196:197]
	v_mov_b64_e32 v[24:25], v[198:199]
	v_pk_mul_f32 v[22:23], v[38:39], v[22:23]
	v_pk_mul_f32 v[24:25], v[40:41], v[24:25]
	v_mul_f32_e32 v23, 0x41c80000, v23
	v_mul_f32_e32 v22, 0x41c80000, v22
	v_mul_f32_e32 v24, 0x41c80000, v24
	v_mul_f32_e32 v25, 0x41c80000, v25
	v_med3_f32 v23, v23, s11, v102
	v_med3_f32 v22, v22, s11, v102
	v_med3_f32 v24, v24, s11, v102
	v_med3_f32 v25, v25, s11, v102
	v_rndne_f32_e32 v23, v23
	v_rndne_f32_e32 v22, v22
	v_rndne_f32_e32 v24, v24
	v_rndne_f32_e32 v25, v25
	v_cvt_i32_f32_e32 v23, v23
	v_cvt_i32_f32_e32 v22, v22
	v_cvt_i32_f32_sdwa v24, v24 dst_sel:WORD_1 dst_unused:UNUSED_PAD src0_sel:DWORD
	v_cvt_i32_f32_e32 v25, v25
	v_lshlrev_b32_e32 v23, 8, v23
	v_and_b32_e32 v23, 0xff00, v23
	v_and_b32_e32 v24, 0xff0000, v24
	v_perm_b32 v22, v25, v22, s28
	v_or3_b32 v22, v22, v23, v24
	global_store_dword v[98:99], v22, off offset:2304
	v_mov_b64_e32 v[22:23], v[200:201]
	v_mov_b64_e32 v[24:25], v[202:203]
	v_pk_mul_f32 v[22:23], v[34:35], v[22:23]
	v_pk_mul_f32 v[24:25], v[36:37], v[24:25]
	v_mul_f32_e32 v23, 0x41c80000, v23
	v_mul_f32_e32 v22, 0x41c80000, v22
; __device__ __forceinline__ unsigned pk4_i8(float a, float b, float c, float d) {
;     const int q0 = (int)rintf(fminf(fmaxf(a, -127.f), 127.f)), q1 = (int)rintf(fminf(fmaxf(b, -127.f), 127.f)), q2 = (int)rintf(fminf(fmaxf(c, -127.f), 127.f)), q3 = (int)rintf(fminf(fmaxf(d, -127.f), 127.f));
;     return (unsigned)(q0 & 0xff) | ((unsigned)(q1 & 0xff) << 8) | ((unsigned)(q2 & 0xff) << 16) | ((unsigned)q3 << 24);
; __device__ __forceinline__ void rms_row_to_both(const float* xrow, const float* g, bf16* orow, unsigned char* orow8, int lane) {
;     ...
;     unsigned* o4 = (unsigned*)orow8 + lane; (void)orow;
; #pragma unroll
;     for (int j = 0; j < 16; ++j) { const f32x4 y = v[j] * rs * gr[64 * j]; o4[64 * j] = pk4_i8(y.x * I8_SA, y.y * I8_SA, y.z * I8_SA, y.w * I8_SA); }
	v_mul_f32_e32 v24, 0x41c80000, v24
	v_mul_f32_e32 v25, 0x41c80000, v25
	v_med3_f32 v23, v23, s11, v102
	v_med3_f32 v22, v22, s11, v102
	v_med3_f32 v24, v24, s11, v102
	v_med3_f32 v25, v25, s11, v102
	v_rndne_f32_e32 v23, v23
	v_rndne_f32_e32 v22, v22
	v_rndne_f32_e32 v24, v24
	v_rndne_f32_e32 v25, v25
	v_cvt_i32_f32_e32 v23, v23
	v_cvt_i32_f32_e32 v22, v22
	v_cvt_i32_f32_sdwa v24, v24 dst_sel:WORD_1 dst_unused:UNUSED_PAD src0_sel:DWORD
	v_cvt_i32_f32_e32 v25, v25
	v_lshlrev_b32_e32 v23, 8, v23
	v_and_b32_e32 v23, 0xff00, v23
	v_and_b32_e32 v24, 0xff0000, v24
	v_perm_b32 v22, v25, v22, s28
	v_or3_b32 v22, v22, v23, v24
	global_store_dword v[98:99], v22, off offset:2560
	v_mov_b64_e32 v[22:23], v[204:205]
	v_mov_b64_e32 v[24:25], v[206:207]
	v_pk_mul_f32 v[18:19], v[18:19], v[22:23]
	v_pk_mul_f32 v[20:21], v[20:21], v[24:25]
	v_mul_f32_e32 v19, 0x41c80000, v19
	v_mul_f32_e32 v18, 0x41c80000, v18
	v_mul_f32_e32 v20, 0x41c80000, v20
	v_mul_f32_e32 v21, 0x41c80000, v21
	v_med3_f32 v19, v19, s11, v102
	v_med3_f32 v18, v18, s11, v102
	v_med3_f32 v20, v20, s11, v102
	v_med3_f32 v21, v21, s11, v102
	v_rndne_f32_e32 v19, v19
	v_rndne_f32_e32 v18, v18
	v_rndne_f32_e32 v20, v20
	v_rndne_f32_e32 v21, v21
	v_cvt_i32_f32_e32 v19, v19
	v_cvt_i32_f32_e32 v18, v18
	v_cvt_i32_f32_sdwa v20, v20 dst_sel:WORD_1 dst_unused:UNUSED_PAD src0_sel:DWORD
	v_cvt_i32_f32_e32 v21, v21
	v_lshlrev_b32_e32 v19, 8, v19
	v_and_b32_e32 v19, 0xff00, v19
	v_and_b32_e32 v20, 0xff0000, v20
	v_perm_b32 v18, v21, v18, s28
	v_or3_b32 v18, v18, v19, v20
	global_store_dword v[98:99], v18, off offset:2816
	v_mov_b64_e32 v[18:19], v[208:209]
	v_mov_b64_e32 v[20:21], v[210:211]
	v_pk_mul_f32 v[14:15], v[14:15], v[18:19]
	v_pk_mul_f32 v[16:17], v[16:17], v[20:21]
	v_mul_f32_e32 v15, 0x41c80000, v15
	v_mul_f32_e32 v14, 0x41c80000, v14
	v_mul_f32_e32 v16, 0x41c80000, v16
	v_mul_f32_e32 v17, 0x41c80000, v17
	v_med3_f32 v15, v15, s11, v102
	v_med3_f32 v14, v14, s11, v102
	v_med3_f32 v16, v16, s11, v102
	v_med3_f32 v17, v17, s11, v102
	v_rndne_f32_e32 v15, v15
	v_rndne_f32_e32 v14, v14
	v_rndne_f32_e32 v16, v16
	v_rndne_f32_e32 v17, v17
	v_cvt_i32_f32_e32 v15, v15
	v_cvt_i32_f32_e32 v14, v14
	v_cvt_i32_f32_sdwa v16, v16 dst_sel:WORD_1 dst_unused:UNUSED_PAD src0_sel:DWORD
	v_cvt_i32_f32_e32 v17, v17
	v_lshlrev_b32_e32 v15, 8, v15
	v_and_b32_e32 v15, 0xff00, v15
	v_and_b32_e32 v16, 0xff0000, v16
	v_perm_b32 v14, v17, v14, s28
	v_or3_b32 v14, v14, v15, v16
	global_store_dword v[98:99], v14, off offset:3072
	v_mov_b64_e32 v[14:15], v[212:213]
	v_mov_b64_e32 v[16:17], v[214:215]
	v_pk_mul_f32 v[10:11], v[10:11], v[14:15]
	v_pk_mul_f32 v[12:13], v[12:13], v[16:17]
	v_mul_f32_e32 v11, 0x41c80000, v11
	v_mul_f32_e32 v10, 0x41c80000, v10
	v_mul_f32_e32 v12, 0x41c80000, v12
	v_mul_f32_e32 v13, 0x41c80000, v13
	v_med3_f32 v11, v11, s11, v102
	v_med3_f32 v10, v10, s11, v102
	v_med3_f32 v12, v12, s11, v102
	v_med3_f32 v13, v13, s11, v102
	v_rndne_f32_e32 v11, v11
	v_rndne_f32_e32 v10, v10
	v_rndne_f32_e32 v12, v12
	v_rndne_f32_e32 v13, v13
	v_cvt_i32_f32_e32 v11, v11
	v_cvt_i32_f32_e32 v10, v10
	v_cvt_i32_f32_sdwa v12, v12 dst_sel:WORD_1 dst_unused:UNUSED_PAD src0_sel:DWORD
	v_cvt_i32_f32_e32 v13, v13
	v_lshlrev_b32_e32 v11, 8, v11
	v_and_b32_e32 v11, 0xff00, v11
	v_and_b32_e32 v12, 0xff0000, v12
	v_perm_b32 v10, v13, v10, s28
	v_or3_b32 v10, v10, v11, v12
	global_store_dword v[98:99], v10, off offset:3328
	v_mov_b64_e32 v[10:11], v[216:217]
	v_mov_b64_e32 v[12:13], v[218:219]
	v_pk_mul_f32 v[6:7], v[6:7], v[10:11]
	v_pk_mul_f32 v[8:9], v[8:9], v[12:13]
	v_mul_f32_e32 v7, 0x41c80000, v7
	v_mul_f32_e32 v6, 0x41c80000, v6
	v_mul_f32_e32 v8, 0x41c80000, v8
	v_mul_f32_e32 v9, 0x41c80000, v9
	v_med3_f32 v7, v7, s11, v102
	v_med3_f32 v6, v6, s11, v102
	v_med3_f32 v8, v8, s11, v102
	v_med3_f32 v9, v9, s11, v102
	v_rndne_f32_e32 v7, v7
	v_rndne_f32_e32 v6, v6
	v_rndne_f32_e32 v8, v8
	v_rndne_f32_e32 v9, v9
	v_cvt_i32_f32_e32 v7, v7
	v_cvt_i32_f32_e32 v6, v6
	v_cvt_i32_f32_sdwa v8, v8 dst_sel:WORD_1 dst_unused:UNUSED_PAD src0_sel:DWORD
	v_cvt_i32_f32_e32 v9, v9
	v_lshlrev_b32_e32 v7, 8, v7
	v_and_b32_e32 v7, 0xff00, v7
	v_and_b32_e32 v8, 0xff0000, v8
	v_perm_b32 v6, v9, v6, s28
	v_or3_b32 v6, v6, v7, v8
	global_store_dword v[98:99], v6, off offset:3584
	v_mov_b64_e32 v[6:7], v[220:221]
	v_mov_b64_e32 v[8:9], v[222:223]
	v_pk_mul_f32 v[2:3], v[2:3], v[6:7]
	v_pk_mul_f32 v[4:5], v[4:5], v[8:9]
	v_mul_f32_e32 v3, 0x41c80000, v3
	v_mul_f32_e32 v2, 0x41c80000, v2
	v_mul_f32_e32 v4, 0x41c80000, v4
	v_mul_f32_e32 v5, 0x41c80000, v5
	v_med3_f32 v3, v3, s11, v102
	v_med3_f32 v2, v2, s11, v102
	v_med3_f32 v4, v4, s11, v102
	v_med3_f32 v5, v5, s11, v102
	v_rndne_f32_e32 v3, v3
	v_rndne_f32_e32 v2, v2
	v_rndne_f32_e32 v4, v4
	v_rndne_f32_e32 v5, v5
	v_cvt_i32_f32_e32 v3, v3
	v_cvt_i32_f32_e32 v2, v2
	v_cvt_i32_f32_sdwa v4, v4 dst_sel:WORD_1 dst_unused:UNUSED_PAD src0_sel:DWORD
	v_cvt_i32_f32_e32 v5, v5
	v_lshlrev_b32_e32 v3, 8, v3
	v_and_b32_e32 v3, 0xff00, v3
	v_and_b32_e32 v4, 0xff0000, v4
	v_perm_b32 v2, v5, v2, s28
	v_or3_b32 v2, v2, v3, v4
	global_store_dword v[98:99], v2, off offset:3840
	v_lshl_add_u64 v[98:99], v[98:99], 0, s[6:7]
	s_cbranch_scc1 .LBB0_49
	s_mov_b32 s95, s33

; #define P12_ISSUE(c_, i_, h_, CW_, SC_) do { _Pragma("unroll") for (int bb = 0; bb < 8; ++bb) { const unsigned ro = (unsigned)(c_) * 16384u + (unsigned)EL[(i_) * 128 + ((h_) * 8 + bb) * 8 + g8]; \
;         CW_[bb] = *(const v4u*)(U4 + (size_t)(ro * 128u + 16u * (unsigned)k8)); SC_[bb] = USS[(size_t)(ro * 8u + (unsigned)k8)]; } } while (0)
; #define P12_COMP(i_, h_, CW_, SC_) do { _Pragma("unroll") for (int bb = 0; bb < 8; ++bb) { int a0 = 0, a1 = 0; P12_U4(CW_[bb].x, xa.x, xa.y, a0); P12_U4(CW_[bb].y, xa.z, xa.w, a1); P12_U4(CW_[bb].z, xb.x, xb.y, a0); P12_U4(CW_[bb].w, xb.z, xb.w, a1); \
;         psum[(i_)][(h_) * 8 + bb] += __uint_as_float(SC_[bb] << 16) * (float)((a0 + a1) - xo); } } while (0)
; #define P12_BAR() asm volatile("" ::: "memory")
; __device__ __forceinline__ void p12_peer(Frame& F) {
;     ...
;     { v4u cwA[8], cwB[8]; unsigned scA[8], scB[8]; v4u xa, xb; int xo;
;       P12_ISSUE(0, 0, 0, cwA, scA);
; _Pragma("nounroll")
;       for (int c = 0; c < 16; ++c) { const int cn = c + 1 < 16 ? c + 1 : 15;
;           P12_XQ(c, 0); P12_ISSUE(c, 0, 1, cwB, scB); P12_BAR(); P12_COMP(0, 0, cwA, scA); P12_ISSUE(c, 1, 0, cwA, scA); P12_BAR(); P12_COMP(0, 1, cwB, scB);
;           P12_XQ(c, 1); P12_ISSUE(c, 1, 1, cwB, scB); P12_BAR(); P12_COMP(1, 0, cwA, scA); P12_ISSUE(c, 2, 0, cwA, scA); P12_BAR(); P12_COMP(1, 1, cwB, scB);
;           P12_XQ(c, 2); P12_ISSUE(c, 2, 1, cwB, scB); P12_BAR(); P12_COMP(2, 0, cwA, scA); P12_ISSUE(c, 3, 0, cwA, scA); P12_BAR(); P12_COMP(2, 1, cwB, scB);
;           P12_XQ(c, 3); P12_ISSUE(c, 3, 1, cwB, scB); P12_BAR(); P12_COMP(3, 0, cwA, scA); P12_ISSUE(cn, 0, 0, cwA, scA); P12_BAR(); P12_COMP(3, 1, cwB, scB);
;       } }
.LBB0_3272:
	ds_read_b128 v[36:39], v166
	ds_read_b128 v[32:35], v166 offset:16
	ds_read_u16 v44, v93 offset:16512
	ds_read_u16 v45, v93 offset:16528
	ds_read_u16 v46, v93 offset:16544
	ds_read_u16 v47, v93 offset:16560
	v_mov_b32_e32 v48, 0
	s_waitcnt lgkmcnt(3)
	v_add_u32_e32 v44, s44, v44
	v_lshl_or_b32 v49, v44, 7, v165
	global_load_dwordx4 v[88:91], v49, s[0:1]
	v_lshl_or_b32 v49, v44, 4, v95
	s_waitcnt lgkmcnt(2)
	v_add_u32_e32 v44, s44, v45
	v_lshl_or_b32 v45, v44, 7, v165
	v_lshl_or_b32 v50, v44, 4, v95
	s_waitcnt lgkmcnt(1)
	v_add_u32_e32 v44, s44, v46
	global_load_dwordx4 v[84:87], v45, s[0:1]
	v_lshl_or_b32 v45, v44, 7, v165
	v_lshl_or_b32 v51, v44, 4, v95
	s_waitcnt lgkmcnt(0)
	v_add_u32_e32 v44, s44, v47
	global_load_dwordx4 v[80:83], v45, s[0:1]
	v_lshl_or_b32 v45, v44, 7, v165
	v_lshl_or_b32 v56, v44, 4, v95
	ds_read_u16 v44, v93 offset:16576
	global_load_dwordx4 v[76:79], v45, s[0:1]
	v_dot4c_i32_i8_e32 v48, 0x1010101, v36
	v_dot4c_i32_i8_e32 v48, 0x1010101, v37
	v_dot4c_i32_i8_e32 v48, 0x1010101, v38
	s_waitcnt lgkmcnt(0)
	v_add_u32_e32 v44, s44, v44
	v_lshl_or_b32 v45, v44, 7, v165
	v_lshl_or_b32 v57, v44, 4, v95
	ds_read_u16 v44, v93 offset:16592
	global_load_dwordx4 v[68:71], v45, s[0:1]
	v_dot4c_i32_i8_e32 v48, 0x1010101, v39
	v_dot4c_i32_i8_e32 v48, 0x1010101, v32
	v_dot4c_i32_i8_e32 v48, 0x1010101, v33
	s_waitcnt lgkmcnt(0)
	v_add_u32_e32 v44, s44, v44
	v_lshl_or_b32 v45, v44, 7, v165
	v_lshl_or_b32 v58, v44, 4, v95
	ds_read_u16 v44, v93 offset:16608
	global_load_dwordx4 v[60:63], v45, s[0:1]
	v_dot4c_i32_i8_e32 v48, 0x1010101, v34
	v_dot4c_i32_i8_e32 v48, 0x1010101, v35
	s_add_i32 s45, s44, 0x4000
	s_waitcnt lgkmcnt(0)
	v_add_u32_e32 v44, s44, v44
	v_lshl_or_b32 v45, v44, 7, v165
	v_lshl_or_b32 v59, v44, 4, v95
	ds_read_u16 v44, v93 offset:16624
	global_load_dwordx4 v[52:55], v45, s[0:1]
	v_lshlrev_b32_e32 v171, 3, v48
	s_waitcnt vmcnt(14)
	v_and_b32_e32 v48, 0xf0f0f0f, v28
	v_lshrrev_b32_e32 v28, 4, v28
	s_waitcnt lgkmcnt(0)
	v_add_u32_e32 v64, s44, v44
	v_lshl_or_b32 v44, v64, 7, v165
	global_load_dwordx4 v[44:47], v44, s[0:1]
	v_lshl_or_b32 v64, v64, 4, v95
	global_load_ushort v182, v50, s[18:19]
	global_load_ushort v183, v49, s[18:19]
	global_load_ushort v180, v56, s[18:19]
	global_load_ushort v181, v51, s[18:19]
	global_load_ushort v176, v58, s[18:19]
	global_load_ushort v177, v57, s[18:19]
	global_load_ushort v172, v64, s[18:19]
	global_load_ushort v173, v59, s[18:19]
	v_mov_b32_e32 v49, 0
	v_dot4c_i32_i8_e32 v49, v48, v36
	v_and_b32_e32 v28, 0xf0f0f0f, v28
	v_dot4c_i32_i8_e32 v49, v28, v37
	v_and_b32_e32 v28, 0xf0f0f0f, v29
	v_mov_b32_e32 v48, 0
	v_dot4c_i32_i8_e32 v48, v28, v38
	v_lshrrev_b32_e32 v28, 4, v29
	v_and_b32_e32 v28, 0xf0f0f0f, v28
	v_dot4c_i32_i8_e32 v48, v28, v39
	v_and_b32_e32 v28, 0xf0f0f0f, v30
	v_dot4c_i32_i8_e32 v49, v28, v32
	v_lshrrev_b32_e32 v28, 4, v30
	v_and_b32_e32 v28, 0xf0f0f0f, v28
	v_dot4c_i32_i8_e32 v49, v28, v33
	v_and_b32_e32 v28, 0xf0f0f0f, v31
	v_dot4c_i32_i8_e32 v48, v28, v34
	v_lshrrev_b32_e32 v28, 4, v31
	v_and_b32_e32 v28, 0xf0f0f0f, v28
	v_dot4c_i32_i8_e32 v48, v28, v35
	s_waitcnt vmcnt(22)
	v_and_b32_e32 v28, 0xf0f0f0f, v24
	v_mov_b32_e32 v29, 0
	v_lshrrev_b32_e32 v24, 4, v24
	v_dot4c_i32_i8_e32 v29, v28, v36
	v_and_b32_e32 v24, 0xf0f0f0f, v24
	v_dot4c_i32_i8_e32 v29, v24, v37
	v_and_b32_e32 v24, 0xf0f0f0f, v25
	v_mov_b32_e32 v28, 0
	v_dot4c_i32_i8_e32 v28, v24, v38
	v_lshrrev_b32_e32 v24, 4, v25
	v_and_b32_e32 v24, 0xf0f0f0f, v24
	v_dot4c_i32_i8_e32 v28, v24, v39
	v_and_b32_e32 v24, 0xf0f0f0f, v26
	v_dot4c_i32_i8_e32 v29, v24, v32
	v_lshrrev_b32_e32 v24, 4, v26
	v_and_b32_e32 v24, 0xf0f0f0f, v24
	v_dot4c_i32_i8_e32 v29, v24, v33
	v_and_b32_e32 v24, 0xf0f0f0f, v27
	v_dot4c_i32_i8_e32 v28, v24, v34
	v_lshrrev_b32_e32 v24, 4, v27
	v_and_b32_e32 v24, 0xf0f0f0f, v24
	v_dot4c_i32_i8_e32 v28, v24, v35
	v_add_u32_e32 v26, v49, v48
	v_sub_u32_e32 v26, v26, v171
	v_and_b32_e32 v25, 0xffff0000, v43
	v_add_u32_e32 v27, v29, v28
	v_sub_u32_e32 v28, v27, v171
	v_cvt_f32_i32_e32 v27, v26
	v_cvt_f32_i32_e32 v26, v28
	v_lshlrev_b32_e32 v24, 16, v43
	s_cmp_eq_u32 s44, 0x3c000
	v_pk_fma_f32 v[158:159], v[24:25], v[26:27], v[158:159]
	s_waitcnt vmcnt(21)
	v_and_b32_e32 v24, 0xf0f0f0f, v20
	v_mov_b32_e32 v25, 0
	v_lshrrev_b32_e32 v20, 4, v20
	v_dot4c_i32_i8_e32 v25, v24, v36
	v_and_b32_e32 v20, 0xf0f0f0f, v20
	v_dot4c_i32_i8_e32 v25, v20, v37
	v_and_b32_e32 v20, 0xf0f0f0f, v21
	v_mov_b32_e32 v24, 0
	v_dot4c_i32_i8_e32 v24, v20, v38
	v_lshrrev_b32_e32 v20, 4, v21
	v_and_b32_e32 v20, 0xf0f0f0f, v20
	v_dot4c_i32_i8_e32 v24, v20, v39
	v_and_b32_e32 v20, 0xf0f0f0f, v22
	v_dot4c_i32_i8_e32 v25, v20, v32
	v_lshrrev_b32_e32 v20, 4, v22
	v_and_b32_e32 v20, 0xf0f0f0f, v20
	v_dot4c_i32_i8_e32 v25, v20, v33
	v_and_b32_e32 v20, 0xf0f0f0f, v23
	v_dot4c_i32_i8_e32 v24, v20, v34
	v_lshrrev_b32_e32 v20, 4, v23
	v_and_b32_e32 v20, 0xf0f0f0f, v20
	v_dot4c_i32_i8_e32 v24, v20, v35
	s_waitcnt vmcnt(20)
	v_and_b32_e32 v20, 0xf0f0f0f, v16
	v_mov_b32_e32 v21, 0
	v_lshrrev_b32_e32 v16, 4, v16
	v_dot4c_i32_i8_e32 v21, v20, v36
	v_and_b32_e32 v16, 0xf0f0f0f, v16
	v_dot4c_i32_i8_e32 v21, v16, v37
	v_and_b32_e32 v16, 0xf0f0f0f, v17
	v_mov_b32_e32 v20, 0
	v_dot4c_i32_i8_e32 v20, v16, v38
	v_lshrrev_b32_e32 v16, 4, v17
	v_and_b32_e32 v16, 0xf0f0f0f, v16
	v_dot4c_i32_i8_e32 v20, v16, v39
	v_and_b32_e32 v16, 0xf0f0f0f, v18
	v_dot4c_i32_i8_e32 v21, v16, v32
	v_lshrrev_b32_e32 v16, 4, v18
	v_and_b32_e32 v16, 0xf0f0f0f, v16
	v_dot4c_i32_i8_e32 v21, v16, v33
	v_and_b32_e32 v16, 0xf0f0f0f, v19
	v_dot4c_i32_i8_e32 v20, v16, v34
	v_lshrrev_b32_e32 v16, 4, v19
	v_and_b32_e32 v16, 0xf0f0f0f, v16
	v_dot4c_i32_i8_e32 v20, v16, v35
	v_add_u32_e32 v18, v25, v24
	v_sub_u32_e32 v18, v18, v171
	v_and_b32_e32 v17, 0xffff0000, v42
	v_add_u32_e32 v19, v21, v20
	v_sub_u32_e32 v20, v19, v171
	v_cvt_f32_i32_e32 v19, v18
	v_cvt_f32_i32_e32 v18, v20
	v_lshlrev_b32_e32 v16, 16, v42
	v_pk_fma_f32 v[156:157], v[16:17], v[18:19], v[156:157]
	s_waitcnt vmcnt(19)
; #define P12_ISSUE(c_, i_, h_, CW_, SC_) do { _Pragma("unroll") for (int bb = 0; bb < 8; ++bb) { const unsigned ro = (unsigned)(c_) * 16384u + (unsigned)EL[(i_) * 128 + ((h_) * 8 + bb) * 8 + g8]; \
;         CW_[bb] = *(const v4u*)(U4 + (size_t)(ro * 128u + 16u * (unsigned)k8)); SC_[bb] = USS[(size_t)(ro * 8u + (unsigned)k8)]; } } while (0)
; #define P12_COMP(i_, h_, CW_, SC_) do { _Pragma("unroll") for (int bb = 0; bb < 8; ++bb) { int a0 = 0, a1 = 0; P12_U4(CW_[bb].x, xa.x, xa.y, a0); P12_U4(CW_[bb].y, xa.z, xa.w, a1); P12_U4(CW_[bb].z, xb.x, xb.y, a0); P12_U4(CW_[bb].w, xb.z, xb.w, a1); \
;         psum[(i_)][(h_) * 8 + bb] += __uint_as_float(SC_[bb] << 16) * (float)((a0 + a1) - xo); } } while (0)
; #define P12_BAR() asm volatile("" ::: "memory")
; __device__ __forceinline__ void p12_peer(Frame& F) {
;     ...
;     { v4u cwA[8], cwB[8]; unsigned scA[8], scB[8]; v4u xa, xb; int xo;
;       P12_ISSUE(0, 0, 0, cwA, scA);
; _Pragma("nounroll")
;       for (int c = 0; c < 16; ++c) { const int cn = c + 1 < 16 ? c + 1 : 15;
;           P12_XQ(c, 0); P12_ISSUE(c, 0, 1, cwB, scB); P12_BAR(); P12_COMP(0, 0, cwA, scA); P12_ISSUE(c, 1, 0, cwA, scA); P12_BAR(); P12_COMP(0, 1, cwB, scB);
;           P12_XQ(c, 1); P12_ISSUE(c, 1, 1, cwB, scB); P12_BAR(); P12_COMP(1, 0, cwA, scA); P12_ISSUE(c, 2, 0, cwA, scA); P12_BAR(); P12_COMP(1, 1, cwB, scB);
;           P12_XQ(c, 2); P12_ISSUE(c, 2, 1, cwB, scB); P12_BAR(); P12_COMP(2, 0, cwA, scA); P12_ISSUE(c, 3, 0, cwA, scA); P12_BAR(); P12_COMP(2, 1, cwB, scB);
;           P12_XQ(c, 3); P12_ISSUE(c, 3, 1, cwB, scB); P12_BAR(); P12_COMP(3, 0, cwA, scA); P12_ISSUE(cn, 0, 0, cwA, scA); P12_BAR(); P12_COMP(3, 1, cwB, scB);
;       } }
	v_and_b32_e32 v16, 0xf0f0f0f, v12
	v_mov_b32_e32 v17, 0
	v_lshrrev_b32_e32 v12, 4, v12
	v_dot4c_i32_i8_e32 v17, v16, v36
	v_and_b32_e32 v12, 0xf0f0f0f, v12
	v_dot4c_i32_i8_e32 v17, v12, v37
	v_and_b32_e32 v12, 0xf0f0f0f, v13
	v_mov_b32_e32 v16, 0
	v_dot4c_i32_i8_e32 v16, v12, v38
	v_lshrrev_b32_e32 v12, 4, v13
	v_and_b32_e32 v12, 0xf0f0f0f, v12
	v_dot4c_i32_i8_e32 v16, v12, v39
	v_and_b32_e32 v12, 0xf0f0f0f, v14
	v_dot4c_i32_i8_e32 v17, v12, v32
	v_lshrrev_b32_e32 v12, 4, v14
	v_and_b32_e32 v12, 0xf0f0f0f, v12
	v_dot4c_i32_i8_e32 v17, v12, v33
	v_and_b32_e32 v12, 0xf0f0f0f, v15
	v_dot4c_i32_i8_e32 v16, v12, v34
	v_lshrrev_b32_e32 v12, 4, v15
	v_and_b32_e32 v12, 0xf0f0f0f, v12
	v_dot4c_i32_i8_e32 v16, v12, v35
	s_waitcnt vmcnt(18)
	v_and_b32_e32 v12, 0xf0f0f0f, v8
	v_mov_b32_e32 v13, 0
	v_lshrrev_b32_e32 v8, 4, v8
	v_dot4c_i32_i8_e32 v13, v12, v36
	v_and_b32_e32 v8, 0xf0f0f0f, v8
	v_dot4c_i32_i8_e32 v13, v8, v37
	v_and_b32_e32 v8, 0xf0f0f0f, v9
	v_mov_b32_e32 v12, 0
	v_dot4c_i32_i8_e32 v12, v8, v38
	v_lshrrev_b32_e32 v8, 4, v9
	v_and_b32_e32 v8, 0xf0f0f0f, v8
	v_dot4c_i32_i8_e32 v12, v8, v39
	v_and_b32_e32 v8, 0xf0f0f0f, v10
	v_dot4c_i32_i8_e32 v13, v8, v32
	v_lshrrev_b32_e32 v8, 4, v10
	v_and_b32_e32 v8, 0xf0f0f0f, v8
	v_dot4c_i32_i8_e32 v13, v8, v33
	v_and_b32_e32 v8, 0xf0f0f0f, v11
	v_dot4c_i32_i8_e32 v12, v8, v34
	v_lshrrev_b32_e32 v8, 4, v11
	v_and_b32_e32 v8, 0xf0f0f0f, v8
	v_dot4c_i32_i8_e32 v12, v8, v35
	v_add_u32_e32 v10, v17, v16
	v_sub_u32_e32 v10, v10, v171
	v_and_b32_e32 v9, 0xffff0000, v41
	v_add_u32_e32 v11, v13, v12
	v_sub_u32_e32 v12, v11, v171
	v_cvt_f32_i32_e32 v11, v10
	v_cvt_f32_i32_e32 v10, v12
	v_lshlrev_b32_e32 v8, 16, v41
	v_pk_fma_f32 v[154:155], v[8:9], v[10:11], v[154:155]
	s_waitcnt vmcnt(17)
	v_and_b32_e32 v8, 0xf0f0f0f, v4
	v_mov_b32_e32 v9, 0
	v_lshrrev_b32_e32 v4, 4, v4
	v_dot4c_i32_i8_e32 v9, v8, v36
	v_and_b32_e32 v4, 0xf0f0f0f, v4
	v_dot4c_i32_i8_e32 v9, v4, v37
	v_and_b32_e32 v4, 0xf0f0f0f, v5
	v_mov_b32_e32 v8, 0
	v_dot4c_i32_i8_e32 v8, v4, v38
	v_lshrrev_b32_e32 v4, 4, v5
	v_and_b32_e32 v4, 0xf0f0f0f, v4
	v_dot4c_i32_i8_e32 v8, v4, v39
	v_and_b32_e32 v4, 0xf0f0f0f, v6
	v_dot4c_i32_i8_e32 v9, v4, v32
	v_lshrrev_b32_e32 v4, 4, v6
	v_and_b32_e32 v4, 0xf0f0f0f, v4
	v_dot4c_i32_i8_e32 v9, v4, v33
	v_and_b32_e32 v4, 0xf0f0f0f, v7
	v_dot4c_i32_i8_e32 v8, v4, v34
	v_lshrrev_b32_e32 v4, 4, v7
	v_and_b32_e32 v4, 0xf0f0f0f, v4
	v_dot4c_i32_i8_e32 v8, v4, v35
	s_waitcnt vmcnt(16)
	v_and_b32_e32 v4, 0xf0f0f0f, v0
	v_mov_b32_e32 v5, 0
	v_lshrrev_b32_e32 v0, 4, v0
	v_dot4c_i32_i8_e32 v5, v4, v36
	v_and_b32_e32 v0, 0xf0f0f0f, v0
	v_dot4c_i32_i8_e32 v5, v0, v37
	v_and_b32_e32 v0, 0xf0f0f0f, v1
	v_mov_b32_e32 v4, 0
	v_dot4c_i32_i8_e32 v4, v0, v38
	v_lshrrev_b32_e32 v0, 4, v1
	v_and_b32_e32 v0, 0xf0f0f0f, v0
	v_dot4c_i32_i8_e32 v4, v0, v39
	v_and_b32_e32 v0, 0xf0f0f0f, v2
	v_dot4c_i32_i8_e32 v5, v0, v32
	v_lshrrev_b32_e32 v0, 4, v2
	v_and_b32_e32 v0, 0xf0f0f0f, v0
	v_dot4c_i32_i8_e32 v5, v0, v33
	v_and_b32_e32 v0, 0xf0f0f0f, v3
	v_dot4c_i32_i8_e32 v4, v0, v34
	v_lshrrev_b32_e32 v0, 4, v3
	v_and_b32_e32 v0, 0xf0f0f0f, v0
	v_dot4c_i32_i8_e32 v4, v0, v35
	v_add_u32_e32 v2, v9, v8
	v_sub_u32_e32 v2, v2, v171
	v_and_b32_e32 v1, 0xffff0000, v40
	v_add_u32_e32 v3, v5, v4
	v_sub_u32_e32 v4, v3, v171
	v_cvt_f32_i32_e32 v3, v2
	v_cvt_f32_i32_e32 v2, v4
	v_lshlrev_b32_e32 v0, 16, v40
	v_pk_fma_f32 v[152:153], v[0:1], v[2:3], v[152:153]
	ds_read_u16 v0, v93 offset:16640
	ds_read_u16 v1, v93 offset:16656
	ds_read_u16 v2, v93 offset:16672
	ds_read_u16 v3, v93 offset:16688
	s_waitcnt lgkmcnt(3)
	v_add_u32_e32 v0, s44, v0
	v_lshl_or_b32 v4, v0, 7, v165
	s_waitcnt lgkmcnt(2)
	v_add_u32_e32 v1, s44, v1
	global_load_dwordx4 v[72:75], v4, s[0:1]
	v_lshl_or_b32 v4, v1, 7, v165
	s_waitcnt lgkmcnt(1)
	v_add_u32_e32 v2, s44, v2
	global_load_dwordx4 v[64:67], v4, s[0:1]
	v_lshl_or_b32 v4, v2, 7, v165
	s_waitcnt lgkmcnt(0)
	v_add_u32_e32 v3, s44, v3
	global_load_dwordx4 v[56:59], v4, s[0:1]
	v_lshl_or_b32 v4, v3, 7, v165
	global_load_dwordx4 v[48:51], v4, s[0:1]
	ds_read_u16 v4, v93 offset:16704
	v_lshl_or_b32 v0, v0, 4, v95
	v_lshl_or_b32 v1, v1, 4, v95
	v_lshl_or_b32 v2, v2, 4, v95
	v_lshl_or_b32 v3, v3, 4, v95
	s_waitcnt lgkmcnt(0)
	v_add_u32_e32 v4, s44, v4
	v_lshl_or_b32 v5, v4, 7, v165
	global_load_dwordx4 v[40:43], v5, s[0:1]
	ds_read_u16 v5, v93 offset:16720
	v_lshl_or_b32 v4, v4, 4, v95
	s_waitcnt lgkmcnt(0)
	v_add_u32_e32 v5, s44, v5
	v_lshl_or_b32 v6, v5, 7, v165
	global_load_dwordx4 v[24:27], v6, s[0:1]
	ds_read_u16 v6, v93 offset:16736
	v_lshl_or_b32 v5, v5, 4, v95
	s_waitcnt lgkmcnt(0)
	v_add_u32_e32 v6, s44, v6
	v_lshl_or_b32 v7, v6, 7, v165
	global_load_dwordx4 v[12:15], v7, s[0:1]
	ds_read_u16 v7, v93 offset:16752
	v_lshl_or_b32 v6, v6, 4, v95
	s_waitcnt lgkmcnt(0)
	v_add_u32_e32 v7, s44, v7
	v_lshl_or_b32 v8, v7, 7, v165
	global_load_dwordx4 v[8:11], v8, s[0:1]
	v_lshl_or_b32 v7, v7, 4, v95
	global_load_ushort v178, v1, s[18:19]
	global_load_ushort v179, v0, s[18:19]
	global_load_ushort v174, v3, s[18:19]
	global_load_ushort v175, v2, s[18:19]
	global_load_ushort v169, v5, s[18:19]
	global_load_ushort v170, v4, s[18:19]
	global_load_ushort v167, v7, s[18:19]
	global_load_ushort v168, v6, s[18:19]
	s_waitcnt vmcnt(31)
	v_and_b32_e32 v0, 0xf0f0f0f, v88
	v_mov_b32_e32 v2, 0
	v_dot4c_i32_i8_e32 v2, v0, v36
	v_lshrrev_b32_e32 v0, 4, v88
	v_and_b32_e32 v0, 0xf0f0f0f, v0
	v_dot4c_i32_i8_e32 v2, v0, v37
	v_and_b32_e32 v0, 0xf0f0f0f, v89
	v_mov_b32_e32 v3, 0
	v_dot4c_i32_i8_e32 v3, v0, v38
	v_lshrrev_b32_e32 v0, 4, v89
	v_and_b32_e32 v0, 0xf0f0f0f, v0
	v_dot4c_i32_i8_e32 v3, v0, v39
	v_and_b32_e32 v0, 0xf0f0f0f, v90
	v_dot4c_i32_i8_e32 v2, v0, v32
	v_lshrrev_b32_e32 v0, 4, v90
	v_and_b32_e32 v0, 0xf0f0f0f, v0
	v_dot4c_i32_i8_e32 v2, v0, v33
	v_and_b32_e32 v0, 0xf0f0f0f, v91
	v_dot4c_i32_i8_e32 v3, v0, v34
	v_lshrrev_b32_e32 v0, 4, v91
	v_and_b32_e32 v0, 0xf0f0f0f, v0
	v_dot4c_i32_i8_e32 v3, v0, v35
	s_waitcnt vmcnt(30)
; #define P12_ISSUE(c_, i_, h_, CW_, SC_) do { _Pragma("unroll") for (int bb = 0; bb < 8; ++bb) { const unsigned ro = (unsigned)(c_) * 16384u + (unsigned)EL[(i_) * 128 + ((h_) * 8 + bb) * 8 + g8]; \
;         CW_[bb] = *(const v4u*)(U4 + (size_t)(ro * 128u + 16u * (unsigned)k8)); SC_[bb] = USS[(size_t)(ro * 8u + (unsigned)k8)]; } } while (0)
; #define P12_COMP(i_, h_, CW_, SC_) do { _Pragma("unroll") for (int bb = 0; bb < 8; ++bb) { int a0 = 0, a1 = 0; P12_U4(CW_[bb].x, xa.x, xa.y, a0); P12_U4(CW_[bb].y, xa.z, xa.w, a1); P12_U4(CW_[bb].z, xb.x, xb.y, a0); P12_U4(CW_[bb].w, xb.z, xb.w, a1); \
;         psum[(i_)][(h_) * 8 + bb] += __uint_as_float(SC_[bb] << 16) * (float)((a0 + a1) - xo); } } while (0)
; #define P12_BAR() asm volatile("" ::: "memory")
; __device__ __forceinline__ void p12_peer(Frame& F) {
;     ...
;     { v4u cwA[8], cwB[8]; unsigned scA[8], scB[8]; v4u xa, xb; int xo;
;       P12_ISSUE(0, 0, 0, cwA, scA);
; _Pragma("nounroll")
;       for (int c = 0; c < 16; ++c) { const int cn = c + 1 < 16 ? c + 1 : 15;
;           P12_XQ(c, 0); P12_ISSUE(c, 0, 1, cwB, scB); P12_BAR(); P12_COMP(0, 0, cwA, scA); P12_ISSUE(c, 1, 0, cwA, scA); P12_BAR(); P12_COMP(0, 1, cwB, scB);
;           P12_XQ(c, 1); P12_ISSUE(c, 1, 1, cwB, scB); P12_BAR(); P12_COMP(1, 0, cwA, scA); P12_ISSUE(c, 2, 0, cwA, scA); P12_BAR(); P12_COMP(1, 1, cwB, scB);
;           P12_XQ(c, 2); P12_ISSUE(c, 2, 1, cwB, scB); P12_BAR(); P12_COMP(2, 0, cwA, scA); P12_ISSUE(c, 3, 0, cwA, scA); P12_BAR(); P12_COMP(2, 1, cwB, scB);
;           P12_XQ(c, 3); P12_ISSUE(c, 3, 1, cwB, scB); P12_BAR(); P12_COMP(3, 0, cwA, scA); P12_ISSUE(cn, 0, 0, cwA, scA); P12_BAR(); P12_COMP(3, 1, cwB, scB);
;       } }
	v_and_b32_e32 v0, 0xf0f0f0f, v84
	v_mov_b32_e32 v4, 0
	v_dot4c_i32_i8_e32 v4, v0, v36
	v_lshrrev_b32_e32 v0, 4, v84
	v_and_b32_e32 v0, 0xf0f0f0f, v0
	v_dot4c_i32_i8_e32 v4, v0, v37
	v_and_b32_e32 v0, 0xf0f0f0f, v85
	v_mov_b32_e32 v5, 0
	v_dot4c_i32_i8_e32 v5, v0, v38
	v_lshrrev_b32_e32 v0, 4, v85
	v_and_b32_e32 v0, 0xf0f0f0f, v0
	v_dot4c_i32_i8_e32 v5, v0, v39
	v_and_b32_e32 v0, 0xf0f0f0f, v86
	v_dot4c_i32_i8_e32 v4, v0, v32
	v_lshrrev_b32_e32 v0, 4, v86
	v_and_b32_e32 v0, 0xf0f0f0f, v0
	v_dot4c_i32_i8_e32 v4, v0, v33
	v_and_b32_e32 v0, 0xf0f0f0f, v87
	v_dot4c_i32_i8_e32 v5, v0, v34
	v_lshrrev_b32_e32 v0, 4, v87
	v_and_b32_e32 v0, 0xf0f0f0f, v0
	v_dot4c_i32_i8_e32 v5, v0, v35
	v_add_u32_e32 v2, v2, v3
	v_sub_u32_e32 v2, v2, v171
	s_waitcnt vmcnt(22)
	v_lshlrev_b32_e32 v1, 16, v183
	v_sub_u32_e32 v3, v5, v171
	v_add_u32_e32 v4, v3, v4
	v_cvt_f32_i32_e32 v3, v2
	v_cvt_f32_i32_e32 v2, v4
	v_lshlrev_b32_e32 v0, 16, v182
	v_mov_b32_e32 v4, 0
	v_mov_b32_e32 v5, 0
	v_pk_fma_f32 v[150:151], v[0:1], v[2:3], v[150:151]
	v_and_b32_e32 v0, 0xf0f0f0f, v80
	v_mov_b32_e32 v2, 0
	v_dot4c_i32_i8_e32 v2, v0, v36
	v_lshrrev_b32_e32 v0, 4, v80
	v_and_b32_e32 v0, 0xf0f0f0f, v0
	v_dot4c_i32_i8_e32 v2, v0, v37
	v_and_b32_e32 v0, 0xf0f0f0f, v81
	v_mov_b32_e32 v3, 0
	v_dot4c_i32_i8_e32 v3, v0, v38
	v_lshrrev_b32_e32 v0, 4, v81
	v_and_b32_e32 v0, 0xf0f0f0f, v0
	v_dot4c_i32_i8_e32 v3, v0, v39
	v_and_b32_e32 v0, 0xf0f0f0f, v82
	v_dot4c_i32_i8_e32 v2, v0, v32
	v_lshrrev_b32_e32 v0, 4, v82
	v_and_b32_e32 v0, 0xf0f0f0f, v0
	v_dot4c_i32_i8_e32 v2, v0, v33
	v_and_b32_e32 v0, 0xf0f0f0f, v83
	v_dot4c_i32_i8_e32 v3, v0, v34
	v_lshrrev_b32_e32 v0, 4, v83
	v_and_b32_e32 v0, 0xf0f0f0f, v0
	v_dot4c_i32_i8_e32 v3, v0, v35
	v_and_b32_e32 v0, 0xf0f0f0f, v76
	v_dot4c_i32_i8_e32 v4, v0, v36
	v_lshrrev_b32_e32 v0, 4, v76
	v_and_b32_e32 v0, 0xf0f0f0f, v0
	v_dot4c_i32_i8_e32 v4, v0, v37
	v_and_b32_e32 v0, 0xf0f0f0f, v77
	v_dot4c_i32_i8_e32 v5, v0, v38
	v_lshrrev_b32_e32 v0, 4, v77
	v_and_b32_e32 v0, 0xf0f0f0f, v0
	v_dot4c_i32_i8_e32 v5, v0, v39
	v_and_b32_e32 v0, 0xf0f0f0f, v78
	v_dot4c_i32_i8_e32 v4, v0, v32
	v_lshrrev_b32_e32 v0, 4, v78
	v_and_b32_e32 v0, 0xf0f0f0f, v0
	v_dot4c_i32_i8_e32 v4, v0, v33
	v_and_b32_e32 v0, 0xf0f0f0f, v79
	v_dot4c_i32_i8_e32 v5, v0, v34
	v_lshrrev_b32_e32 v0, 4, v79
	v_and_b32_e32 v0, 0xf0f0f0f, v0
	v_dot4c_i32_i8_e32 v5, v0, v35
	v_sub_u32_e32 v3, v3, v171
	v_add_u32_e32 v2, v3, v2
	v_cvt_f32_i32_e32 v3, v2
	v_sub_u32_e32 v5, v5, v171
	v_add_u32_e32 v4, v5, v4
	v_cvt_f32_i32_e32 v2, v4
	s_waitcnt vmcnt(20)
	v_lshlrev_b32_e32 v1, 16, v181
	v_lshlrev_b32_e32 v0, 16, v180
	v_mov_b32_e32 v4, 0
	v_pk_fma_f32 v[148:149], v[0:1], v[2:3], v[148:149]
	v_and_b32_e32 v0, 0xf0f0f0f, v68
	v_mov_b32_e32 v2, 0
	v_dot4c_i32_i8_e32 v2, v0, v36
	v_lshrrev_b32_e32 v0, 4, v68
	v_and_b32_e32 v0, 0xf0f0f0f, v0
	v_dot4c_i32_i8_e32 v2, v0, v37
	v_and_b32_e32 v0, 0xf0f0f0f, v69
	v_mov_b32_e32 v3, 0
	v_dot4c_i32_i8_e32 v3, v0, v38
	v_lshrrev_b32_e32 v0, 4, v69
	v_and_b32_e32 v0, 0xf0f0f0f, v0
	v_dot4c_i32_i8_e32 v3, v0, v39
	v_and_b32_e32 v0, 0xf0f0f0f, v70
	v_dot4c_i32_i8_e32 v2, v0, v32
	v_lshrrev_b32_e32 v0, 4, v70
	v_and_b32_e32 v0, 0xf0f0f0f, v0
	v_dot4c_i32_i8_e32 v2, v0, v33
	v_and_b32_e32 v0, 0xf0f0f0f, v71
	v_dot4c_i32_i8_e32 v3, v0, v34
	v_lshrrev_b32_e32 v0, 4, v71
	v_and_b32_e32 v0, 0xf0f0f0f, v0
	v_dot4c_i32_i8_e32 v3, v0, v35
	v_and_b32_e32 v0, 0xf0f0f0f, v60
	v_dot4c_i32_i8_e32 v4, v0, v36
	v_lshrrev_b32_e32 v0, 4, v60
	v_and_b32_e32 v0, 0xf0f0f0f, v0
	v_dot4c_i32_i8_e32 v4, v0, v37
	v_and_b32_e32 v0, 0xf0f0f0f, v61
	v_mov_b32_e32 v5, 0
	v_dot4c_i32_i8_e32 v5, v0, v38
	v_lshrrev_b32_e32 v0, 4, v61
	v_and_b32_e32 v0, 0xf0f0f0f, v0
	v_dot4c_i32_i8_e32 v5, v0, v39
	v_and_b32_e32 v0, 0xf0f0f0f, v62
	v_dot4c_i32_i8_e32 v4, v0, v32
	v_lshrrev_b32_e32 v0, 4, v62
	v_and_b32_e32 v0, 0xf0f0f0f, v0
	v_dot4c_i32_i8_e32 v4, v0, v33
	v_and_b32_e32 v0, 0xf0f0f0f, v63
	v_dot4c_i32_i8_e32 v5, v0, v34
	v_lshrrev_b32_e32 v0, 4, v63
	v_and_b32_e32 v0, 0xf0f0f0f, v0
	v_dot4c_i32_i8_e32 v5, v0, v35
	v_sub_u32_e32 v3, v3, v171
	v_add_u32_e32 v2, v3, v2
	v_cvt_f32_i32_e32 v3, v2
	v_sub_u32_e32 v5, v5, v171
	v_add_u32_e32 v4, v5, v4
	v_cvt_f32_i32_e32 v2, v4
	s_waitcnt vmcnt(18)
	v_lshlrev_b32_e32 v1, 16, v177
	v_lshlrev_b32_e32 v0, 16, v176
	v_mov_b32_e32 v4, 0
	v_pk_fma_f32 v[146:147], v[0:1], v[2:3], v[146:147]
	v_and_b32_e32 v0, 0xf0f0f0f, v52
	v_mov_b32_e32 v2, 0
	v_dot4c_i32_i8_e32 v2, v0, v36
	v_lshrrev_b32_e32 v0, 4, v52
	v_and_b32_e32 v0, 0xf0f0f0f, v0
	v_dot4c_i32_i8_e32 v2, v0, v37
	v_and_b32_e32 v0, 0xf0f0f0f, v53
	v_mov_b32_e32 v3, 0
	v_dot4c_i32_i8_e32 v3, v0, v38
	v_lshrrev_b32_e32 v0, 4, v53
	v_and_b32_e32 v0, 0xf0f0f0f, v0
	v_dot4c_i32_i8_e32 v3, v0, v39
	v_and_b32_e32 v0, 0xf0f0f0f, v54
	v_dot4c_i32_i8_e32 v2, v0, v32
	v_lshrrev_b32_e32 v0, 4, v54
	v_and_b32_e32 v0, 0xf0f0f0f, v0
	v_dot4c_i32_i8_e32 v2, v0, v33
	v_and_b32_e32 v0, 0xf0f0f0f, v55
	v_dot4c_i32_i8_e32 v3, v0, v34
	v_lshrrev_b32_e32 v0, 4, v55
	v_and_b32_e32 v0, 0xf0f0f0f, v0
	v_dot4c_i32_i8_e32 v3, v0, v35
	v_and_b32_e32 v0, 0xf0f0f0f, v44
	v_dot4c_i32_i8_e32 v4, v0, v36
	v_lshrrev_b32_e32 v0, 4, v44
	v_and_b32_e32 v0, 0xf0f0f0f, v0
	v_dot4c_i32_i8_e32 v4, v0, v37
	v_and_b32_e32 v0, 0xf0f0f0f, v45
	v_mov_b32_e32 v5, 0
	v_dot4c_i32_i8_e32 v5, v0, v38
	v_lshrrev_b32_e32 v0, 4, v45
	v_and_b32_e32 v0, 0xf0f0f0f, v0
	v_dot4c_i32_i8_e32 v5, v0, v39
	v_and_b32_e32 v0, 0xf0f0f0f, v46
	v_dot4c_i32_i8_e32 v4, v0, v32
	v_lshrrev_b32_e32 v0, 4, v46
	v_and_b32_e32 v0, 0xf0f0f0f, v0
	v_dot4c_i32_i8_e32 v4, v0, v33
	v_and_b32_e32 v0, 0xf0f0f0f, v47
	v_dot4c_i32_i8_e32 v5, v0, v34
	v_lshrrev_b32_e32 v0, 4, v47
	v_and_b32_e32 v0, 0xf0f0f0f, v0
	v_dot4c_i32_i8_e32 v5, v0, v35
	v_sub_u32_e32 v3, v3, v171
	v_add_u32_e32 v2, v3, v2
	v_cvt_f32_i32_e32 v3, v2
	v_sub_u32_e32 v5, v5, v171
	v_add_u32_e32 v4, v5, v4
	v_cvt_f32_i32_e32 v2, v4
	s_waitcnt vmcnt(16)
; #define P12_ISSUE(c_, i_, h_, CW_, SC_) do { _Pragma("unroll") for (int bb = 0; bb < 8; ++bb) { const unsigned ro = (unsigned)(c_) * 16384u + (unsigned)EL[(i_) * 128 + ((h_) * 8 + bb) * 8 + g8]; \
;         CW_[bb] = *(const v4u*)(U4 + (size_t)(ro * 128u + 16u * (unsigned)k8)); SC_[bb] = USS[(size_t)(ro * 8u + (unsigned)k8)]; } } while (0)
; #define P12_COMP(i_, h_, CW_, SC_) do { _Pragma("unroll") for (int bb = 0; bb < 8; ++bb) { int a0 = 0, a1 = 0; P12_U4(CW_[bb].x, xa.x, xa.y, a0); P12_U4(CW_[bb].y, xa.z, xa.w, a1); P12_U4(CW_[bb].z, xb.x, xb.y, a0); P12_U4(CW_[bb].w, xb.z, xb.w, a1); \
;         psum[(i_)][(h_) * 8 + bb] += __uint_as_float(SC_[bb] << 16) * (float)((a0 + a1) - xo); } } while (0)
; #define P12_BAR() asm volatile("" ::: "memory")
; __device__ __forceinline__ void p12_peer(Frame& F) {
;     ...
;     { v4u cwA[8], cwB[8]; unsigned scA[8], scB[8]; v4u xa, xb; int xo;
;       P12_ISSUE(0, 0, 0, cwA, scA);
; _Pragma("nounroll")
;       for (int c = 0; c < 16; ++c) { const int cn = c + 1 < 16 ? c + 1 : 15;
;           P12_XQ(c, 0); P12_ISSUE(c, 0, 1, cwB, scB); P12_BAR(); P12_COMP(0, 0, cwA, scA); P12_ISSUE(c, 1, 0, cwA, scA); P12_BAR(); P12_COMP(0, 1, cwB, scB);
;           P12_XQ(c, 1); P12_ISSUE(c, 1, 1, cwB, scB); P12_BAR(); P12_COMP(1, 0, cwA, scA); P12_ISSUE(c, 2, 0, cwA, scA); P12_BAR(); P12_COMP(1, 1, cwB, scB);
;           P12_XQ(c, 2); P12_ISSUE(c, 2, 1, cwB, scB); P12_BAR(); P12_COMP(2, 0, cwA, scA); P12_ISSUE(c, 3, 0, cwA, scA); P12_BAR(); P12_COMP(2, 1, cwB, scB);
;           P12_XQ(c, 3); P12_ISSUE(c, 3, 1, cwB, scB); P12_BAR(); P12_COMP(3, 0, cwA, scA); P12_ISSUE(cn, 0, 0, cwA, scA); P12_BAR(); P12_COMP(3, 1, cwB, scB);
;       } }
	v_lshlrev_b32_e32 v1, 16, v173
	v_lshlrev_b32_e32 v0, 16, v172
	v_pk_fma_f32 v[144:145], v[0:1], v[2:3], v[144:145]
	ds_read_b128 v[4:7], v166 offset:4096
	ds_read_b128 v[0:3], v166 offset:4112
	ds_read_u16 v16, v93 offset:16768
	ds_read_u16 v17, v93 offset:16784
	ds_read_u16 v18, v93 offset:16800
	ds_read_u16 v19, v93 offset:16816
	v_mov_b32_e32 v44, 0
	s_waitcnt lgkmcnt(3)
	v_add_u32_e32 v16, s44, v16
	v_lshl_or_b32 v20, v16, 7, v165
	v_lshl_or_b32 v45, v16, 4, v95
	s_waitcnt lgkmcnt(2)
	v_add_u32_e32 v16, s44, v17
	v_lshl_or_b32 v17, v16, 7, v165
	v_lshl_or_b32 v46, v16, 4, v95
	s_waitcnt lgkmcnt(1)
	v_add_u32_e32 v16, s44, v18
	global_load_dwordx4 v[80:83], v20, s[0:1]
	global_load_dwordx4 v[68:71], v17, s[0:1]
	v_lshl_or_b32 v17, v16, 7, v165
	v_lshl_or_b32 v47, v16, 4, v95
	s_waitcnt lgkmcnt(0)
	v_add_u32_e32 v16, s44, v19
	global_load_dwordx4 v[52:55], v17, s[0:1]
	v_lshl_or_b32 v17, v16, 7, v165
	v_lshl_or_b32 v60, v16, 4, v95
	ds_read_u16 v16, v93 offset:16832
	global_load_dwordx4 v[36:39], v17, s[0:1]
	v_dot4c_i32_i8_e32 v44, 0x1010101, v4
	v_dot4c_i32_i8_e32 v44, 0x1010101, v5
	v_dot4c_i32_i8_e32 v44, 0x1010101, v6
	s_waitcnt lgkmcnt(0)
	v_add_u32_e32 v16, s44, v16
	v_lshl_or_b32 v17, v16, 7, v165
	v_lshl_or_b32 v61, v16, 4, v95
	ds_read_u16 v16, v93 offset:16848
	global_load_dwordx4 v[32:35], v17, s[0:1]
	v_dot4c_i32_i8_e32 v44, 0x1010101, v7
	v_dot4c_i32_i8_e32 v44, 0x1010101, v0
	v_dot4c_i32_i8_e32 v44, 0x1010101, v1
	s_waitcnt lgkmcnt(0)
	v_add_u32_e32 v16, s44, v16
	v_lshl_or_b32 v17, v16, 7, v165
	v_lshl_or_b32 v62, v16, 4, v95
	ds_read_u16 v16, v93 offset:16864
	global_load_dwordx4 v[28:31], v17, s[0:1]
	v_dot4c_i32_i8_e32 v44, 0x1010101, v2
	v_dot4c_i32_i8_e32 v44, 0x1010101, v3
	s_waitcnt lgkmcnt(0)
	v_add_u32_e32 v16, s44, v16
	v_lshl_or_b32 v17, v16, 7, v165
	v_lshl_or_b32 v63, v16, 4, v95
	ds_read_u16 v16, v93 offset:16880
	global_load_dwordx4 v[20:23], v17, s[0:1]
	v_lshlrev_b32_e32 v84, 3, v44
	s_waitcnt vmcnt(22)
	v_and_b32_e32 v44, 0xf0f0f0f, v72
	s_waitcnt lgkmcnt(0)
	v_add_u32_e32 v76, s44, v16
	v_lshl_or_b32 v16, v76, 7, v165
	global_load_dwordx4 v[16:19], v16, s[0:1]
	v_lshl_or_b32 v76, v76, 4, v95
	global_load_ushort v180, v46, s[18:19]
	global_load_ushort v181, v45, s[18:19]
	global_load_ushort v172, v60, s[18:19]
	global_load_ushort v173, v47, s[18:19]
	global_load_ushort v87, v62, s[18:19]
	global_load_ushort v171, v61, s[18:19]
	global_load_ushort v85, v76, s[18:19]
	global_load_ushort v86, v63, s[18:19]
	v_mov_b32_e32 v46, 0
	v_dot4c_i32_i8_e32 v46, v44, v4
	v_lshrrev_b32_e32 v44, 4, v72
	v_and_b32_e32 v44, 0xf0f0f0f, v44
	v_dot4c_i32_i8_e32 v46, v44, v5
	v_and_b32_e32 v44, 0xf0f0f0f, v73
	v_mov_b32_e32 v47, 0
	v_dot4c_i32_i8_e32 v47, v44, v6
	v_lshrrev_b32_e32 v44, 4, v73
	v_and_b32_e32 v44, 0xf0f0f0f, v44
	v_dot4c_i32_i8_e32 v47, v44, v7
	v_and_b32_e32 v44, 0xf0f0f0f, v74
	v_dot4c_i32_i8_e32 v46, v44, v0
	v_lshrrev_b32_e32 v44, 4, v74
	v_and_b32_e32 v44, 0xf0f0f0f, v44
	v_dot4c_i32_i8_e32 v46, v44, v1
	v_and_b32_e32 v44, 0xf0f0f0f, v75
	v_dot4c_i32_i8_e32 v47, v44, v2
	v_lshrrev_b32_e32 v44, 4, v75
	v_and_b32_e32 v44, 0xf0f0f0f, v44
	v_dot4c_i32_i8_e32 v47, v44, v3
	s_waitcnt vmcnt(30)
	v_and_b32_e32 v44, 0xf0f0f0f, v64
	v_mov_b32_e32 v60, 0
	v_dot4c_i32_i8_e32 v60, v44, v4
	v_lshrrev_b32_e32 v44, 4, v64
	v_and_b32_e32 v44, 0xf0f0f0f, v44
	v_dot4c_i32_i8_e32 v60, v44, v5
	v_and_b32_e32 v44, 0xf0f0f0f, v65
	v_mov_b32_e32 v61, 0
	v_dot4c_i32_i8_e32 v61, v44, v6
	v_lshrrev_b32_e32 v44, 4, v65
	v_and_b32_e32 v44, 0xf0f0f0f, v44
	v_dot4c_i32_i8_e32 v61, v44, v7
	v_and_b32_e32 v44, 0xf0f0f0f, v66
	v_dot4c_i32_i8_e32 v60, v44, v0
	v_lshrrev_b32_e32 v44, 4, v66
	v_and_b32_e32 v44, 0xf0f0f0f, v44
	v_dot4c_i32_i8_e32 v60, v44, v1
	v_and_b32_e32 v44, 0xf0f0f0f, v67
	v_dot4c_i32_i8_e32 v61, v44, v2
	v_lshrrev_b32_e32 v44, 4, v67
	v_and_b32_e32 v44, 0xf0f0f0f, v44
	v_dot4c_i32_i8_e32 v61, v44, v3
	v_add_u32_e32 v46, v46, v47
	v_sub_u32_e32 v46, v46, v84
	s_waitcnt vmcnt(22)
	v_lshlrev_b32_e32 v45, 16, v179
	v_add_u32_e32 v47, v60, v61
	v_sub_u32_e32 v60, v47, v84
	v_cvt_f32_i32_e32 v47, v46
	v_cvt_f32_i32_e32 v46, v60
	v_lshlrev_b32_e32 v44, 16, v178
	v_pk_fma_f32 v[142:143], v[44:45], v[46:47], v[142:143]
	v_and_b32_e32 v44, 0xf0f0f0f, v56
	v_mov_b32_e32 v46, 0
	v_dot4c_i32_i8_e32 v46, v44, v4
	v_lshrrev_b32_e32 v44, 4, v56
	v_and_b32_e32 v44, 0xf0f0f0f, v44
	v_dot4c_i32_i8_e32 v46, v44, v5
	v_and_b32_e32 v44, 0xf0f0f0f, v57
	v_mov_b32_e32 v47, 0
	v_dot4c_i32_i8_e32 v47, v44, v6
	v_lshrrev_b32_e32 v44, 4, v57
	v_and_b32_e32 v44, 0xf0f0f0f, v44
	v_dot4c_i32_i8_e32 v47, v44, v7
	v_and_b32_e32 v44, 0xf0f0f0f, v58
	v_dot4c_i32_i8_e32 v46, v44, v0
	v_lshrrev_b32_e32 v44, 4, v58
	v_and_b32_e32 v44, 0xf0f0f0f, v44
	v_dot4c_i32_i8_e32 v46, v44, v1
	v_and_b32_e32 v44, 0xf0f0f0f, v59
	v_dot4c_i32_i8_e32 v47, v44, v2
	v_lshrrev_b32_e32 v44, 4, v59
	v_and_b32_e32 v44, 0xf0f0f0f, v44
	v_dot4c_i32_i8_e32 v47, v44, v3
	v_and_b32_e32 v44, 0xf0f0f0f, v48
	v_mov_b32_e32 v56, 0
	v_dot4c_i32_i8_e32 v56, v44, v4
	v_lshrrev_b32_e32 v44, 4, v48
	v_and_b32_e32 v44, 0xf0f0f0f, v44
	v_dot4c_i32_i8_e32 v56, v44, v5
	v_and_b32_e32 v44, 0xf0f0f0f, v49
	v_mov_b32_e32 v48, 0
	v_dot4c_i32_i8_e32 v48, v44, v6
	v_lshrrev_b32_e32 v44, 4, v49
	v_and_b32_e32 v44, 0xf0f0f0f, v44
	v_dot4c_i32_i8_e32 v48, v44, v7
	v_and_b32_e32 v44, 0xf0f0f0f, v50
	v_dot4c_i32_i8_e32 v56, v44, v0
	v_lshrrev_b32_e32 v44, 4, v50
	v_and_b32_e32 v44, 0xf0f0f0f, v44
	v_dot4c_i32_i8_e32 v56, v44, v1
	v_and_b32_e32 v44, 0xf0f0f0f, v51
	v_dot4c_i32_i8_e32 v48, v44, v2
	v_lshrrev_b32_e32 v44, 4, v51
	v_and_b32_e32 v44, 0xf0f0f0f, v44
	v_dot4c_i32_i8_e32 v48, v44, v3
	v_add_u32_e32 v46, v46, v47
	v_sub_u32_e32 v46, v46, v84
	s_waitcnt vmcnt(20)
; #define P12_ISSUE(c_, i_, h_, CW_, SC_) do { _Pragma("unroll") for (int bb = 0; bb < 8; ++bb) { const unsigned ro = (unsigned)(c_) * 16384u + (unsigned)EL[(i_) * 128 + ((h_) * 8 + bb) * 8 + g8]; \
;         CW_[bb] = *(const v4u*)(U4 + (size_t)(ro * 128u + 16u * (unsigned)k8)); SC_[bb] = USS[(size_t)(ro * 8u + (unsigned)k8)]; } } while (0)
; #define P12_COMP(i_, h_, CW_, SC_) do { _Pragma("unroll") for (int bb = 0; bb < 8; ++bb) { int a0 = 0, a1 = 0; P12_U4(CW_[bb].x, xa.x, xa.y, a0); P12_U4(CW_[bb].y, xa.z, xa.w, a1); P12_U4(CW_[bb].z, xb.x, xb.y, a0); P12_U4(CW_[bb].w, xb.z, xb.w, a1); \
;         psum[(i_)][(h_) * 8 + bb] += __uint_as_float(SC_[bb] << 16) * (float)((a0 + a1) - xo); } } while (0)
; #define P12_BAR() asm volatile("" ::: "memory")
; __device__ __forceinline__ void p12_peer(Frame& F) {
;     ...
;     { v4u cwA[8], cwB[8]; unsigned scA[8], scB[8]; v4u xa, xb; int xo;
;       P12_ISSUE(0, 0, 0, cwA, scA);
; _Pragma("nounroll")
;       for (int c = 0; c < 16; ++c) { const int cn = c + 1 < 16 ? c + 1 : 15;
;           P12_XQ(c, 0); P12_ISSUE(c, 0, 1, cwB, scB); P12_BAR(); P12_COMP(0, 0, cwA, scA); P12_ISSUE(c, 1, 0, cwA, scA); P12_BAR(); P12_COMP(0, 1, cwB, scB);
;           P12_XQ(c, 1); P12_ISSUE(c, 1, 1, cwB, scB); P12_BAR(); P12_COMP(1, 0, cwA, scA); P12_ISSUE(c, 2, 0, cwA, scA); P12_BAR(); P12_COMP(1, 1, cwB, scB);
;           P12_XQ(c, 2); P12_ISSUE(c, 2, 1, cwB, scB); P12_BAR(); P12_COMP(2, 0, cwA, scA); P12_ISSUE(c, 3, 0, cwA, scA); P12_BAR(); P12_COMP(2, 1, cwB, scB);
;           P12_XQ(c, 3); P12_ISSUE(c, 3, 1, cwB, scB); P12_BAR(); P12_COMP(3, 0, cwA, scA); P12_ISSUE(cn, 0, 0, cwA, scA); P12_BAR(); P12_COMP(3, 1, cwB, scB);
;       } }
	v_lshlrev_b32_e32 v45, 16, v175
	v_add_u32_e32 v47, v56, v48
	v_sub_u32_e32 v48, v47, v84
	v_cvt_f32_i32_e32 v47, v46
	v_cvt_f32_i32_e32 v46, v48
	v_lshlrev_b32_e32 v44, 16, v174
	v_pk_fma_f32 v[140:141], v[44:45], v[46:47], v[140:141]
	v_and_b32_e32 v44, 0xf0f0f0f, v40
	v_mov_b32_e32 v45, 0
	v_lshrrev_b32_e32 v40, 4, v40
	v_dot4c_i32_i8_e32 v45, v44, v4
	v_and_b32_e32 v40, 0xf0f0f0f, v40
	v_dot4c_i32_i8_e32 v45, v40, v5
	v_and_b32_e32 v40, 0xf0f0f0f, v41
	v_mov_b32_e32 v44, 0
	v_dot4c_i32_i8_e32 v44, v40, v6
	v_lshrrev_b32_e32 v40, 4, v41
	v_and_b32_e32 v40, 0xf0f0f0f, v40
	v_dot4c_i32_i8_e32 v44, v40, v7
	v_and_b32_e32 v40, 0xf0f0f0f, v42
	v_dot4c_i32_i8_e32 v45, v40, v0
	v_lshrrev_b32_e32 v40, 4, v42
	v_and_b32_e32 v40, 0xf0f0f0f, v40
	v_dot4c_i32_i8_e32 v45, v40, v1
	v_and_b32_e32 v40, 0xf0f0f0f, v43
	v_dot4c_i32_i8_e32 v44, v40, v2
	v_lshrrev_b32_e32 v40, 4, v43
	v_and_b32_e32 v40, 0xf0f0f0f, v40
	v_dot4c_i32_i8_e32 v44, v40, v3
	v_and_b32_e32 v40, 0xf0f0f0f, v24
	v_mov_b32_e32 v41, 0
	v_lshrrev_b32_e32 v24, 4, v24
	v_dot4c_i32_i8_e32 v41, v40, v4
	v_and_b32_e32 v24, 0xf0f0f0f, v24
	v_dot4c_i32_i8_e32 v41, v24, v5
	v_and_b32_e32 v24, 0xf0f0f0f, v25
	v_mov_b32_e32 v40, 0
	v_dot4c_i32_i8_e32 v40, v24, v6
	v_lshrrev_b32_e32 v24, 4, v25
	v_and_b32_e32 v24, 0xf0f0f0f, v24
	v_dot4c_i32_i8_e32 v40, v24, v7
	v_and_b32_e32 v24, 0xf0f0f0f, v26
	v_dot4c_i32_i8_e32 v41, v24, v0
	v_lshrrev_b32_e32 v24, 4, v26
	v_and_b32_e32 v24, 0xf0f0f0f, v24
	v_dot4c_i32_i8_e32 v41, v24, v1
	v_and_b32_e32 v24, 0xf0f0f0f, v27
	v_dot4c_i32_i8_e32 v40, v24, v2
	v_lshrrev_b32_e32 v24, 4, v27
	v_and_b32_e32 v24, 0xf0f0f0f, v24
	v_dot4c_i32_i8_e32 v40, v24, v3
	v_add_u32_e32 v26, v45, v44
	v_sub_u32_e32 v26, v26, v84
	s_waitcnt vmcnt(18)
	v_lshlrev_b32_e32 v25, 16, v170
	v_add_u32_e32 v27, v41, v40
	v_sub_u32_e32 v40, v27, v84
	v_cvt_f32_i32_e32 v27, v26
	v_cvt_f32_i32_e32 v26, v40
	v_lshlrev_b32_e32 v24, 16, v169
	v_pk_fma_f32 v[138:139], v[24:25], v[26:27], v[138:139]
	v_and_b32_e32 v24, 0xf0f0f0f, v12
	v_mov_b32_e32 v25, 0
	v_lshrrev_b32_e32 v12, 4, v12
	v_dot4c_i32_i8_e32 v25, v24, v4
	v_and_b32_e32 v12, 0xf0f0f0f, v12
	v_dot4c_i32_i8_e32 v25, v12, v5
	v_and_b32_e32 v12, 0xf0f0f0f, v13
	v_mov_b32_e32 v24, 0
	v_dot4c_i32_i8_e32 v24, v12, v6
	v_lshrrev_b32_e32 v12, 4, v13
	v_and_b32_e32 v12, 0xf0f0f0f, v12
	v_dot4c_i32_i8_e32 v24, v12, v7
	v_and_b32_e32 v12, 0xf0f0f0f, v14
	v_dot4c_i32_i8_e32 v25, v12, v0
	v_lshrrev_b32_e32 v12, 4, v14
	v_and_b32_e32 v12, 0xf0f0f0f, v12
	v_dot4c_i32_i8_e32 v25, v12, v1
	v_and_b32_e32 v12, 0xf0f0f0f, v15
	v_dot4c_i32_i8_e32 v24, v12, v2
	v_lshrrev_b32_e32 v12, 4, v15
	v_and_b32_e32 v12, 0xf0f0f0f, v12
	v_dot4c_i32_i8_e32 v24, v12, v3
	v_and_b32_e32 v12, 0xf0f0f0f, v8
	v_mov_b32_e32 v13, 0
	v_lshrrev_b32_e32 v8, 4, v8
	v_dot4c_i32_i8_e32 v13, v12, v4
	v_and_b32_e32 v8, 0xf0f0f0f, v8
	v_dot4c_i32_i8_e32 v13, v8, v5
	v_and_b32_e32 v8, 0xf0f0f0f, v9
	v_mov_b32_e32 v12, 0
	v_dot4c_i32_i8_e32 v12, v8, v6
	v_lshrrev_b32_e32 v8, 4, v9
	v_and_b32_e32 v8, 0xf0f0f0f, v8
	v_dot4c_i32_i8_e32 v12, v8, v7
	v_and_b32_e32 v8, 0xf0f0f0f, v10
	v_dot4c_i32_i8_e32 v13, v8, v0
	v_lshrrev_b32_e32 v8, 4, v10
	v_and_b32_e32 v8, 0xf0f0f0f, v8
	v_dot4c_i32_i8_e32 v13, v8, v1
	v_and_b32_e32 v8, 0xf0f0f0f, v11
	v_dot4c_i32_i8_e32 v12, v8, v2
	v_lshrrev_b32_e32 v8, 4, v11
	v_and_b32_e32 v8, 0xf0f0f0f, v8
	v_dot4c_i32_i8_e32 v12, v8, v3
	v_add_u32_e32 v10, v25, v24
	v_sub_u32_e32 v10, v10, v84
	s_waitcnt vmcnt(16)
	v_lshlrev_b32_e32 v9, 16, v168
	v_add_u32_e32 v11, v13, v12
	v_sub_u32_e32 v12, v11, v84
	v_cvt_f32_i32_e32 v11, v10
	v_cvt_f32_i32_e32 v10, v12
	v_lshlrev_b32_e32 v8, 16, v167
	v_pk_fma_f32 v[136:137], v[8:9], v[10:11], v[136:137]
	ds_read_u16 v8, v93 offset:16896
	ds_read_u16 v9, v93 offset:16912
	ds_read_u16 v10, v93 offset:16928
	ds_read_u16 v11, v93 offset:16944
	s_waitcnt lgkmcnt(3)
	v_add_u32_e32 v8, s44, v8
	v_lshl_or_b32 v12, v8, 7, v165
	v_lshl_or_b32 v40, v8, 4, v95
	s_waitcnt lgkmcnt(2)
	v_add_u32_e32 v8, s44, v9
	v_lshl_or_b32 v9, v8, 7, v165
	v_lshl_or_b32 v41, v8, 4, v95
	s_waitcnt lgkmcnt(1)
	v_add_u32_e32 v8, s44, v10
	global_load_dwordx4 v[76:79], v12, s[0:1]
	global_load_dwordx4 v[72:75], v9, s[0:1]
	v_lshl_or_b32 v9, v8, 7, v165
	v_lshl_or_b32 v42, v8, 4, v95
	s_waitcnt lgkmcnt(0)
	v_add_u32_e32 v8, s44, v11
	global_load_dwordx4 v[60:63], v9, s[0:1]
	v_lshl_or_b32 v9, v8, 7, v165
	v_lshl_or_b32 v43, v8, 4, v95
	ds_read_u16 v8, v93 offset:16960
	global_load_dwordx4 v[56:59], v9, s[0:1]
	s_waitcnt lgkmcnt(0)
	v_add_u32_e32 v8, s44, v8
	v_lshl_or_b32 v9, v8, 7, v165
	v_lshl_or_b32 v48, v8, 4, v95
	ds_read_u16 v8, v93 offset:16976
	global_load_dwordx4 v[44:47], v9, s[0:1]
	s_waitcnt lgkmcnt(0)
	v_add_u32_e32 v8, s44, v8
	v_lshl_or_b32 v9, v8, 7, v165
	v_lshl_or_b32 v49, v8, 4, v95
	ds_read_u16 v8, v93 offset:16992
	global_load_dwordx4 v[24:27], v9, s[0:1]
	s_waitcnt lgkmcnt(0)
	v_add_u32_e32 v8, s44, v8
	v_lshl_or_b32 v9, v8, 7, v165
	v_lshl_or_b32 v50, v8, 4, v95
	ds_read_u16 v8, v93 offset:17008
	global_load_dwordx4 v[12:15], v9, s[0:1]
	s_waitcnt lgkmcnt(0)
	v_add_u32_e32 v51, s44, v8
	v_lshl_or_b32 v8, v51, 7, v165
	global_load_dwordx4 v[8:11], v8, s[0:1]
	v_lshl_or_b32 v51, v51, 4, v95
	global_load_ushort v176, v41, s[18:19]
	global_load_ushort v177, v40, s[18:19]
	global_load_ushort v167, v43, s[18:19]
	global_load_ushort v168, v42, s[18:19]
	global_load_ushort v90, v49, s[18:19]
	global_load_ushort v91, v48, s[18:19]
	global_load_ushort v88, v51, s[18:19]
	global_load_ushort v89, v50, s[18:19]
	s_waitcnt vmcnt(31)
; #define P12_ISSUE(c_, i_, h_, CW_, SC_) do { _Pragma("unroll") for (int bb = 0; bb < 8; ++bb) { const unsigned ro = (unsigned)(c_) * 16384u + (unsigned)EL[(i_) * 128 + ((h_) * 8 + bb) * 8 + g8]; \
;         CW_[bb] = *(const v4u*)(U4 + (size_t)(ro * 128u + 16u * (unsigned)k8)); SC_[bb] = USS[(size_t)(ro * 8u + (unsigned)k8)]; } } while (0)
; #define P12_COMP(i_, h_, CW_, SC_) do { _Pragma("unroll") for (int bb = 0; bb < 8; ++bb) { int a0 = 0, a1 = 0; P12_U4(CW_[bb].x, xa.x, xa.y, a0); P12_U4(CW_[bb].y, xa.z, xa.w, a1); P12_U4(CW_[bb].z, xb.x, xb.y, a0); P12_U4(CW_[bb].w, xb.z, xb.w, a1); \
;         psum[(i_)][(h_) * 8 + bb] += __uint_as_float(SC_[bb] << 16) * (float)((a0 + a1) - xo); } } while (0)
; #define P12_BAR() asm volatile("" ::: "memory")
; __device__ __forceinline__ void p12_peer(Frame& F) {
;     ...
;     { v4u cwA[8], cwB[8]; unsigned scA[8], scB[8]; v4u xa, xb; int xo;
;       P12_ISSUE(0, 0, 0, cwA, scA);
; _Pragma("nounroll")
;       for (int c = 0; c < 16; ++c) { const int cn = c + 1 < 16 ? c + 1 : 15;
;           P12_XQ(c, 0); P12_ISSUE(c, 0, 1, cwB, scB); P12_BAR(); P12_COMP(0, 0, cwA, scA); P12_ISSUE(c, 1, 0, cwA, scA); P12_BAR(); P12_COMP(0, 1, cwB, scB);
;           P12_XQ(c, 1); P12_ISSUE(c, 1, 1, cwB, scB); P12_BAR(); P12_COMP(1, 0, cwA, scA); P12_ISSUE(c, 2, 0, cwA, scA); P12_BAR(); P12_COMP(1, 1, cwB, scB);
;           P12_XQ(c, 2); P12_ISSUE(c, 2, 1, cwB, scB); P12_BAR(); P12_COMP(2, 0, cwA, scA); P12_ISSUE(c, 3, 0, cwA, scA); P12_BAR(); P12_COMP(2, 1, cwB, scB);
;           P12_XQ(c, 3); P12_ISSUE(c, 3, 1, cwB, scB); P12_BAR(); P12_COMP(3, 0, cwA, scA); P12_ISSUE(cn, 0, 0, cwA, scA); P12_BAR(); P12_COMP(3, 1, cwB, scB);
;       } }
	v_and_b32_e32 v40, 0xf0f0f0f, v80
	v_mov_b32_e32 v42, 0
	v_dot4c_i32_i8_e32 v42, v40, v4
	v_lshrrev_b32_e32 v40, 4, v80
	v_and_b32_e32 v40, 0xf0f0f0f, v40
	v_dot4c_i32_i8_e32 v42, v40, v5
	v_and_b32_e32 v40, 0xf0f0f0f, v81
	v_mov_b32_e32 v43, 0
	v_dot4c_i32_i8_e32 v43, v40, v6
	v_lshrrev_b32_e32 v40, 4, v81
	v_and_b32_e32 v40, 0xf0f0f0f, v40
	v_dot4c_i32_i8_e32 v43, v40, v7
	v_and_b32_e32 v40, 0xf0f0f0f, v82
	v_dot4c_i32_i8_e32 v42, v40, v0
	v_lshrrev_b32_e32 v40, 4, v82
	v_and_b32_e32 v40, 0xf0f0f0f, v40
	v_dot4c_i32_i8_e32 v42, v40, v1
	v_and_b32_e32 v40, 0xf0f0f0f, v83
	v_dot4c_i32_i8_e32 v43, v40, v2
	v_lshrrev_b32_e32 v40, 4, v83
	v_and_b32_e32 v40, 0xf0f0f0f, v40
	v_dot4c_i32_i8_e32 v43, v40, v3
	s_waitcnt vmcnt(30)
	v_and_b32_e32 v40, 0xf0f0f0f, v68
	v_mov_b32_e32 v48, 0
	v_dot4c_i32_i8_e32 v48, v40, v4
	v_lshrrev_b32_e32 v40, 4, v68
	v_and_b32_e32 v40, 0xf0f0f0f, v40
	v_dot4c_i32_i8_e32 v48, v40, v5
	v_and_b32_e32 v40, 0xf0f0f0f, v69
	v_mov_b32_e32 v49, 0
	v_dot4c_i32_i8_e32 v49, v40, v6
	v_lshrrev_b32_e32 v40, 4, v69
	v_and_b32_e32 v40, 0xf0f0f0f, v40
	v_dot4c_i32_i8_e32 v49, v40, v7
	v_and_b32_e32 v40, 0xf0f0f0f, v70
	v_dot4c_i32_i8_e32 v48, v40, v0
	v_lshrrev_b32_e32 v40, 4, v70
	v_and_b32_e32 v40, 0xf0f0f0f, v40
	v_dot4c_i32_i8_e32 v48, v40, v1
	v_and_b32_e32 v40, 0xf0f0f0f, v71
	v_dot4c_i32_i8_e32 v49, v40, v2
	v_lshrrev_b32_e32 v40, 4, v71
	v_and_b32_e32 v40, 0xf0f0f0f, v40
	v_dot4c_i32_i8_e32 v49, v40, v3
	v_add_u32_e32 v42, v42, v43
	v_sub_u32_e32 v42, v42, v84
	s_waitcnt vmcnt(22)
	v_lshlrev_b32_e32 v41, 16, v181
	v_sub_u32_e32 v43, v49, v84
	v_add_u32_e32 v48, v43, v48
	v_cvt_f32_i32_e32 v43, v42
	v_cvt_f32_i32_e32 v42, v48
	v_lshlrev_b32_e32 v40, 16, v180
	v_pk_fma_f32 v[134:135], v[40:41], v[42:43], v[134:135]
	v_and_b32_e32 v40, 0xf0f0f0f, v52
	v_mov_b32_e32 v41, 0
	v_dot4c_i32_i8_e32 v41, v40, v4
	v_lshrrev_b32_e32 v40, 4, v52
	v_and_b32_e32 v40, 0xf0f0f0f, v40
	v_dot4c_i32_i8_e32 v41, v40, v5
	v_and_b32_e32 v40, 0xf0f0f0f, v53
	v_mov_b32_e32 v42, 0
	v_dot4c_i32_i8_e32 v42, v40, v6
	v_lshrrev_b32_e32 v40, 4, v53
	v_and_b32_e32 v40, 0xf0f0f0f, v40
	v_dot4c_i32_i8_e32 v42, v40, v7
	v_and_b32_e32 v40, 0xf0f0f0f, v54
	v_dot4c_i32_i8_e32 v41, v40, v0
	v_lshrrev_b32_e32 v40, 4, v54
	v_and_b32_e32 v40, 0xf0f0f0f, v40
	v_dot4c_i32_i8_e32 v41, v40, v1
	v_and_b32_e32 v40, 0xf0f0f0f, v55
	v_dot4c_i32_i8_e32 v42, v40, v2
	v_lshrrev_b32_e32 v40, 4, v55
	v_and_b32_e32 v40, 0xf0f0f0f, v40
	v_dot4c_i32_i8_e32 v42, v40, v3
	v_and_b32_e32 v40, 0xf0f0f0f, v36
	v_mov_b32_e32 v43, 0
	v_lshrrev_b32_e32 v36, 4, v36
	v_dot4c_i32_i8_e32 v43, v40, v4
	v_and_b32_e32 v36, 0xf0f0f0f, v36
	v_dot4c_i32_i8_e32 v43, v36, v5
	v_and_b32_e32 v36, 0xf0f0f0f, v37
	v_mov_b32_e32 v40, 0
	v_dot4c_i32_i8_e32 v40, v36, v6
	v_lshrrev_b32_e32 v36, 4, v37
	v_and_b32_e32 v36, 0xf0f0f0f, v36
	v_dot4c_i32_i8_e32 v40, v36, v7
	v_and_b32_e32 v36, 0xf0f0f0f, v38
	v_dot4c_i32_i8_e32 v43, v36, v0
	v_lshrrev_b32_e32 v36, 4, v38
	v_and_b32_e32 v36, 0xf0f0f0f, v36
	v_dot4c_i32_i8_e32 v43, v36, v1
	v_and_b32_e32 v36, 0xf0f0f0f, v39
	v_dot4c_i32_i8_e32 v40, v36, v2
	v_lshrrev_b32_e32 v36, 4, v39
	v_and_b32_e32 v36, 0xf0f0f0f, v36
	v_dot4c_i32_i8_e32 v40, v36, v3
	v_sub_u32_e32 v38, v42, v84
	v_add_u32_e32 v38, v38, v41
	s_waitcnt vmcnt(20)
	v_lshlrev_b32_e32 v37, 16, v173
	v_sub_u32_e32 v39, v40, v84
	v_add_u32_e32 v40, v39, v43
	v_cvt_f32_i32_e32 v39, v38
	v_cvt_f32_i32_e32 v38, v40
	v_lshlrev_b32_e32 v36, 16, v172
	v_pk_fma_f32 v[132:133], v[36:37], v[38:39], v[132:133]
	v_and_b32_e32 v36, 0xf0f0f0f, v32
	v_mov_b32_e32 v37, 0
	v_lshrrev_b32_e32 v32, 4, v32
	v_dot4c_i32_i8_e32 v37, v36, v4
	v_and_b32_e32 v32, 0xf0f0f0f, v32
	v_dot4c_i32_i8_e32 v37, v32, v5
	v_and_b32_e32 v32, 0xf0f0f0f, v33
	v_mov_b32_e32 v36, 0
	v_dot4c_i32_i8_e32 v36, v32, v6
	v_lshrrev_b32_e32 v32, 4, v33
	v_and_b32_e32 v32, 0xf0f0f0f, v32
	v_dot4c_i32_i8_e32 v36, v32, v7
	v_and_b32_e32 v32, 0xf0f0f0f, v34
	v_dot4c_i32_i8_e32 v37, v32, v0
	v_lshrrev_b32_e32 v32, 4, v34
	v_and_b32_e32 v32, 0xf0f0f0f, v32
	v_dot4c_i32_i8_e32 v37, v32, v1
	v_and_b32_e32 v32, 0xf0f0f0f, v35
	v_dot4c_i32_i8_e32 v36, v32, v2
	v_lshrrev_b32_e32 v32, 4, v35
	v_and_b32_e32 v32, 0xf0f0f0f, v32
	v_dot4c_i32_i8_e32 v36, v32, v3
	v_and_b32_e32 v32, 0xf0f0f0f, v28
	v_mov_b32_e32 v33, 0
	v_lshrrev_b32_e32 v28, 4, v28
	v_dot4c_i32_i8_e32 v33, v32, v4
	v_and_b32_e32 v28, 0xf0f0f0f, v28
	v_dot4c_i32_i8_e32 v33, v28, v5
	v_and_b32_e32 v28, 0xf0f0f0f, v29
	v_mov_b32_e32 v32, 0
	v_dot4c_i32_i8_e32 v32, v28, v6
	v_lshrrev_b32_e32 v28, 4, v29
	v_and_b32_e32 v28, 0xf0f0f0f, v28
	v_dot4c_i32_i8_e32 v32, v28, v7
	v_and_b32_e32 v28, 0xf0f0f0f, v30
	v_dot4c_i32_i8_e32 v33, v28, v0
	v_lshrrev_b32_e32 v28, 4, v30
	v_and_b32_e32 v28, 0xf0f0f0f, v28
	v_dot4c_i32_i8_e32 v33, v28, v1
	v_and_b32_e32 v28, 0xf0f0f0f, v31
	v_dot4c_i32_i8_e32 v32, v28, v2
	v_lshrrev_b32_e32 v28, 4, v31
	v_and_b32_e32 v28, 0xf0f0f0f, v28
	v_dot4c_i32_i8_e32 v32, v28, v3
	v_sub_u32_e32 v30, v36, v84
	v_add_u32_e32 v30, v30, v37
	s_waitcnt vmcnt(18)
; #define P12_ISSUE(c_, i_, h_, CW_, SC_) do { _Pragma("unroll") for (int bb = 0; bb < 8; ++bb) { const unsigned ro = (unsigned)(c_) * 16384u + (unsigned)EL[(i_) * 128 + ((h_) * 8 + bb) * 8 + g8]; \
;         CW_[bb] = *(const v4u*)(U4 + (size_t)(ro * 128u + 16u * (unsigned)k8)); SC_[bb] = USS[(size_t)(ro * 8u + (unsigned)k8)]; } } while (0)
; #define P12_COMP(i_, h_, CW_, SC_) do { _Pragma("unroll") for (int bb = 0; bb < 8; ++bb) { int a0 = 0, a1 = 0; P12_U4(CW_[bb].x, xa.x, xa.y, a0); P12_U4(CW_[bb].y, xa.z, xa.w, a1); P12_U4(CW_[bb].z, xb.x, xb.y, a0); P12_U4(CW_[bb].w, xb.z, xb.w, a1); \
;         psum[(i_)][(h_) * 8 + bb] += __uint_as_float(SC_[bb] << 16) * (float)((a0 + a1) - xo); } } while (0)
; #define P12_BAR() asm volatile("" ::: "memory")
; __device__ __forceinline__ void p12_peer(Frame& F) {
;     ...
;     { v4u cwA[8], cwB[8]; unsigned scA[8], scB[8]; v4u xa, xb; int xo;
;       P12_ISSUE(0, 0, 0, cwA, scA);
; _Pragma("nounroll")
;       for (int c = 0; c < 16; ++c) { const int cn = c + 1 < 16 ? c + 1 : 15;
;           P12_XQ(c, 0); P12_ISSUE(c, 0, 1, cwB, scB); P12_BAR(); P12_COMP(0, 0, cwA, scA); P12_ISSUE(c, 1, 0, cwA, scA); P12_BAR(); P12_COMP(0, 1, cwB, scB);
;           P12_XQ(c, 1); P12_ISSUE(c, 1, 1, cwB, scB); P12_BAR(); P12_COMP(1, 0, cwA, scA); P12_ISSUE(c, 2, 0, cwA, scA); P12_BAR(); P12_COMP(1, 1, cwB, scB);
;           P12_XQ(c, 2); P12_ISSUE(c, 2, 1, cwB, scB); P12_BAR(); P12_COMP(2, 0, cwA, scA); P12_ISSUE(c, 3, 0, cwA, scA); P12_BAR(); P12_COMP(2, 1, cwB, scB);
;           P12_XQ(c, 3); P12_ISSUE(c, 3, 1, cwB, scB); P12_BAR(); P12_COMP(3, 0, cwA, scA); P12_ISSUE(cn, 0, 0, cwA, scA); P12_BAR(); P12_COMP(3, 1, cwB, scB);
;       } }
	v_lshlrev_b32_e32 v29, 16, v171
	v_sub_u32_e32 v31, v32, v84
	v_add_u32_e32 v32, v31, v33
	v_cvt_f32_i32_e32 v31, v30
	v_cvt_f32_i32_e32 v30, v32
	v_lshlrev_b32_e32 v28, 16, v87
	v_pk_fma_f32 v[130:131], v[28:29], v[30:31], v[130:131]
	v_and_b32_e32 v28, 0xf0f0f0f, v20
	v_mov_b32_e32 v29, 0
	v_lshrrev_b32_e32 v20, 4, v20
	v_dot4c_i32_i8_e32 v29, v28, v4
	v_and_b32_e32 v20, 0xf0f0f0f, v20
	v_dot4c_i32_i8_e32 v29, v20, v5
	v_and_b32_e32 v20, 0xf0f0f0f, v21
	v_mov_b32_e32 v28, 0
	v_dot4c_i32_i8_e32 v28, v20, v6
	v_lshrrev_b32_e32 v20, 4, v21
	v_and_b32_e32 v20, 0xf0f0f0f, v20
	v_dot4c_i32_i8_e32 v28, v20, v7
	v_and_b32_e32 v20, 0xf0f0f0f, v22
	v_dot4c_i32_i8_e32 v29, v20, v0
	v_lshrrev_b32_e32 v20, 4, v22
	v_and_b32_e32 v20, 0xf0f0f0f, v20
	v_dot4c_i32_i8_e32 v29, v20, v1
	v_and_b32_e32 v20, 0xf0f0f0f, v23
	v_dot4c_i32_i8_e32 v28, v20, v2
	v_lshrrev_b32_e32 v20, 4, v23
	v_and_b32_e32 v20, 0xf0f0f0f, v20
	v_dot4c_i32_i8_e32 v28, v20, v3
	v_and_b32_e32 v20, 0xf0f0f0f, v16
	v_mov_b32_e32 v21, 0
	v_dot4c_i32_i8_e32 v21, v20, v4
	v_lshrrev_b32_e32 v4, 4, v16
	v_and_b32_e32 v4, 0xf0f0f0f, v4
	v_dot4c_i32_i8_e32 v21, v4, v5
	v_and_b32_e32 v4, 0xf0f0f0f, v17
	v_mov_b32_e32 v5, 0
	v_dot4c_i32_i8_e32 v5, v4, v6
	v_lshrrev_b32_e32 v4, 4, v17
	v_and_b32_e32 v4, 0xf0f0f0f, v4
	v_dot4c_i32_i8_e32 v5, v4, v7
	v_and_b32_e32 v4, 0xf0f0f0f, v18
	v_dot4c_i32_i8_e32 v21, v4, v0
	v_lshrrev_b32_e32 v0, 4, v18
	v_and_b32_e32 v0, 0xf0f0f0f, v0
	v_dot4c_i32_i8_e32 v21, v0, v1
	v_and_b32_e32 v0, 0xf0f0f0f, v19
	v_dot4c_i32_i8_e32 v5, v0, v2
	v_lshrrev_b32_e32 v0, 4, v19
	v_and_b32_e32 v0, 0xf0f0f0f, v0
	v_dot4c_i32_i8_e32 v5, v0, v3
	v_sub_u32_e32 v2, v28, v84
	v_add_u32_e32 v2, v2, v29
	s_waitcnt vmcnt(16)
	v_lshlrev_b32_e32 v1, 16, v86
	v_sub_u32_e32 v3, v5, v84
	v_add_u32_e32 v4, v3, v21
	v_cvt_f32_i32_e32 v3, v2
	v_cvt_f32_i32_e32 v2, v4
	v_lshlrev_b32_e32 v0, 16, v85
	ds_read_b128 v[32:35], v166 offset:8192
	ds_read_b128 v[28:31], v166 offset:8208
	v_pk_fma_f32 v[128:129], v[0:1], v[2:3], v[128:129]
	ds_read_u16 v1, v93 offset:17024
	ds_read_u16 v2, v93 offset:17040
	ds_read_u16 v3, v93 offset:17056
	ds_read_u16 v4, v93 offset:17072
	v_mov_b32_e32 v0, 0
	s_waitcnt lgkmcnt(3)
	v_add_u32_e32 v1, s44, v1
	v_lshl_or_b32 v5, v1, 7, v165
	s_waitcnt lgkmcnt(2)
	v_add_u32_e32 v2, s44, v2
	global_load_dwordx4 v[84:87], v5, s[0:1]
	v_lshl_or_b32 v5, v2, 7, v165
	s_waitcnt lgkmcnt(1)
	v_add_u32_e32 v3, s44, v3
	global_load_dwordx4 v[80:83], v5, s[0:1]
	v_lshl_or_b32 v5, v3, 7, v165
	s_waitcnt lgkmcnt(0)
	v_add_u32_e32 v4, s44, v4
	global_load_dwordx4 v[68:71], v5, s[0:1]
	v_lshl_or_b32 v5, v4, 7, v165
	global_load_dwordx4 v[64:67], v5, s[0:1]
	ds_read_u16 v5, v93 offset:17088
	v_dot4c_i32_i8_e32 v0, 0x1010101, v32
	v_dot4c_i32_i8_e32 v0, 0x1010101, v33
	v_dot4c_i32_i8_e32 v0, 0x1010101, v34
	v_dot4c_i32_i8_e32 v0, 0x1010101, v35
	s_waitcnt lgkmcnt(0)
	v_add_u32_e32 v5, s44, v5
	v_lshl_or_b32 v6, v5, 7, v165
	global_load_dwordx4 v[52:55], v6, s[0:1]
	ds_read_u16 v6, v93 offset:17104
	v_dot4c_i32_i8_e32 v0, 0x1010101, v28
	v_dot4c_i32_i8_e32 v0, 0x1010101, v29
	v_dot4c_i32_i8_e32 v0, 0x1010101, v30
	v_dot4c_i32_i8_e32 v0, 0x1010101, v31
	s_waitcnt lgkmcnt(0)
	v_add_u32_e32 v6, s44, v6
	v_lshl_or_b32 v7, v6, 7, v165
	global_load_dwordx4 v[48:51], v7, s[0:1]
	ds_read_u16 v7, v93 offset:17120
	v_lshl_or_b32 v2, v2, 4, v95
	v_lshl_or_b32 v1, v1, 4, v95
	v_lshl_or_b32 v3, v3, 4, v95
	v_lshl_or_b32 v4, v4, 4, v95
	s_waitcnt lgkmcnt(0)
	v_add_u32_e32 v7, s44, v7
	v_lshl_or_b32 v16, v7, 7, v165
	global_load_dwordx4 v[40:43], v16, s[0:1]
	ds_read_u16 v16, v93 offset:17136
	v_lshl_or_b32 v5, v5, 4, v95
	v_lshl_or_b32 v6, v6, 4, v95
	v_lshl_or_b32 v7, v7, 4, v95
	v_lshlrev_b32_e32 v169, 3, v0
	s_waitcnt lgkmcnt(0)
	v_add_u32_e32 v16, s44, v16
	v_lshl_or_b32 v17, v16, 7, v165
	global_load_dwordx4 v[36:39], v17, s[0:1]
	v_lshl_or_b32 v16, v16, 4, v95
	global_load_ushort v178, v2, s[18:19]
	global_load_ushort v179, v1, s[18:19]
	global_load_ushort v174, v4, s[18:19]
	global_load_ushort v175, v3, s[18:19]
	global_load_ushort v172, v6, s[18:19]
	global_load_ushort v173, v5, s[18:19]
	global_load_ushort v170, v16, s[18:19]
	global_load_ushort v171, v7, s[18:19]
	s_waitcnt vmcnt(31)
	v_and_b32_e32 v0, 0xf0f0f0f, v76
	v_mov_b32_e32 v2, 0
	v_dot4c_i32_i8_e32 v2, v0, v32
	v_lshrrev_b32_e32 v0, 4, v76
	v_and_b32_e32 v0, 0xf0f0f0f, v0
	v_dot4c_i32_i8_e32 v2, v0, v33
	v_and_b32_e32 v0, 0xf0f0f0f, v77
	v_mov_b32_e32 v3, 0
	v_dot4c_i32_i8_e32 v3, v0, v34
	v_lshrrev_b32_e32 v0, 4, v77
	v_and_b32_e32 v0, 0xf0f0f0f, v0
	v_dot4c_i32_i8_e32 v3, v0, v35
	v_and_b32_e32 v0, 0xf0f0f0f, v78
	v_dot4c_i32_i8_e32 v2, v0, v28
	v_lshrrev_b32_e32 v0, 4, v78
	v_and_b32_e32 v0, 0xf0f0f0f, v0
	v_dot4c_i32_i8_e32 v2, v0, v29
	v_and_b32_e32 v0, 0xf0f0f0f, v79
	v_dot4c_i32_i8_e32 v3, v0, v30
	v_lshrrev_b32_e32 v0, 4, v79
	v_and_b32_e32 v0, 0xf0f0f0f, v0
	v_dot4c_i32_i8_e32 v3, v0, v31
	s_waitcnt vmcnt(30)
	v_and_b32_e32 v0, 0xf0f0f0f, v72
	v_mov_b32_e32 v4, 0
	v_dot4c_i32_i8_e32 v4, v0, v32
	v_lshrrev_b32_e32 v0, 4, v72
	v_and_b32_e32 v0, 0xf0f0f0f, v0
	v_dot4c_i32_i8_e32 v4, v0, v33
	v_and_b32_e32 v0, 0xf0f0f0f, v73
	v_mov_b32_e32 v5, 0
	v_dot4c_i32_i8_e32 v5, v0, v34
	v_lshrrev_b32_e32 v0, 4, v73
	v_and_b32_e32 v0, 0xf0f0f0f, v0
	v_dot4c_i32_i8_e32 v5, v0, v35
	v_and_b32_e32 v0, 0xf0f0f0f, v74
	v_dot4c_i32_i8_e32 v4, v0, v28
	v_lshrrev_b32_e32 v0, 4, v74
	v_and_b32_e32 v0, 0xf0f0f0f, v0
	v_dot4c_i32_i8_e32 v4, v0, v29
	v_and_b32_e32 v0, 0xf0f0f0f, v75
	v_dot4c_i32_i8_e32 v5, v0, v30
	v_lshrrev_b32_e32 v0, 4, v75
	v_and_b32_e32 v0, 0xf0f0f0f, v0
	v_dot4c_i32_i8_e32 v5, v0, v31
	v_add_u32_e32 v2, v2, v3
	v_sub_u32_e32 v2, v2, v169
	s_waitcnt vmcnt(22)
; #define P12_ISSUE(c_, i_, h_, CW_, SC_) do { _Pragma("unroll") for (int bb = 0; bb < 8; ++bb) { const unsigned ro = (unsigned)(c_) * 16384u + (unsigned)EL[(i_) * 128 + ((h_) * 8 + bb) * 8 + g8]; \
;         CW_[bb] = *(const v4u*)(U4 + (size_t)(ro * 128u + 16u * (unsigned)k8)); SC_[bb] = USS[(size_t)(ro * 8u + (unsigned)k8)]; } } while (0)
; #define P12_COMP(i_, h_, CW_, SC_) do { _Pragma("unroll") for (int bb = 0; bb < 8; ++bb) { int a0 = 0, a1 = 0; P12_U4(CW_[bb].x, xa.x, xa.y, a0); P12_U4(CW_[bb].y, xa.z, xa.w, a1); P12_U4(CW_[bb].z, xb.x, xb.y, a0); P12_U4(CW_[bb].w, xb.z, xb.w, a1); \
;         psum[(i_)][(h_) * 8 + bb] += __uint_as_float(SC_[bb] << 16) * (float)((a0 + a1) - xo); } } while (0)
; #define P12_BAR() asm volatile("" ::: "memory")
; __device__ __forceinline__ void p12_peer(Frame& F) {
;     ...
;     { v4u cwA[8], cwB[8]; unsigned scA[8], scB[8]; v4u xa, xb; int xo;
;       P12_ISSUE(0, 0, 0, cwA, scA);
; _Pragma("nounroll")
;       for (int c = 0; c < 16; ++c) { const int cn = c + 1 < 16 ? c + 1 : 15;
;           P12_XQ(c, 0); P12_ISSUE(c, 0, 1, cwB, scB); P12_BAR(); P12_COMP(0, 0, cwA, scA); P12_ISSUE(c, 1, 0, cwA, scA); P12_BAR(); P12_COMP(0, 1, cwB, scB);
;           P12_XQ(c, 1); P12_ISSUE(c, 1, 1, cwB, scB); P12_BAR(); P12_COMP(1, 0, cwA, scA); P12_ISSUE(c, 2, 0, cwA, scA); P12_BAR(); P12_COMP(1, 1, cwB, scB);
;           P12_XQ(c, 2); P12_ISSUE(c, 2, 1, cwB, scB); P12_BAR(); P12_COMP(2, 0, cwA, scA); P12_ISSUE(c, 3, 0, cwA, scA); P12_BAR(); P12_COMP(2, 1, cwB, scB);
;           P12_XQ(c, 3); P12_ISSUE(c, 3, 1, cwB, scB); P12_BAR(); P12_COMP(3, 0, cwA, scA); P12_ISSUE(cn, 0, 0, cwA, scA); P12_BAR(); P12_COMP(3, 1, cwB, scB);
;       } }
	v_lshlrev_b32_e32 v1, 16, v177
	v_add_u32_e32 v3, v4, v5
	v_sub_u32_e32 v4, v3, v169
	v_cvt_f32_i32_e32 v3, v2
	v_cvt_f32_i32_e32 v2, v4
	v_lshlrev_b32_e32 v0, 16, v176
	v_mov_b32_e32 v4, 0
	v_mov_b32_e32 v5, 0
	v_pk_fma_f32 v[126:127], v[0:1], v[2:3], v[126:127]
	v_and_b32_e32 v0, 0xf0f0f0f, v60
	v_mov_b32_e32 v2, 0
	v_dot4c_i32_i8_e32 v2, v0, v32
	v_lshrrev_b32_e32 v0, 4, v60
	v_and_b32_e32 v0, 0xf0f0f0f, v0
	v_dot4c_i32_i8_e32 v2, v0, v33
	v_and_b32_e32 v0, 0xf0f0f0f, v61
	v_mov_b32_e32 v3, 0
	v_dot4c_i32_i8_e32 v3, v0, v34
	v_lshrrev_b32_e32 v0, 4, v61
	v_and_b32_e32 v0, 0xf0f0f0f, v0
	v_dot4c_i32_i8_e32 v3, v0, v35
	v_and_b32_e32 v0, 0xf0f0f0f, v62
	v_dot4c_i32_i8_e32 v2, v0, v28
	v_lshrrev_b32_e32 v0, 4, v62
	v_and_b32_e32 v0, 0xf0f0f0f, v0
	v_dot4c_i32_i8_e32 v2, v0, v29
	v_and_b32_e32 v0, 0xf0f0f0f, v63
	v_dot4c_i32_i8_e32 v3, v0, v30
	v_lshrrev_b32_e32 v0, 4, v63
	v_and_b32_e32 v0, 0xf0f0f0f, v0
	v_dot4c_i32_i8_e32 v3, v0, v31
	v_and_b32_e32 v0, 0xf0f0f0f, v56
	v_dot4c_i32_i8_e32 v4, v0, v32
	v_lshrrev_b32_e32 v0, 4, v56
	v_and_b32_e32 v0, 0xf0f0f0f, v0
	v_dot4c_i32_i8_e32 v4, v0, v33
	v_and_b32_e32 v0, 0xf0f0f0f, v57
	v_dot4c_i32_i8_e32 v5, v0, v34
	v_lshrrev_b32_e32 v0, 4, v57
	v_and_b32_e32 v0, 0xf0f0f0f, v0
	v_dot4c_i32_i8_e32 v5, v0, v35
	v_and_b32_e32 v0, 0xf0f0f0f, v58
	v_dot4c_i32_i8_e32 v4, v0, v28
	v_lshrrev_b32_e32 v0, 4, v58
	v_and_b32_e32 v0, 0xf0f0f0f, v0
	v_dot4c_i32_i8_e32 v4, v0, v29
	v_and_b32_e32 v0, 0xf0f0f0f, v59
	v_dot4c_i32_i8_e32 v5, v0, v30
	v_lshrrev_b32_e32 v0, 4, v59
	v_and_b32_e32 v0, 0xf0f0f0f, v0
	v_dot4c_i32_i8_e32 v5, v0, v31
	v_add_u32_e32 v2, v2, v3
	v_sub_u32_e32 v2, v2, v169
	s_waitcnt vmcnt(20)
	v_lshlrev_b32_e32 v1, 16, v168
	v_add_u32_e32 v3, v4, v5
	v_sub_u32_e32 v4, v3, v169
	v_cvt_f32_i32_e32 v3, v2
	v_cvt_f32_i32_e32 v2, v4
	v_lshlrev_b32_e32 v0, 16, v167
	v_mov_b32_e32 v4, 0
	v_mov_b32_e32 v5, 0
	v_pk_fma_f32 v[124:125], v[0:1], v[2:3], v[124:125]
	v_and_b32_e32 v0, 0xf0f0f0f, v44
	v_mov_b32_e32 v2, 0
	v_dot4c_i32_i8_e32 v2, v0, v32
	v_lshrrev_b32_e32 v0, 4, v44
	v_and_b32_e32 v0, 0xf0f0f0f, v0
	v_dot4c_i32_i8_e32 v2, v0, v33
	v_and_b32_e32 v0, 0xf0f0f0f, v45
	v_mov_b32_e32 v3, 0
	v_dot4c_i32_i8_e32 v3, v0, v34
	v_lshrrev_b32_e32 v0, 4, v45
	v_and_b32_e32 v0, 0xf0f0f0f, v0
	v_dot4c_i32_i8_e32 v3, v0, v35
	v_and_b32_e32 v0, 0xf0f0f0f, v46
	v_dot4c_i32_i8_e32 v2, v0, v28
	v_lshrrev_b32_e32 v0, 4, v46
	v_and_b32_e32 v0, 0xf0f0f0f, v0
	v_dot4c_i32_i8_e32 v2, v0, v29
	v_and_b32_e32 v0, 0xf0f0f0f, v47
	v_dot4c_i32_i8_e32 v3, v0, v30
	v_lshrrev_b32_e32 v0, 4, v47
	v_and_b32_e32 v0, 0xf0f0f0f, v0
	v_dot4c_i32_i8_e32 v3, v0, v31
	v_and_b32_e32 v0, 0xf0f0f0f, v24
	v_dot4c_i32_i8_e32 v4, v0, v32
	v_lshrrev_b32_e32 v0, 4, v24
	v_and_b32_e32 v0, 0xf0f0f0f, v0
	v_dot4c_i32_i8_e32 v4, v0, v33
	v_and_b32_e32 v0, 0xf0f0f0f, v25
	v_dot4c_i32_i8_e32 v5, v0, v34
	v_lshrrev_b32_e32 v0, 4, v25
	v_and_b32_e32 v0, 0xf0f0f0f, v0
	v_dot4c_i32_i8_e32 v5, v0, v35
	v_and_b32_e32 v0, 0xf0f0f0f, v26
	v_dot4c_i32_i8_e32 v4, v0, v28
	v_lshrrev_b32_e32 v0, 4, v26
	v_and_b32_e32 v0, 0xf0f0f0f, v0
	v_dot4c_i32_i8_e32 v4, v0, v29
	v_and_b32_e32 v0, 0xf0f0f0f, v27
	v_dot4c_i32_i8_e32 v5, v0, v30
	v_lshrrev_b32_e32 v0, 4, v27
	v_and_b32_e32 v0, 0xf0f0f0f, v0
	v_dot4c_i32_i8_e32 v5, v0, v31
	v_add_u32_e32 v2, v2, v3
	v_sub_u32_e32 v2, v2, v169
	s_waitcnt vmcnt(18)
	v_lshlrev_b32_e32 v1, 16, v91
	v_add_u32_e32 v3, v4, v5
	v_sub_u32_e32 v4, v3, v169
	v_cvt_f32_i32_e32 v3, v2
	v_cvt_f32_i32_e32 v2, v4
	v_lshlrev_b32_e32 v0, 16, v90
	v_mov_b32_e32 v4, 0
	v_mov_b32_e32 v5, 0
	v_pk_fma_f32 v[122:123], v[0:1], v[2:3], v[122:123]
	v_and_b32_e32 v0, 0xf0f0f0f, v12
	v_mov_b32_e32 v2, 0
	v_dot4c_i32_i8_e32 v2, v0, v32
	v_lshrrev_b32_e32 v0, 4, v12
	v_and_b32_e32 v0, 0xf0f0f0f, v0
	v_dot4c_i32_i8_e32 v2, v0, v33
	v_and_b32_e32 v0, 0xf0f0f0f, v13
	v_mov_b32_e32 v3, 0
	v_dot4c_i32_i8_e32 v3, v0, v34
	v_lshrrev_b32_e32 v0, 4, v13
	v_and_b32_e32 v0, 0xf0f0f0f, v0
	v_dot4c_i32_i8_e32 v3, v0, v35
	v_and_b32_e32 v0, 0xf0f0f0f, v14
	v_dot4c_i32_i8_e32 v2, v0, v28
	v_lshrrev_b32_e32 v0, 4, v14
	v_and_b32_e32 v0, 0xf0f0f0f, v0
	v_dot4c_i32_i8_e32 v2, v0, v29
	v_and_b32_e32 v0, 0xf0f0f0f, v15
	v_dot4c_i32_i8_e32 v3, v0, v30
	v_lshrrev_b32_e32 v0, 4, v15
	v_and_b32_e32 v0, 0xf0f0f0f, v0
	v_dot4c_i32_i8_e32 v3, v0, v31
	v_and_b32_e32 v0, 0xf0f0f0f, v8
	v_dot4c_i32_i8_e32 v4, v0, v32
	v_lshrrev_b32_e32 v0, 4, v8
	v_and_b32_e32 v0, 0xf0f0f0f, v0
	v_dot4c_i32_i8_e32 v4, v0, v33
	v_and_b32_e32 v0, 0xf0f0f0f, v9
	v_dot4c_i32_i8_e32 v5, v0, v34
	v_lshrrev_b32_e32 v0, 4, v9
	v_and_b32_e32 v0, 0xf0f0f0f, v0
	v_dot4c_i32_i8_e32 v5, v0, v35
	v_and_b32_e32 v0, 0xf0f0f0f, v10
	v_dot4c_i32_i8_e32 v4, v0, v28
	v_lshrrev_b32_e32 v0, 4, v10
	v_and_b32_e32 v0, 0xf0f0f0f, v0
	v_dot4c_i32_i8_e32 v4, v0, v29
	v_and_b32_e32 v0, 0xf0f0f0f, v11
	v_dot4c_i32_i8_e32 v5, v0, v30
	v_lshrrev_b32_e32 v0, 4, v11
	v_and_b32_e32 v0, 0xf0f0f0f, v0
	v_dot4c_i32_i8_e32 v5, v0, v31
	v_add_u32_e32 v2, v2, v3
	v_sub_u32_e32 v2, v2, v169
	s_waitcnt vmcnt(16)
	v_lshlrev_b32_e32 v1, 16, v89
	v_add_u32_e32 v3, v4, v5
	v_sub_u32_e32 v4, v3, v169
	v_cvt_f32_i32_e32 v3, v2
	v_cvt_f32_i32_e32 v2, v4
	v_lshlrev_b32_e32 v0, 16, v88
	v_pk_fma_f32 v[120:121], v[0:1], v[2:3], v[120:121]
	ds_read_u16 v0, v93 offset:17152
	ds_read_u16 v1, v93 offset:17168
	ds_read_u16 v2, v93 offset:17184
	ds_read_u16 v3, v93 offset:17200
	s_waitcnt lgkmcnt(3)
	v_add_u32_e32 v0, s44, v0
	v_lshl_or_b32 v4, v0, 7, v165
	v_lshl_or_b32 v44, v0, 4, v95
	s_waitcnt lgkmcnt(2)
	v_add_u32_e32 v0, s44, v1
	v_lshl_or_b32 v1, v0, 7, v165
	v_lshl_or_b32 v45, v0, 4, v95
	s_waitcnt lgkmcnt(1)
; #define P12_ISSUE(c_, i_, h_, CW_, SC_) do { _Pragma("unroll") for (int bb = 0; bb < 8; ++bb) { const unsigned ro = (unsigned)(c_) * 16384u + (unsigned)EL[(i_) * 128 + ((h_) * 8 + bb) * 8 + g8]; \
;         CW_[bb] = *(const v4u*)(U4 + (size_t)(ro * 128u + 16u * (unsigned)k8)); SC_[bb] = USS[(size_t)(ro * 8u + (unsigned)k8)]; } } while (0)
; #define P12_COMP(i_, h_, CW_, SC_) do { _Pragma("unroll") for (int bb = 0; bb < 8; ++bb) { int a0 = 0, a1 = 0; P12_U4(CW_[bb].x, xa.x, xa.y, a0); P12_U4(CW_[bb].y, xa.z, xa.w, a1); P12_U4(CW_[bb].z, xb.x, xb.y, a0); P12_U4(CW_[bb].w, xb.z, xb.w, a1); \
;         psum[(i_)][(h_) * 8 + bb] += __uint_as_float(SC_[bb] << 16) * (float)((a0 + a1) - xo); } } while (0)
; #define P12_BAR() asm volatile("" ::: "memory")
; __device__ __forceinline__ void p12_peer(Frame& F) {
;     ...
;     { v4u cwA[8], cwB[8]; unsigned scA[8], scB[8]; v4u xa, xb; int xo;
;       P12_ISSUE(0, 0, 0, cwA, scA);
; _Pragma("nounroll")
;       for (int c = 0; c < 16; ++c) { const int cn = c + 1 < 16 ? c + 1 : 15;
;           P12_XQ(c, 0); P12_ISSUE(c, 0, 1, cwB, scB); P12_BAR(); P12_COMP(0, 0, cwA, scA); P12_ISSUE(c, 1, 0, cwA, scA); P12_BAR(); P12_COMP(0, 1, cwB, scB);
;           P12_XQ(c, 1); P12_ISSUE(c, 1, 1, cwB, scB); P12_BAR(); P12_COMP(1, 0, cwA, scA); P12_ISSUE(c, 2, 0, cwA, scA); P12_BAR(); P12_COMP(1, 1, cwB, scB);
;           P12_XQ(c, 2); P12_ISSUE(c, 2, 1, cwB, scB); P12_BAR(); P12_COMP(2, 0, cwA, scA); P12_ISSUE(c, 3, 0, cwA, scA); P12_BAR(); P12_COMP(2, 1, cwB, scB);
;           P12_XQ(c, 3); P12_ISSUE(c, 3, 1, cwB, scB); P12_BAR(); P12_COMP(3, 0, cwA, scA); P12_ISSUE(cn, 0, 0, cwA, scA); P12_BAR(); P12_COMP(3, 1, cwB, scB);
;       } }
	v_add_u32_e32 v0, s44, v2
	global_load_dwordx4 v[72:75], v4, s[0:1]
	global_load_dwordx4 v[24:27], v1, s[0:1]
	v_lshl_or_b32 v1, v0, 7, v165
	v_lshl_or_b32 v46, v0, 4, v95
	s_waitcnt lgkmcnt(0)
	v_add_u32_e32 v0, s44, v3
	global_load_dwordx4 v[20:23], v1, s[0:1]
	v_lshl_or_b32 v1, v0, 7, v165
	v_lshl_or_b32 v47, v0, 4, v95
	ds_read_u16 v0, v93 offset:17216
	global_load_dwordx4 v[16:19], v1, s[0:1]
	s_waitcnt lgkmcnt(0)
	v_add_u32_e32 v0, s44, v0
	v_lshl_or_b32 v1, v0, 7, v165
	v_lshl_or_b32 v56, v0, 4, v95
	ds_read_u16 v0, v93 offset:17232
	global_load_dwordx4 v[12:15], v1, s[0:1]
	s_waitcnt lgkmcnt(0)
	v_add_u32_e32 v0, s44, v0
	v_lshl_or_b32 v1, v0, 7, v165
	v_lshl_or_b32 v57, v0, 4, v95
	ds_read_u16 v0, v93 offset:17248
	global_load_dwordx4 v[8:11], v1, s[0:1]
	s_waitcnt lgkmcnt(0)
	v_add_u32_e32 v0, s44, v0
	v_lshl_or_b32 v1, v0, 7, v165
	v_lshl_or_b32 v58, v0, 4, v95
	ds_read_u16 v0, v93 offset:17264
	global_load_dwordx4 v[4:7], v1, s[0:1]
	s_waitcnt lgkmcnt(0)
	v_add_u32_e32 v59, s44, v0
	v_lshl_or_b32 v0, v59, 7, v165
	global_load_dwordx4 v[0:3], v0, s[0:1]
	v_lshl_or_b32 v59, v59, 4, v95
	global_load_ushort v167, v45, s[18:19]
	global_load_ushort v168, v44, s[18:19]
	global_load_ushort v90, v47, s[18:19]
	global_load_ushort v91, v46, s[18:19]
	global_load_ushort v88, v56, s[18:19]
	global_load_ushort v89, v57, s[18:19]
	global_load_ushort v76, v58, s[18:19]
	global_load_ushort v77, v59, s[18:19]
	s_waitcnt vmcnt(31)
	v_and_b32_e32 v44, 0xf0f0f0f, v84
	v_mov_b32_e32 v46, 0
	v_dot4c_i32_i8_e32 v46, v44, v32
	v_lshrrev_b32_e32 v44, 4, v84
	v_and_b32_e32 v44, 0xf0f0f0f, v44
	v_dot4c_i32_i8_e32 v46, v44, v33
	v_and_b32_e32 v44, 0xf0f0f0f, v85
	v_mov_b32_e32 v47, 0
	v_dot4c_i32_i8_e32 v47, v44, v34
	v_lshrrev_b32_e32 v44, 4, v85
	v_and_b32_e32 v44, 0xf0f0f0f, v44
	v_dot4c_i32_i8_e32 v47, v44, v35
	v_and_b32_e32 v44, 0xf0f0f0f, v86
	v_dot4c_i32_i8_e32 v46, v44, v28
	v_lshrrev_b32_e32 v44, 4, v86
	v_and_b32_e32 v44, 0xf0f0f0f, v44
	v_dot4c_i32_i8_e32 v46, v44, v29
	v_and_b32_e32 v44, 0xf0f0f0f, v87
	v_dot4c_i32_i8_e32 v47, v44, v30
	v_lshrrev_b32_e32 v44, 4, v87
	v_and_b32_e32 v44, 0xf0f0f0f, v44
	v_dot4c_i32_i8_e32 v47, v44, v31
	s_waitcnt vmcnt(30)
	v_and_b32_e32 v44, 0xf0f0f0f, v80
	v_mov_b32_e32 v56, 0
	v_dot4c_i32_i8_e32 v56, v44, v32
	v_lshrrev_b32_e32 v44, 4, v80
	v_and_b32_e32 v44, 0xf0f0f0f, v44
	v_dot4c_i32_i8_e32 v56, v44, v33
	v_and_b32_e32 v44, 0xf0f0f0f, v81
	v_mov_b32_e32 v57, 0
	v_dot4c_i32_i8_e32 v57, v44, v34
	v_lshrrev_b32_e32 v44, 4, v81
	v_and_b32_e32 v44, 0xf0f0f0f, v44
	v_dot4c_i32_i8_e32 v57, v44, v35
	v_and_b32_e32 v44, 0xf0f0f0f, v82
	v_dot4c_i32_i8_e32 v56, v44, v28
	v_lshrrev_b32_e32 v44, 4, v82
	v_and_b32_e32 v44, 0xf0f0f0f, v44
	v_dot4c_i32_i8_e32 v56, v44, v29
	v_and_b32_e32 v44, 0xf0f0f0f, v83
	v_dot4c_i32_i8_e32 v57, v44, v30
	v_lshrrev_b32_e32 v44, 4, v83
	v_and_b32_e32 v44, 0xf0f0f0f, v44
	v_dot4c_i32_i8_e32 v57, v44, v31
	v_add_u32_e32 v46, v46, v47
	v_sub_u32_e32 v46, v46, v169
	s_waitcnt vmcnt(22)
	v_lshlrev_b32_e32 v45, 16, v179
	v_sub_u32_e32 v47, v57, v169
	v_add_u32_e32 v56, v47, v56
	v_cvt_f32_i32_e32 v47, v46
	v_cvt_f32_i32_e32 v46, v56
	v_lshlrev_b32_e32 v44, 16, v178
	v_mov_b32_e32 v56, 0
	v_mov_b32_e32 v57, 0
	v_pk_fma_f32 v[118:119], v[44:45], v[46:47], v[118:119]
	v_and_b32_e32 v44, 0xf0f0f0f, v68
	v_mov_b32_e32 v46, 0
	v_dot4c_i32_i8_e32 v46, v44, v32
	v_lshrrev_b32_e32 v44, 4, v68
	v_and_b32_e32 v44, 0xf0f0f0f, v44
	v_dot4c_i32_i8_e32 v46, v44, v33
	v_and_b32_e32 v44, 0xf0f0f0f, v69
	v_mov_b32_e32 v47, 0
	v_dot4c_i32_i8_e32 v47, v44, v34
	v_lshrrev_b32_e32 v44, 4, v69
	v_and_b32_e32 v44, 0xf0f0f0f, v44
	v_dot4c_i32_i8_e32 v47, v44, v35
	v_and_b32_e32 v44, 0xf0f0f0f, v70
	v_dot4c_i32_i8_e32 v46, v44, v28
	v_lshrrev_b32_e32 v44, 4, v70
	v_and_b32_e32 v44, 0xf0f0f0f, v44
	v_dot4c_i32_i8_e32 v46, v44, v29
	v_and_b32_e32 v44, 0xf0f0f0f, v71
	v_dot4c_i32_i8_e32 v47, v44, v30
	v_lshrrev_b32_e32 v44, 4, v71
	v_and_b32_e32 v44, 0xf0f0f0f, v44
	v_dot4c_i32_i8_e32 v47, v44, v31
	v_and_b32_e32 v44, 0xf0f0f0f, v64
	v_dot4c_i32_i8_e32 v56, v44, v32
	v_lshrrev_b32_e32 v44, 4, v64
	v_and_b32_e32 v44, 0xf0f0f0f, v44
	v_dot4c_i32_i8_e32 v56, v44, v33
	v_and_b32_e32 v44, 0xf0f0f0f, v65
	v_dot4c_i32_i8_e32 v57, v44, v34
	v_lshrrev_b32_e32 v44, 4, v65
	v_and_b32_e32 v44, 0xf0f0f0f, v44
	v_dot4c_i32_i8_e32 v57, v44, v35
	v_and_b32_e32 v44, 0xf0f0f0f, v66
	v_dot4c_i32_i8_e32 v56, v44, v28
	v_lshrrev_b32_e32 v44, 4, v66
	v_and_b32_e32 v44, 0xf0f0f0f, v44
	v_dot4c_i32_i8_e32 v56, v44, v29
	v_and_b32_e32 v44, 0xf0f0f0f, v67
	v_dot4c_i32_i8_e32 v57, v44, v30
	v_lshrrev_b32_e32 v44, 4, v67
	v_and_b32_e32 v44, 0xf0f0f0f, v44
	v_dot4c_i32_i8_e32 v57, v44, v31
	v_sub_u32_e32 v47, v47, v169
	v_add_u32_e32 v46, v47, v46
	v_cvt_f32_i32_e32 v47, v46
	v_sub_u32_e32 v57, v57, v169
	v_add_u32_e32 v56, v57, v56
	v_cvt_f32_i32_e32 v46, v56
	s_waitcnt vmcnt(20)
; #define P12_ISSUE(c_, i_, h_, CW_, SC_) do { _Pragma("unroll") for (int bb = 0; bb < 8; ++bb) { const unsigned ro = (unsigned)(c_) * 16384u + (unsigned)EL[(i_) * 128 + ((h_) * 8 + bb) * 8 + g8]; \
;         CW_[bb] = *(const v4u*)(U4 + (size_t)(ro * 128u + 16u * (unsigned)k8)); SC_[bb] = USS[(size_t)(ro * 8u + (unsigned)k8)]; } } while (0)
; #define P12_COMP(i_, h_, CW_, SC_) do { _Pragma("unroll") for (int bb = 0; bb < 8; ++bb) { int a0 = 0, a1 = 0; P12_U4(CW_[bb].x, xa.x, xa.y, a0); P12_U4(CW_[bb].y, xa.z, xa.w, a1); P12_U4(CW_[bb].z, xb.x, xb.y, a0); P12_U4(CW_[bb].w, xb.z, xb.w, a1); \
;         psum[(i_)][(h_) * 8 + bb] += __uint_as_float(SC_[bb] << 16) * (float)((a0 + a1) - xo); } } while (0)
; #define P12_BAR() asm volatile("" ::: "memory")
; __device__ __forceinline__ void p12_peer(Frame& F) {
;     ...
;     { v4u cwA[8], cwB[8]; unsigned scA[8], scB[8]; v4u xa, xb; int xo;
;       P12_ISSUE(0, 0, 0, cwA, scA);
; _Pragma("nounroll")
;       for (int c = 0; c < 16; ++c) { const int cn = c + 1 < 16 ? c + 1 : 15;
;           P12_XQ(c, 0); P12_ISSUE(c, 0, 1, cwB, scB); P12_BAR(); P12_COMP(0, 0, cwA, scA); P12_ISSUE(c, 1, 0, cwA, scA); P12_BAR(); P12_COMP(0, 1, cwB, scB);
;           P12_XQ(c, 1); P12_ISSUE(c, 1, 1, cwB, scB); P12_BAR(); P12_COMP(1, 0, cwA, scA); P12_ISSUE(c, 2, 0, cwA, scA); P12_BAR(); P12_COMP(1, 1, cwB, scB);
;           P12_XQ(c, 2); P12_ISSUE(c, 2, 1, cwB, scB); P12_BAR(); P12_COMP(2, 0, cwA, scA); P12_ISSUE(c, 3, 0, cwA, scA); P12_BAR(); P12_COMP(2, 1, cwB, scB);
;           P12_XQ(c, 3); P12_ISSUE(c, 3, 1, cwB, scB); P12_BAR(); P12_COMP(3, 0, cwA, scA); P12_ISSUE(cn, 0, 0, cwA, scA); P12_BAR(); P12_COMP(3, 1, cwB, scB);
;       } }
	v_lshlrev_b32_e32 v45, 16, v175
	v_lshlrev_b32_e32 v44, 16, v174
	v_pk_fma_f32 v[116:117], v[44:45], v[46:47], v[116:117]
	v_and_b32_e32 v44, 0xf0f0f0f, v52
	v_mov_b32_e32 v46, 0
	v_dot4c_i32_i8_e32 v46, v44, v32
	v_lshrrev_b32_e32 v44, 4, v52
	v_and_b32_e32 v44, 0xf0f0f0f, v44
	v_dot4c_i32_i8_e32 v46, v44, v33
	v_and_b32_e32 v44, 0xf0f0f0f, v53
	v_mov_b32_e32 v47, 0
	v_dot4c_i32_i8_e32 v47, v44, v34
	v_lshrrev_b32_e32 v44, 4, v53
	v_and_b32_e32 v44, 0xf0f0f0f, v44
	v_dot4c_i32_i8_e32 v47, v44, v35
	v_and_b32_e32 v44, 0xf0f0f0f, v54
	v_dot4c_i32_i8_e32 v46, v44, v28
	v_lshrrev_b32_e32 v44, 4, v54
	v_and_b32_e32 v44, 0xf0f0f0f, v44
	v_dot4c_i32_i8_e32 v46, v44, v29
	v_and_b32_e32 v44, 0xf0f0f0f, v55
	v_dot4c_i32_i8_e32 v47, v44, v30
	v_lshrrev_b32_e32 v44, 4, v55
	v_and_b32_e32 v44, 0xf0f0f0f, v44
	v_dot4c_i32_i8_e32 v47, v44, v31
	v_and_b32_e32 v44, 0xf0f0f0f, v48
	v_mov_b32_e32 v52, 0
	v_dot4c_i32_i8_e32 v52, v44, v32
	v_lshrrev_b32_e32 v44, 4, v48
	v_and_b32_e32 v44, 0xf0f0f0f, v44
	v_dot4c_i32_i8_e32 v52, v44, v33
	v_and_b32_e32 v44, 0xf0f0f0f, v49
	v_mov_b32_e32 v48, 0
	v_dot4c_i32_i8_e32 v48, v44, v34
	v_lshrrev_b32_e32 v44, 4, v49
	v_and_b32_e32 v44, 0xf0f0f0f, v44
	v_dot4c_i32_i8_e32 v48, v44, v35
	v_and_b32_e32 v44, 0xf0f0f0f, v50
	v_dot4c_i32_i8_e32 v52, v44, v28
	v_lshrrev_b32_e32 v44, 4, v50
	v_and_b32_e32 v44, 0xf0f0f0f, v44
	v_dot4c_i32_i8_e32 v52, v44, v29
	v_and_b32_e32 v44, 0xf0f0f0f, v51
	v_dot4c_i32_i8_e32 v48, v44, v30
	v_lshrrev_b32_e32 v44, 4, v51
	v_and_b32_e32 v44, 0xf0f0f0f, v44
	v_dot4c_i32_i8_e32 v48, v44, v31
	v_sub_u32_e32 v47, v47, v169
	v_add_u32_e32 v46, v47, v46
	v_cvt_f32_i32_e32 v47, v46
	v_sub_u32_e32 v48, v48, v169
	v_add_u32_e32 v48, v48, v52
	v_cvt_f32_i32_e32 v46, v48
	s_waitcnt vmcnt(18)
	v_lshlrev_b32_e32 v45, 16, v173
	v_lshlrev_b32_e32 v44, 16, v172
	v_pk_fma_f32 v[114:115], v[44:45], v[46:47], v[114:115]
	v_and_b32_e32 v44, 0xf0f0f0f, v40
	v_mov_b32_e32 v45, 0
	v_lshrrev_b32_e32 v40, 4, v40
	v_dot4c_i32_i8_e32 v45, v44, v32
	v_and_b32_e32 v40, 0xf0f0f0f, v40
	v_dot4c_i32_i8_e32 v45, v40, v33
	v_and_b32_e32 v40, 0xf0f0f0f, v41
	v_mov_b32_e32 v44, 0
	v_dot4c_i32_i8_e32 v44, v40, v34
	v_lshrrev_b32_e32 v40, 4, v41
	v_and_b32_e32 v40, 0xf0f0f0f, v40
	v_dot4c_i32_i8_e32 v44, v40, v35
	v_and_b32_e32 v40, 0xf0f0f0f, v42
	v_dot4c_i32_i8_e32 v45, v40, v28
	v_lshrrev_b32_e32 v40, 4, v42
	v_and_b32_e32 v40, 0xf0f0f0f, v40
	v_dot4c_i32_i8_e32 v45, v40, v29
	v_and_b32_e32 v40, 0xf0f0f0f, v43
	v_dot4c_i32_i8_e32 v44, v40, v30
	v_lshrrev_b32_e32 v40, 4, v43
	v_and_b32_e32 v40, 0xf0f0f0f, v40
	v_dot4c_i32_i8_e32 v44, v40, v31
	v_and_b32_e32 v40, 0xf0f0f0f, v36
	v_mov_b32_e32 v41, 0
	v_dot4c_i32_i8_e32 v41, v40, v32
	v_lshrrev_b32_e32 v32, 4, v36
	v_and_b32_e32 v32, 0xf0f0f0f, v32
	v_dot4c_i32_i8_e32 v41, v32, v33
	v_and_b32_e32 v32, 0xf0f0f0f, v37
	v_mov_b32_e32 v33, 0
	v_dot4c_i32_i8_e32 v33, v32, v34
	v_lshrrev_b32_e32 v32, 4, v37
	v_and_b32_e32 v32, 0xf0f0f0f, v32
	v_dot4c_i32_i8_e32 v33, v32, v35
	v_and_b32_e32 v32, 0xf0f0f0f, v38
	v_dot4c_i32_i8_e32 v41, v32, v28
	v_lshrrev_b32_e32 v28, 4, v38
	v_and_b32_e32 v28, 0xf0f0f0f, v28
	v_dot4c_i32_i8_e32 v41, v28, v29
	v_and_b32_e32 v28, 0xf0f0f0f, v39
	v_dot4c_i32_i8_e32 v33, v28, v30
	v_lshrrev_b32_e32 v28, 4, v39
	v_and_b32_e32 v28, 0xf0f0f0f, v28
	v_dot4c_i32_i8_e32 v33, v28, v31
	v_sub_u32_e32 v30, v44, v169
	v_add_u32_e32 v30, v30, v45
	s_waitcnt vmcnt(16)
	v_lshlrev_b32_e32 v29, 16, v171
	v_sub_u32_e32 v31, v33, v169
	v_add_u32_e32 v32, v31, v41
	v_cvt_f32_i32_e32 v31, v30
	v_cvt_f32_i32_e32 v30, v32
	v_lshlrev_b32_e32 v28, 16, v170
	ds_read_b128 v[36:39], v166 offset:12288
	ds_read_b128 v[32:35], v166 offset:12304
	v_add_u32_e32 v166, 0x100, v166
	v_pk_fma_f32 v[112:113], v[28:29], v[30:31], v[112:113]
	ds_read_u16 v29, v93 offset:17280
	ds_read_u16 v30, v93 offset:17296
	ds_read_u16 v31, v93 offset:17312
	ds_read_u16 v40, v93 offset:17328
	v_mov_b32_e32 v28, 0
	s_waitcnt lgkmcnt(3)
	v_add_u32_e32 v29, s44, v29
	v_lshl_or_b32 v41, v29, 7, v165
	s_waitcnt lgkmcnt(2)
	v_add_u32_e32 v30, s44, v30
	global_load_dwordx4 v[68:71], v41, s[0:1]
	v_lshl_or_b32 v41, v30, 7, v165
	s_waitcnt lgkmcnt(1)
	v_add_u32_e32 v31, s44, v31
	global_load_dwordx4 v[64:67], v41, s[0:1]
	v_lshl_or_b32 v41, v31, 7, v165
	s_waitcnt lgkmcnt(0)
	v_add_u32_e32 v40, s44, v40
	global_load_dwordx4 v[60:63], v41, s[0:1]
	v_lshl_or_b32 v41, v40, 7, v165
	v_lshl_or_b32 v79, v40, 4, v95
	ds_read_u16 v40, v93 offset:17344
	global_load_dwordx4 v[56:59], v41, s[0:1]
	v_dot4c_i32_i8_e32 v28, 0x1010101, v36
	v_dot4c_i32_i8_e32 v28, 0x1010101, v37
	v_dot4c_i32_i8_e32 v28, 0x1010101, v38
	s_waitcnt lgkmcnt(0)
	v_add_u32_e32 v40, s44, v40
	v_lshl_or_b32 v41, v40, 7, v165
	v_lshl_or_b32 v80, v40, 4, v95
	ds_read_u16 v40, v93 offset:17360
	global_load_dwordx4 v[52:55], v41, s[0:1]
	v_dot4c_i32_i8_e32 v28, 0x1010101, v39
	v_dot4c_i32_i8_e32 v28, 0x1010101, v32
	v_dot4c_i32_i8_e32 v28, 0x1010101, v33
	s_waitcnt lgkmcnt(0)
	v_add_u32_e32 v40, s44, v40
	v_lshl_or_b32 v41, v40, 7, v165
	v_lshl_or_b32 v82, v40, 4, v95
	ds_read_u16 v40, v93 offset:17376
	global_load_dwordx4 v[48:51], v41, s[0:1]
	v_dot4c_i32_i8_e32 v28, 0x1010101, v34
	v_dot4c_i32_i8_e32 v28, 0x1010101, v35
	v_lshl_or_b32 v29, v29, 4, v95
	s_waitcnt lgkmcnt(0)
	v_add_u32_e32 v40, s44, v40
	v_lshl_or_b32 v41, v40, 7, v165
	v_lshl_or_b32 v87, v40, 4, v95
	ds_read_u16 v40, v93 offset:17392
	v_lshl_or_b32 v30, v30, 4, v95
	v_lshl_or_b32 v31, v31, 4, v95
	global_load_dwordx4 v[44:47], v41, s[0:1]
	s_waitcnt lgkmcnt(0)
; #define P12_ISSUE(c_, i_, h_, CW_, SC_) do { _Pragma("unroll") for (int bb = 0; bb < 8; ++bb) { const unsigned ro = (unsigned)(c_) * 16384u + (unsigned)EL[(i_) * 128 + ((h_) * 8 + bb) * 8 + g8]; \
;         CW_[bb] = *(const v4u*)(U4 + (size_t)(ro * 128u + 16u * (unsigned)k8)); SC_[bb] = USS[(size_t)(ro * 8u + (unsigned)k8)]; } } while (0)
; #define P12_COMP(i_, h_, CW_, SC_) do { _Pragma("unroll") for (int bb = 0; bb < 8; ++bb) { int a0 = 0, a1 = 0; P12_U4(CW_[bb].x, xa.x, xa.y, a0); P12_U4(CW_[bb].y, xa.z, xa.w, a1); P12_U4(CW_[bb].z, xb.x, xb.y, a0); P12_U4(CW_[bb].w, xb.z, xb.w, a1); \
;         psum[(i_)][(h_) * 8 + bb] += __uint_as_float(SC_[bb] << 16) * (float)((a0 + a1) - xo); } } while (0)
; #define P12_BAR() asm volatile("" ::: "memory")
; __device__ __forceinline__ void p12_peer(Frame& F) {
;     ...
;     { v4u cwA[8], cwB[8]; unsigned scA[8], scB[8]; v4u xa, xb; int xo;
;       P12_ISSUE(0, 0, 0, cwA, scA);
; _Pragma("nounroll")
;       for (int c = 0; c < 16; ++c) { const int cn = c + 1 < 16 ? c + 1 : 15;
;           P12_XQ(c, 0); P12_ISSUE(c, 0, 1, cwB, scB); P12_BAR(); P12_COMP(0, 0, cwA, scA); P12_ISSUE(c, 1, 0, cwA, scA); P12_BAR(); P12_COMP(0, 1, cwB, scB);
;           P12_XQ(c, 1); P12_ISSUE(c, 1, 1, cwB, scB); P12_BAR(); P12_COMP(1, 0, cwA, scA); P12_ISSUE(c, 2, 0, cwA, scA); P12_BAR(); P12_COMP(1, 1, cwB, scB);
;           P12_XQ(c, 2); P12_ISSUE(c, 2, 1, cwB, scB); P12_BAR(); P12_COMP(2, 0, cwA, scA); P12_ISSUE(c, 3, 0, cwA, scA); P12_BAR(); P12_COMP(2, 1, cwB, scB);
;           P12_XQ(c, 3); P12_ISSUE(c, 3, 1, cwB, scB); P12_BAR(); P12_COMP(3, 0, cwA, scA); P12_ISSUE(cn, 0, 0, cwA, scA); P12_BAR(); P12_COMP(3, 1, cwB, scB);
;       } }
	v_add_u32_e32 v78, s44, v40
	v_lshl_or_b32 v40, v78, 7, v165
	global_load_dwordx4 v[40:43], v40, s[0:1]
	v_lshl_or_b32 v169, v78, 4, v95
	v_lshlrev_b32_e32 v78, 3, v28
	global_load_ushort v85, v29, s[18:19]
	global_load_ushort v86, v30, s[18:19]
	global_load_ushort v83, v31, s[18:19]
	global_load_ushort v84, v79, s[18:19]
	global_load_ushort v81, v80, s[18:19]
	s_nop 0
	global_load_ushort v82, v82, s[18:19]
	s_nop 0
	global_load_ushort v79, v87, s[18:19]
	global_load_ushort v80, v169, s[18:19]
	s_waitcnt vmcnt(31)
	v_and_b32_e32 v29, 0xf0f0f0f, v72
	v_mov_b32_e32 v28, 0
	v_dot4c_i32_i8_e32 v28, v29, v36
	v_lshrrev_b32_e32 v29, 4, v72
	v_and_b32_e32 v29, 0xf0f0f0f, v29
	v_dot4c_i32_i8_e32 v28, v29, v37
	v_and_b32_e32 v30, 0xf0f0f0f, v73
	v_mov_b32_e32 v29, 0
	v_dot4c_i32_i8_e32 v29, v30, v38
	v_lshrrev_b32_e32 v30, 4, v73
	v_and_b32_e32 v30, 0xf0f0f0f, v30
	v_dot4c_i32_i8_e32 v29, v30, v39
	v_and_b32_e32 v30, 0xf0f0f0f, v74
	v_dot4c_i32_i8_e32 v28, v30, v32
	v_lshrrev_b32_e32 v30, 4, v74
	v_and_b32_e32 v30, 0xf0f0f0f, v30
	v_dot4c_i32_i8_e32 v28, v30, v33
	v_and_b32_e32 v30, 0xf0f0f0f, v75
	v_dot4c_i32_i8_e32 v29, v30, v34
	v_lshrrev_b32_e32 v30, 4, v75
	v_and_b32_e32 v30, 0xf0f0f0f, v30
	v_dot4c_i32_i8_e32 v29, v30, v35
	s_waitcnt vmcnt(30)
	v_and_b32_e32 v31, 0xf0f0f0f, v24
	v_mov_b32_e32 v30, 0
	v_lshrrev_b32_e32 v24, 4, v24
	v_dot4c_i32_i8_e32 v30, v31, v36
	v_and_b32_e32 v24, 0xf0f0f0f, v24
	v_dot4c_i32_i8_e32 v30, v24, v37
	v_and_b32_e32 v24, 0xf0f0f0f, v25
	v_mov_b32_e32 v31, 0
	v_dot4c_i32_i8_e32 v31, v24, v38
	v_lshrrev_b32_e32 v24, 4, v25
	v_and_b32_e32 v24, 0xf0f0f0f, v24
	v_dot4c_i32_i8_e32 v31, v24, v39
	v_and_b32_e32 v24, 0xf0f0f0f, v26
	v_dot4c_i32_i8_e32 v30, v24, v32
	v_lshrrev_b32_e32 v24, 4, v26
	v_and_b32_e32 v24, 0xf0f0f0f, v24
	v_dot4c_i32_i8_e32 v30, v24, v33
	v_and_b32_e32 v24, 0xf0f0f0f, v27
	v_dot4c_i32_i8_e32 v31, v24, v34
	v_lshrrev_b32_e32 v24, 4, v27
	v_and_b32_e32 v24, 0xf0f0f0f, v24
	v_dot4c_i32_i8_e32 v31, v24, v35
	v_add_u32_e32 v26, v28, v29
	v_sub_u32_e32 v26, v26, v78
	s_waitcnt vmcnt(22)
	v_lshlrev_b32_e32 v25, 16, v168
	v_add_u32_e32 v27, v30, v31
	v_sub_u32_e32 v28, v27, v78
	v_cvt_f32_i32_e32 v27, v26
	v_cvt_f32_i32_e32 v26, v28
	v_lshlrev_b32_e32 v24, 16, v167
	s_cselect_b32 s44, s44, s45
	v_pk_fma_f32 v[110:111], v[24:25], v[26:27], v[110:111]
	v_and_b32_e32 v24, 0xf0f0f0f, v20
	v_mov_b32_e32 v25, 0
	v_lshrrev_b32_e32 v20, 4, v20
	v_dot4c_i32_i8_e32 v25, v24, v36
	v_and_b32_e32 v20, 0xf0f0f0f, v20
	v_dot4c_i32_i8_e32 v25, v20, v37
	v_and_b32_e32 v20, 0xf0f0f0f, v21
	v_mov_b32_e32 v24, 0
	v_dot4c_i32_i8_e32 v24, v20, v38
	v_lshrrev_b32_e32 v20, 4, v21
	v_and_b32_e32 v20, 0xf0f0f0f, v20
	v_dot4c_i32_i8_e32 v24, v20, v39
	v_and_b32_e32 v20, 0xf0f0f0f, v22
	v_dot4c_i32_i8_e32 v25, v20, v32
	v_lshrrev_b32_e32 v20, 4, v22
	v_and_b32_e32 v20, 0xf0f0f0f, v20
	v_dot4c_i32_i8_e32 v25, v20, v33
	v_and_b32_e32 v20, 0xf0f0f0f, v23
	v_dot4c_i32_i8_e32 v24, v20, v34
	v_lshrrev_b32_e32 v20, 4, v23
	v_and_b32_e32 v20, 0xf0f0f0f, v20
	v_dot4c_i32_i8_e32 v24, v20, v35
	v_and_b32_e32 v20, 0xf0f0f0f, v16
	v_mov_b32_e32 v21, 0
	v_lshrrev_b32_e32 v16, 4, v16
	v_dot4c_i32_i8_e32 v21, v20, v36
	v_and_b32_e32 v16, 0xf0f0f0f, v16
	v_dot4c_i32_i8_e32 v21, v16, v37
	v_and_b32_e32 v16, 0xf0f0f0f, v17
	v_mov_b32_e32 v20, 0
	v_dot4c_i32_i8_e32 v20, v16, v38
	v_lshrrev_b32_e32 v16, 4, v17
	v_and_b32_e32 v16, 0xf0f0f0f, v16
	v_dot4c_i32_i8_e32 v20, v16, v39
	v_and_b32_e32 v16, 0xf0f0f0f, v18
	v_dot4c_i32_i8_e32 v21, v16, v32
	v_lshrrev_b32_e32 v16, 4, v18
	v_and_b32_e32 v16, 0xf0f0f0f, v16
	v_dot4c_i32_i8_e32 v21, v16, v33
	v_and_b32_e32 v16, 0xf0f0f0f, v19
	v_dot4c_i32_i8_e32 v20, v16, v34
	v_lshrrev_b32_e32 v16, 4, v19
	v_and_b32_e32 v16, 0xf0f0f0f, v16
	v_dot4c_i32_i8_e32 v20, v16, v35
	v_add_u32_e32 v18, v25, v24
	v_sub_u32_e32 v18, v18, v78
	s_waitcnt vmcnt(20)
	v_lshlrev_b32_e32 v17, 16, v91
	v_add_u32_e32 v19, v21, v20
	v_sub_u32_e32 v20, v19, v78
	v_cvt_f32_i32_e32 v19, v18
	v_cvt_f32_i32_e32 v18, v20
	v_lshlrev_b32_e32 v16, 16, v90
	v_mov_b32_e32 v90, 0
	s_cmp_eq_u32 s45, 0x40000
	v_pk_fma_f32 v[108:109], v[16:17], v[18:19], v[108:109]
	v_and_b32_e32 v16, 0xf0f0f0f, v12
	v_mov_b32_e32 v17, 0
	v_lshrrev_b32_e32 v12, 4, v12
	v_dot4c_i32_i8_e32 v17, v16, v36
	v_and_b32_e32 v12, 0xf0f0f0f, v12
	v_dot4c_i32_i8_e32 v17, v12, v37
	v_and_b32_e32 v12, 0xf0f0f0f, v13
	v_mov_b32_e32 v16, 0
	v_dot4c_i32_i8_e32 v16, v12, v38
	v_lshrrev_b32_e32 v12, 4, v13
	v_and_b32_e32 v12, 0xf0f0f0f, v12
	v_dot4c_i32_i8_e32 v16, v12, v39
	v_and_b32_e32 v12, 0xf0f0f0f, v14
	v_dot4c_i32_i8_e32 v17, v12, v32
	v_lshrrev_b32_e32 v12, 4, v14
	v_and_b32_e32 v12, 0xf0f0f0f, v12
	v_dot4c_i32_i8_e32 v17, v12, v33
	v_and_b32_e32 v12, 0xf0f0f0f, v15
	v_dot4c_i32_i8_e32 v16, v12, v34
	v_lshrrev_b32_e32 v12, 4, v15
	v_and_b32_e32 v12, 0xf0f0f0f, v12
	v_dot4c_i32_i8_e32 v16, v12, v35
	v_and_b32_e32 v12, 0xf0f0f0f, v8
	v_mov_b32_e32 v13, 0
	v_lshrrev_b32_e32 v8, 4, v8
	v_dot4c_i32_i8_e32 v13, v12, v36
	v_and_b32_e32 v8, 0xf0f0f0f, v8
	v_dot4c_i32_i8_e32 v13, v8, v37
	v_and_b32_e32 v8, 0xf0f0f0f, v9
	v_mov_b32_e32 v12, 0
	v_dot4c_i32_i8_e32 v12, v8, v38
	v_lshrrev_b32_e32 v8, 4, v9
	v_and_b32_e32 v8, 0xf0f0f0f, v8
	v_dot4c_i32_i8_e32 v12, v8, v39
	v_and_b32_e32 v8, 0xf0f0f0f, v10
	v_dot4c_i32_i8_e32 v13, v8, v32
	v_lshrrev_b32_e32 v8, 4, v10
	v_and_b32_e32 v8, 0xf0f0f0f, v8
	v_dot4c_i32_i8_e32 v13, v8, v33
	v_and_b32_e32 v8, 0xf0f0f0f, v11
	v_dot4c_i32_i8_e32 v12, v8, v34
	v_lshrrev_b32_e32 v8, 4, v11
	v_and_b32_e32 v8, 0xf0f0f0f, v8
	v_dot4c_i32_i8_e32 v12, v8, v35
	v_add_u32_e32 v11, v17, v16
	s_waitcnt vmcnt(18)
; #define P12_ISSUE(c_, i_, h_, CW_, SC_) do { _Pragma("unroll") for (int bb = 0; bb < 8; ++bb) { const unsigned ro = (unsigned)(c_) * 16384u + (unsigned)EL[(i_) * 128 + ((h_) * 8 + bb) * 8 + g8]; \
;         CW_[bb] = *(const v4u*)(U4 + (size_t)(ro * 128u + 16u * (unsigned)k8)); SC_[bb] = USS[(size_t)(ro * 8u + (unsigned)k8)]; } } while (0)
; #define P12_COMP(i_, h_, CW_, SC_) do { _Pragma("unroll") for (int bb = 0; bb < 8; ++bb) { int a0 = 0, a1 = 0; P12_U4(CW_[bb].x, xa.x, xa.y, a0); P12_U4(CW_[bb].y, xa.z, xa.w, a1); P12_U4(CW_[bb].z, xb.x, xb.y, a0); P12_U4(CW_[bb].w, xb.z, xb.w, a1); \
;         psum[(i_)][(h_) * 8 + bb] += __uint_as_float(SC_[bb] << 16) * (float)((a0 + a1) - xo); } } while (0)
; #define P12_BAR() asm volatile("" ::: "memory")
; __device__ __forceinline__ void p12_peer(Frame& F) {
;     ...
;     { v4u cwA[8], cwB[8]; unsigned scA[8], scB[8]; v4u xa, xb; int xo;
;       P12_ISSUE(0, 0, 0, cwA, scA);
; _Pragma("nounroll")
;       for (int c = 0; c < 16; ++c) { const int cn = c + 1 < 16 ? c + 1 : 15;
;           P12_XQ(c, 0); P12_ISSUE(c, 0, 1, cwB, scB); P12_BAR(); P12_COMP(0, 0, cwA, scA); P12_ISSUE(c, 1, 0, cwA, scA); P12_BAR(); P12_COMP(0, 1, cwB, scB);
;           P12_XQ(c, 1); P12_ISSUE(c, 1, 1, cwB, scB); P12_BAR(); P12_COMP(1, 0, cwA, scA); P12_ISSUE(c, 2, 0, cwA, scA); P12_BAR(); P12_COMP(1, 1, cwB, scB);
;           P12_XQ(c, 2); P12_ISSUE(c, 2, 1, cwB, scB); P12_BAR(); P12_COMP(2, 0, cwA, scA); P12_ISSUE(c, 3, 0, cwA, scA); P12_BAR(); P12_COMP(2, 1, cwB, scB);
;           P12_XQ(c, 3); P12_ISSUE(c, 3, 1, cwB, scB); P12_BAR(); P12_COMP(3, 0, cwA, scA); P12_ISSUE(cn, 0, 0, cwA, scA); P12_BAR(); P12_COMP(3, 1, cwB, scB);
;       } }
	v_lshlrev_b32_e32 v9, 16, v89
	v_lshlrev_b32_e32 v8, 16, v88
	v_add_u32_e32 v10, v13, v12
	v_sub_u32_e32 v12, v11, v78
	v_sub_u32_e32 v10, v10, v78
	v_cvt_f32_i32_e32 v11, v10
	v_cvt_f32_i32_e32 v10, v12
	s_waitcnt vmcnt(15)
	v_and_b32_e32 v89, 0xf0f0f0f, v68
	v_lshrrev_b32_e32 v68, 4, v68
	v_dot4c_i32_i8_e32 v90, v89, v36
	v_pk_fma_f32 v[106:107], v[8:9], v[10:11], v[106:107]
	v_and_b32_e32 v8, 0xf0f0f0f, v4
	v_mov_b32_e32 v9, 0
	v_lshrrev_b32_e32 v4, 4, v4
	v_dot4c_i32_i8_e32 v9, v8, v36
	v_and_b32_e32 v4, 0xf0f0f0f, v4
	v_dot4c_i32_i8_e32 v9, v4, v37
	v_and_b32_e32 v4, 0xf0f0f0f, v5
	v_mov_b32_e32 v8, 0
	v_dot4c_i32_i8_e32 v8, v4, v38
	v_lshrrev_b32_e32 v4, 4, v5
	v_and_b32_e32 v4, 0xf0f0f0f, v4
	v_dot4c_i32_i8_e32 v8, v4, v39
	v_and_b32_e32 v4, 0xf0f0f0f, v6
	v_dot4c_i32_i8_e32 v9, v4, v32
	v_lshrrev_b32_e32 v4, 4, v6
	v_and_b32_e32 v4, 0xf0f0f0f, v4
	v_dot4c_i32_i8_e32 v9, v4, v33
	v_and_b32_e32 v4, 0xf0f0f0f, v7
	v_dot4c_i32_i8_e32 v8, v4, v34
	v_lshrrev_b32_e32 v4, 4, v7
	v_and_b32_e32 v4, 0xf0f0f0f, v4
	v_dot4c_i32_i8_e32 v8, v4, v35
	v_and_b32_e32 v4, 0xf0f0f0f, v0
	v_mov_b32_e32 v5, 0
	v_lshrrev_b32_e32 v0, 4, v0
	v_dot4c_i32_i8_e32 v5, v4, v36
	v_and_b32_e32 v0, 0xf0f0f0f, v0
	v_dot4c_i32_i8_e32 v5, v0, v37
	v_and_b32_e32 v0, 0xf0f0f0f, v1
	v_mov_b32_e32 v4, 0
	v_dot4c_i32_i8_e32 v4, v0, v38
	v_lshrrev_b32_e32 v0, 4, v1
	v_and_b32_e32 v0, 0xf0f0f0f, v0
	v_dot4c_i32_i8_e32 v4, v0, v39
	v_and_b32_e32 v0, 0xf0f0f0f, v2
	v_dot4c_i32_i8_e32 v5, v0, v32
	v_lshrrev_b32_e32 v0, 4, v2
	v_and_b32_e32 v0, 0xf0f0f0f, v0
	v_dot4c_i32_i8_e32 v5, v0, v33
	v_and_b32_e32 v0, 0xf0f0f0f, v3
	v_dot4c_i32_i8_e32 v4, v0, v34
	v_lshrrev_b32_e32 v0, 4, v3
	v_and_b32_e32 v0, 0xf0f0f0f, v0
	v_dot4c_i32_i8_e32 v4, v0, v35
	v_add_u32_e32 v3, v9, v8
	v_lshlrev_b32_e32 v1, 16, v77
	v_lshlrev_b32_e32 v0, 16, v76
	v_add_u32_e32 v2, v5, v4
	v_sub_u32_e32 v4, v3, v78
	v_sub_u32_e32 v2, v2, v78
	v_cvt_f32_i32_e32 v3, v2
	v_cvt_f32_i32_e32 v2, v4
	v_and_b32_e32 v68, 0xf0f0f0f, v68
	v_dot4c_i32_i8_e32 v90, v68, v37
	v_and_b32_e32 v68, 0xf0f0f0f, v69
	v_pk_fma_f32 v[104:105], v[0:1], v[2:3], v[104:105]
	ds_read_u16 v0, v93 offset:16384
	ds_read_u16 v1, v93 offset:16400
	ds_read_u16 v2, v93 offset:16416
	ds_read_u16 v3, v93 offset:16432
	v_mov_b32_e32 v89, 0
	s_waitcnt lgkmcnt(3)
	v_add_u32_e32 v0, s44, v0
	v_lshl_or_b32 v4, v0, 7, v165
	v_lshl_or_b32 v0, v0, 4, v95
	global_load_dwordx4 v[28:31], v4, s[0:1]
	global_load_ushort v72, v0, s[18:19]
	s_waitcnt lgkmcnt(2)
	v_add_u32_e32 v0, s44, v1
	v_dot4c_i32_i8_e32 v89, v68, v38
	v_lshrrev_b32_e32 v68, 4, v69
	v_lshl_or_b32 v1, v0, 7, v165
	v_lshl_or_b32 v0, v0, 4, v95
	v_and_b32_e32 v68, 0xf0f0f0f, v68
	global_load_dwordx4 v[24:27], v1, s[0:1]
	global_load_ushort v73, v0, s[18:19]
	s_waitcnt lgkmcnt(1)
	v_add_u32_e32 v0, s44, v2
	v_dot4c_i32_i8_e32 v89, v68, v39
	v_and_b32_e32 v68, 0xf0f0f0f, v70
	v_lshl_or_b32 v1, v0, 7, v165
	v_lshl_or_b32 v0, v0, 4, v95
	v_dot4c_i32_i8_e32 v90, v68, v32
	v_lshrrev_b32_e32 v68, 4, v70
	global_load_dwordx4 v[20:23], v1, s[0:1]
	global_load_ushort v74, v0, s[18:19]
	s_waitcnt lgkmcnt(0)
	v_add_u32_e32 v0, s44, v3
	v_and_b32_e32 v68, 0xf0f0f0f, v68
	v_lshl_or_b32 v1, v0, 7, v165
	v_lshl_or_b32 v0, v0, 4, v95
	v_dot4c_i32_i8_e32 v90, v68, v33
	v_and_b32_e32 v68, 0xf0f0f0f, v71
	global_load_dwordx4 v[16:19], v1, s[0:1]
	global_load_ushort v75, v0, s[18:19]
	ds_read_u16 v0, v93 offset:16448
	v_dot4c_i32_i8_e32 v89, v68, v34
	v_lshrrev_b32_e32 v68, 4, v71
	v_and_b32_e32 v68, 0xf0f0f0f, v68
	v_dot4c_i32_i8_e32 v89, v68, v35
	s_waitcnt vmcnt(22)
	v_and_b32_e32 v68, 0xf0f0f0f, v64
	v_mov_b32_e32 v69, 0
	v_lshrrev_b32_e32 v64, 4, v64
	v_dot4c_i32_i8_e32 v69, v68, v36
	v_and_b32_e32 v64, 0xf0f0f0f, v64
	v_dot4c_i32_i8_e32 v69, v64, v37
	v_and_b32_e32 v64, 0xf0f0f0f, v65
	v_mov_b32_e32 v68, 0
	s_waitcnt lgkmcnt(0)
	v_add_u32_e32 v0, s44, v0
	v_dot4c_i32_i8_e32 v68, v64, v38
	v_lshrrev_b32_e32 v64, 4, v65
	v_lshl_or_b32 v1, v0, 7, v165
	v_lshl_or_b32 v0, v0, 4, v95
	v_and_b32_e32 v64, 0xf0f0f0f, v64
	global_load_dwordx4 v[12:15], v1, s[0:1]
	global_load_ushort v76, v0, s[18:19]
	ds_read_u16 v0, v93 offset:16464
	v_dot4c_i32_i8_e32 v68, v64, v39
	v_and_b32_e32 v64, 0xf0f0f0f, v66
	v_dot4c_i32_i8_e32 v69, v64, v32
	v_lshrrev_b32_e32 v64, 4, v66
	v_and_b32_e32 v64, 0xf0f0f0f, v64
	v_dot4c_i32_i8_e32 v69, v64, v33
	v_and_b32_e32 v64, 0xf0f0f0f, v67
	v_dot4c_i32_i8_e32 v68, v64, v34
	v_lshrrev_b32_e32 v64, 4, v67
	s_waitcnt lgkmcnt(0)
	v_add_u32_e32 v0, s44, v0
	v_and_b32_e32 v64, 0xf0f0f0f, v64
	v_lshl_or_b32 v1, v0, 7, v165
	v_lshl_or_b32 v0, v0, 4, v95
	v_dot4c_i32_i8_e32 v68, v64, v35
	global_load_dwordx4 v[8:11], v1, s[0:1]
	global_load_ushort v77, v0, s[18:19]
	ds_read_u16 v0, v93 offset:16480
	v_add_u32_e32 v66, v90, v89
	v_sub_u32_e32 v67, v68, v78
	v_add_u32_e32 v67, v67, v69
	v_sub_u32_e32 v66, v66, v78
	v_cvt_f32_i32_e32 v66, v66
	v_cvt_f32_i32_e32 v67, v67
	s_waitcnt lgkmcnt(0)
	v_add_u32_e32 v0, s44, v0
	s_waitcnt vmcnt(18)
	v_lshlrev_b32_e32 v65, 16, v86
	v_lshlrev_b32_e32 v64, 16, v85
	v_lshl_or_b32 v1, v0, 7, v165
	v_lshl_or_b32 v0, v0, 4, v95
	v_pk_fma_f32 v[102:103], v[64:65], v[66:67], v[102:103]
	v_and_b32_e32 v64, 0xf0f0f0f, v60
	v_mov_b32_e32 v65, 0
	v_lshrrev_b32_e32 v60, 4, v60
	global_load_dwordx4 v[4:7], v1, s[0:1]
	global_load_ushort v87, v0, s[18:19]
	ds_read_u16 v0, v93 offset:16496
	v_dot4c_i32_i8_e32 v65, v64, v36
	v_and_b32_e32 v60, 0xf0f0f0f, v60
	v_dot4c_i32_i8_e32 v65, v60, v37
	v_and_b32_e32 v60, 0xf0f0f0f, v61
	v_mov_b32_e32 v64, 0
	v_dot4c_i32_i8_e32 v64, v60, v38
	v_lshrrev_b32_e32 v60, 4, v61
	v_and_b32_e32 v60, 0xf0f0f0f, v60
	v_dot4c_i32_i8_e32 v64, v60, v39
	v_and_b32_e32 v60, 0xf0f0f0f, v62
	s_waitcnt lgkmcnt(0)
; #define P12_ISSUE(c_, i_, h_, CW_, SC_) do { _Pragma("unroll") for (int bb = 0; bb < 8; ++bb) { const unsigned ro = (unsigned)(c_) * 16384u + (unsigned)EL[(i_) * 128 + ((h_) * 8 + bb) * 8 + g8]; \
;         CW_[bb] = *(const v4u*)(U4 + (size_t)(ro * 128u + 16u * (unsigned)k8)); SC_[bb] = USS[(size_t)(ro * 8u + (unsigned)k8)]; } } while (0)
; #define P12_COMP(i_, h_, CW_, SC_) do { _Pragma("unroll") for (int bb = 0; bb < 8; ++bb) { int a0 = 0, a1 = 0; P12_U4(CW_[bb].x, xa.x, xa.y, a0); P12_U4(CW_[bb].y, xa.z, xa.w, a1); P12_U4(CW_[bb].z, xb.x, xb.y, a0); P12_U4(CW_[bb].w, xb.z, xb.w, a1); \
;         psum[(i_)][(h_) * 8 + bb] += __uint_as_float(SC_[bb] << 16) * (float)((a0 + a1) - xo); } } while (0)
; #define P12_BAR() asm volatile("" ::: "memory")
; __device__ __forceinline__ void p12_peer(Frame& F) {
;     ...
;     { v4u cwA[8], cwB[8]; unsigned scA[8], scB[8]; v4u xa, xb; int xo;
;       P12_ISSUE(0, 0, 0, cwA, scA);
; _Pragma("nounroll")
;       for (int c = 0; c < 16; ++c) { const int cn = c + 1 < 16 ? c + 1 : 15;
;           P12_XQ(c, 0); P12_ISSUE(c, 0, 1, cwB, scB); P12_BAR(); P12_COMP(0, 0, cwA, scA); P12_ISSUE(c, 1, 0, cwA, scA); P12_BAR(); P12_COMP(0, 1, cwB, scB);
;           P12_XQ(c, 1); P12_ISSUE(c, 1, 1, cwB, scB); P12_BAR(); P12_COMP(1, 0, cwA, scA); P12_ISSUE(c, 2, 0, cwA, scA); P12_BAR(); P12_COMP(1, 1, cwB, scB);
;           P12_XQ(c, 2); P12_ISSUE(c, 2, 1, cwB, scB); P12_BAR(); P12_COMP(2, 0, cwA, scA); P12_ISSUE(c, 3, 0, cwA, scA); P12_BAR(); P12_COMP(2, 1, cwB, scB);
;           P12_XQ(c, 3); P12_ISSUE(c, 3, 1, cwB, scB); P12_BAR(); P12_COMP(3, 0, cwA, scA); P12_ISSUE(cn, 0, 0, cwA, scA); P12_BAR(); P12_COMP(3, 1, cwB, scB);
;       } }
	v_add_u32_e32 v88, s44, v0
	v_dot4c_i32_i8_e32 v65, v60, v32
	v_lshrrev_b32_e32 v60, 4, v62
	v_lshl_or_b32 v0, v88, 7, v165
	v_lshl_or_b32 v88, v88, 4, v95
	v_and_b32_e32 v60, 0xf0f0f0f, v60
	global_load_dwordx4 v[0:3], v0, s[0:1]
	v_dot4c_i32_i8_e32 v65, v60, v33
	global_load_ushort v88, v88, s[18:19]
	v_and_b32_e32 v60, 0xf0f0f0f, v63
	v_dot4c_i32_i8_e32 v64, v60, v34
	v_lshrrev_b32_e32 v60, 4, v63
	v_and_b32_e32 v60, 0xf0f0f0f, v60
	v_dot4c_i32_i8_e32 v64, v60, v35
	v_and_b32_e32 v60, 0xf0f0f0f, v56
	v_mov_b32_e32 v61, 0
	v_lshrrev_b32_e32 v56, 4, v56
	v_dot4c_i32_i8_e32 v61, v60, v36
	v_and_b32_e32 v56, 0xf0f0f0f, v56
	v_dot4c_i32_i8_e32 v61, v56, v37
	v_and_b32_e32 v56, 0xf0f0f0f, v57
	v_mov_b32_e32 v60, 0
	v_dot4c_i32_i8_e32 v60, v56, v38
	v_lshrrev_b32_e32 v56, 4, v57
	v_and_b32_e32 v56, 0xf0f0f0f, v56
	v_dot4c_i32_i8_e32 v60, v56, v39
	v_and_b32_e32 v56, 0xf0f0f0f, v58
	v_dot4c_i32_i8_e32 v61, v56, v32
	v_lshrrev_b32_e32 v56, 4, v58
	v_and_b32_e32 v56, 0xf0f0f0f, v56
	v_dot4c_i32_i8_e32 v61, v56, v33
	v_and_b32_e32 v56, 0xf0f0f0f, v59
	v_dot4c_i32_i8_e32 v60, v56, v34
	v_lshrrev_b32_e32 v56, 4, v59
	v_and_b32_e32 v56, 0xf0f0f0f, v56
	v_dot4c_i32_i8_e32 v60, v56, v35
	v_sub_u32_e32 v59, v64, v78
	s_waitcnt vmcnt(20)
	v_lshlrev_b32_e32 v57, 16, v84
	v_lshlrev_b32_e32 v56, 16, v83
	v_sub_u32_e32 v58, v60, v78
	v_add_u32_e32 v60, v59, v65
	v_add_u32_e32 v58, v58, v61
	v_cvt_f32_i32_e32 v59, v58
	v_cvt_f32_i32_e32 v58, v60
	s_mov_b32 s44, s45
	v_pk_fma_f32 v[100:101], v[56:57], v[58:59], v[100:101]
	v_and_b32_e32 v56, 0xf0f0f0f, v52
	v_mov_b32_e32 v57, 0
	v_lshrrev_b32_e32 v52, 4, v52
	v_dot4c_i32_i8_e32 v57, v56, v36
	v_and_b32_e32 v52, 0xf0f0f0f, v52
	v_dot4c_i32_i8_e32 v57, v52, v37
	v_and_b32_e32 v52, 0xf0f0f0f, v53
	v_mov_b32_e32 v56, 0
	v_dot4c_i32_i8_e32 v56, v52, v38
	v_lshrrev_b32_e32 v52, 4, v53
	v_and_b32_e32 v52, 0xf0f0f0f, v52
	v_dot4c_i32_i8_e32 v56, v52, v39
	v_and_b32_e32 v52, 0xf0f0f0f, v54
	v_dot4c_i32_i8_e32 v57, v52, v32
	v_lshrrev_b32_e32 v52, 4, v54
	v_and_b32_e32 v52, 0xf0f0f0f, v52
	v_dot4c_i32_i8_e32 v57, v52, v33
	v_and_b32_e32 v52, 0xf0f0f0f, v55
	v_dot4c_i32_i8_e32 v56, v52, v34
	v_lshrrev_b32_e32 v52, 4, v55
	v_and_b32_e32 v52, 0xf0f0f0f, v52
	v_dot4c_i32_i8_e32 v56, v52, v35
	v_and_b32_e32 v52, 0xf0f0f0f, v48
	v_mov_b32_e32 v53, 0
	v_lshrrev_b32_e32 v48, 4, v48
	v_dot4c_i32_i8_e32 v53, v52, v36
	v_and_b32_e32 v48, 0xf0f0f0f, v48
	v_dot4c_i32_i8_e32 v53, v48, v37
	v_and_b32_e32 v48, 0xf0f0f0f, v49
	v_mov_b32_e32 v52, 0
	v_dot4c_i32_i8_e32 v52, v48, v38
	v_lshrrev_b32_e32 v48, 4, v49
	v_and_b32_e32 v48, 0xf0f0f0f, v48
	v_dot4c_i32_i8_e32 v52, v48, v39
	v_and_b32_e32 v48, 0xf0f0f0f, v50
	v_dot4c_i32_i8_e32 v53, v48, v32
	v_lshrrev_b32_e32 v48, 4, v50
	v_and_b32_e32 v48, 0xf0f0f0f, v48
	v_dot4c_i32_i8_e32 v53, v48, v33
	v_and_b32_e32 v48, 0xf0f0f0f, v51
	v_dot4c_i32_i8_e32 v52, v48, v34
	v_lshrrev_b32_e32 v48, 4, v51
	v_and_b32_e32 v48, 0xf0f0f0f, v48
	v_dot4c_i32_i8_e32 v52, v48, v35
	v_sub_u32_e32 v51, v56, v78
	s_waitcnt vmcnt(18)
	v_lshlrev_b32_e32 v49, 16, v82
	v_lshlrev_b32_e32 v48, 16, v81
	v_sub_u32_e32 v50, v52, v78
	v_add_u32_e32 v52, v51, v57
	v_add_u32_e32 v50, v50, v53
	v_cvt_f32_i32_e32 v51, v50
	v_cvt_f32_i32_e32 v50, v52
	v_pk_fma_f32 v[98:99], v[48:49], v[50:51], v[98:99]
	v_and_b32_e32 v48, 0xf0f0f0f, v44
	v_mov_b32_e32 v49, 0
	v_lshrrev_b32_e32 v44, 4, v44
	v_dot4c_i32_i8_e32 v49, v48, v36
	v_and_b32_e32 v44, 0xf0f0f0f, v44
	v_dot4c_i32_i8_e32 v49, v44, v37
	v_and_b32_e32 v44, 0xf0f0f0f, v45
	v_mov_b32_e32 v48, 0
	v_dot4c_i32_i8_e32 v48, v44, v38
	v_lshrrev_b32_e32 v44, 4, v45
	v_and_b32_e32 v44, 0xf0f0f0f, v44
	v_dot4c_i32_i8_e32 v48, v44, v39
	v_and_b32_e32 v44, 0xf0f0f0f, v46
	v_dot4c_i32_i8_e32 v49, v44, v32
	v_lshrrev_b32_e32 v44, 4, v46
	v_and_b32_e32 v44, 0xf0f0f0f, v44
	v_dot4c_i32_i8_e32 v49, v44, v33
	v_and_b32_e32 v44, 0xf0f0f0f, v47
	v_dot4c_i32_i8_e32 v48, v44, v34
	v_lshrrev_b32_e32 v44, 4, v47
	v_and_b32_e32 v44, 0xf0f0f0f, v44
	v_dot4c_i32_i8_e32 v48, v44, v35
	v_and_b32_e32 v44, 0xf0f0f0f, v40
	v_mov_b32_e32 v45, 0
	v_dot4c_i32_i8_e32 v45, v44, v36
	v_lshrrev_b32_e32 v36, 4, v40
	v_and_b32_e32 v36, 0xf0f0f0f, v36
	v_dot4c_i32_i8_e32 v45, v36, v37
	v_and_b32_e32 v36, 0xf0f0f0f, v41
	v_mov_b32_e32 v37, 0
	v_dot4c_i32_i8_e32 v37, v36, v38
	v_lshrrev_b32_e32 v36, 4, v41
	v_and_b32_e32 v36, 0xf0f0f0f, v36
	v_dot4c_i32_i8_e32 v37, v36, v39
	v_and_b32_e32 v36, 0xf0f0f0f, v42
	v_dot4c_i32_i8_e32 v45, v36, v32
	v_lshrrev_b32_e32 v32, 4, v42
	v_and_b32_e32 v32, 0xf0f0f0f, v32
	v_dot4c_i32_i8_e32 v45, v32, v33
	v_and_b32_e32 v32, 0xf0f0f0f, v43
	v_dot4c_i32_i8_e32 v37, v32, v34
	v_lshrrev_b32_e32 v32, 4, v43
	v_and_b32_e32 v32, 0xf0f0f0f, v32
	v_dot4c_i32_i8_e32 v37, v32, v35
	v_sub_u32_e32 v35, v48, v78
	v_add_u32_e32 v36, v35, v49
	s_waitcnt vmcnt(16)
	v_lshlrev_b32_e32 v33, 16, v80
	v_sub_u32_e32 v34, v37, v78
	v_add_u32_e32 v34, v34, v45
	v_cvt_f32_i32_e32 v35, v34
	v_cvt_f32_i32_e32 v34, v36
	v_lshlrev_b32_e32 v32, 16, v79
	s_waitcnt vmcnt(0)
	v_perm_b32 v40, v87, v88, s43
	v_perm_b32 v41, v76, v77, s43
	v_pk_fma_f32 v[96:97], v[32:33], v[34:35], v[96:97]
	v_perm_b32 v42, v74, v75, s43
	v_perm_b32 v43, v72, v73, s43
	s_cbranch_scc0 .LBB0_3272
; __device__ __forceinline__ float gelu_erf(float v) {
;     const float av = fabsf(v), tt = __builtin_amdgcn_rcpf(av * 0.2316418882f + 1.0f);
;     float q = tt * 0.5307027145f + (-0.7265760135f); q = q * tt + 0.7107068705f; q = q * tt + (-0.142248368f); q = q * tt + 0.127414796f; q = q * tt;
;     const float e = __builtin_amdgcn_exp2f((v * v) * (-0.72134752044f));
;     const float m = v * (q * e); return v < 0.f ? m : v - m;
; }
; __device__ __forceinline__ void p12_peer(Frame& F) {
;     ...
; #pragma unroll
;     for (int i = 0; i < 4; ++i) { const int t = F.gw + i * F.NGW;
; #pragma unroll
;         for (int b = 0; b < 16; ++b) { float d = psum[i][b];
;             d += __builtin_bit_cast(float, __builtin_amdgcn_update_dpp(0, __builtin_bit_cast(int, d), 0xB1, 0xF, 0xF, false));
;             d += __builtin_bit_cast(float, __builtin_amdgcn_update_dpp(0, __builtin_bit_cast(int, d), 0x4E, 0xF, 0xF, false));
;             d += __builtin_bit_cast(float, __builtin_amdgcn_update_dpp(0, __builtin_bit_cast(int, d), 0x141, 0xF, 0xF, false));
;             const int idx = b * 8 + g8; const float w = PGT[(size_t)t * 128 + idx] * gelu_erf(sx[i] * d) * VSC[EL[i * 128 + idx]];
;             if (k8 == 0) WL[i * 128 + idx] = w; } }
	v_mov_b32_e32 v0, s41
	v_mov_b32_e32 v1, s42
	v_add_f32_e32 v0, s39, v0
	v_add_f32_e32 v1, s40, v1
	v_add_f32_e32 v0, v0, v1
	v_mov_b32_e32 v1, 0x358637bd
	v_fmac_f32_e32 v1, 0x39800000, v0
	s_mov_b32 s0, 0xf800000
	v_mul_f32_e32 v0, 0x4f800000, v1
	v_cmp_gt_f32_e32 vcc, s0, v1
	s_add_u32 s43, s68, 0x1200000
	s_addc_u32 s44, s69, 0
	v_cndmask_b32_e32 v0, v1, v0, vcc
	v_sqrt_f32_e32 v1, v0
	s_add_u32 s18, s68, 0xf000000
	s_addc_u32 s19, s69, 0
	v_add_u32_e32 v2, -1, v1
	v_fma_f32 v3, -v2, v1, v0
	v_cmp_ge_f32_e64 s[0:1], 0, v3
	v_add_u32_e32 v3, 1, v1
	s_add_u32 s2, s43, s2
	v_cndmask_b32_e64 v2, v1, v2, s[0:1]
	v_fma_f32 v1, -v3, v1, v0
	v_cmp_lt_f32_e64 s[0:1], 0, v1
	s_waitcnt lgkmcnt(0)
	s_addc_u32 s3, s44, s3
	v_ashrrev_i32_e32 v95, 31, v94
	v_cndmask_b32_e64 v1, v2, v3, s[0:1]
	v_mul_f32_e32 v2, 0x37800000, v1
	v_cndmask_b32_e32 v1, v1, v2, vcc
	v_mov_b32_e32 v2, 0x260
	v_cmp_class_f32_e32 vcc, v0, v2
	s_nop 1
	v_cndmask_b32_e32 v2, v1, v0, vcc
	v_div_scale_f32 v3, s[0:1], v2, v2, 1.0
	v_rcp_f32_e32 v4, v3
	v_lshl_add_u64 v[0:1], v[94:95], 2, s[2:3]
	ds_read_u16 v20, v93 offset:16384
	ds_read_u16 v21, v93 offset:16400
	ds_read_u16 v22, v93 offset:16416
	ds_read_u16 v23, v93 offset:16432
	ds_read_u16 v24, v93 offset:16448
	ds_read_u16 v25, v93 offset:16464
	ds_read_u16 v26, v93 offset:16480
	ds_read_u16 v27, v93 offset:16496
	s_waitcnt lgkmcnt(0)
	ds_read_u16 v28, v93 offset:16512
	ds_read_u16 v29, v93 offset:16528
	ds_read_u16 v30, v93 offset:16544
	ds_read_u16 v31, v93 offset:16560
	ds_read_u16 v32, v93 offset:16576
	ds_read_u16 v33, v93 offset:16592
	ds_read_u16 v34, v93 offset:16608
	ds_read_u16 v35, v93 offset:16624
	s_waitcnt lgkmcnt(0)
	v_lshlrev_b32_e32 v20, 2, v20
	v_lshlrev_b32_e32 v21, 2, v21
	v_lshlrev_b32_e32 v22, 2, v22
	v_lshlrev_b32_e32 v23, 2, v23
	v_lshlrev_b32_e32 v24, 2, v24
	v_lshlrev_b32_e32 v25, 2, v25
	v_lshlrev_b32_e32 v26, 2, v26
	v_lshlrev_b32_e32 v27, 2, v27
	v_lshlrev_b32_e32 v28, 2, v28
	v_lshlrev_b32_e32 v29, 2, v29
	v_lshlrev_b32_e32 v30, 2, v30
	v_lshlrev_b32_e32 v31, 2, v31
	v_lshlrev_b32_e32 v32, 2, v32
	v_lshlrev_b32_e32 v33, 2, v33
	v_lshlrev_b32_e32 v34, 2, v34
	v_lshlrev_b32_e32 v35, 2, v35
	global_load_dword v40, v[0:1], off offset:0
	global_load_dword v60, v20, s[18:19]
	global_load_dword v41, v[0:1], off offset:32
	global_load_dword v61, v21, s[18:19]
	global_load_dword v42, v[0:1], off offset:64
	global_load_dword v62, v22, s[18:19]
	global_load_dword v43, v[0:1], off offset:96
	global_load_dword v63, v23, s[18:19]
	global_load_dword v44, v[0:1], off offset:128
	global_load_dword v64, v24, s[18:19]
	global_load_dword v45, v[0:1], off offset:160
	global_load_dword v65, v25, s[18:19]
	global_load_dword v46, v[0:1], off offset:192
	global_load_dword v66, v26, s[18:19]
	global_load_dword v47, v[0:1], off offset:224
	global_load_dword v67, v27, s[18:19]
	global_load_dword v48, v[0:1], off offset:256
	global_load_dword v68, v28, s[18:19]
	global_load_dword v49, v[0:1], off offset:288
	global_load_dword v69, v29, s[18:19]
	global_load_dword v50, v[0:1], off offset:320
	global_load_dword v70, v30, s[18:19]
	global_load_dword v51, v[0:1], off offset:352
	global_load_dword v71, v31, s[18:19]
	global_load_dword v52, v[0:1], off offset:384
	global_load_dword v72, v32, s[18:19]
	global_load_dword v53, v[0:1], off offset:416
	global_load_dword v73, v33, s[18:19]
	global_load_dword v54, v[0:1], off offset:448
	global_load_dword v74, v34, s[18:19]
	global_load_dword v55, v[0:1], off offset:480
	global_load_dword v75, v35, s[18:19]
	s_waitcnt vmcnt(0)
	v_cmp_eq_u32_e64 s[0:1], 0, v164
	v_fma_f32 v5, -v3, v4, 1.0
	v_fmac_f32_e32 v4, v5, v4
	v_div_scale_f32 v5, vcc, 1.0, v2, 1.0
	v_mul_f32_e32 v6, v5, v4
	v_fma_f32 v7, -v3, v6, v5
	v_fmac_f32_e32 v6, v7, v4
	v_fma_f32 v3, -v3, v6, v5
	v_div_fmas_f32 v3, v3, v4, v6
	v_div_fixup_f32 v2, v3, v2, 1.0
	v_add_f32_dpp v5, v159, v159 quad_perm:[1,0,3,2] row_mask:0xf bank_mask:0xf bound_ctrl:1
	v_mul_f32_e32 v3, v163, v2
	v_mov_b32_e32 v6, 0
	v_add_f32_dpp v5, v5, v5 quad_perm:[2,3,0,1] row_mask:0xf bank_mask:0xf bound_ctrl:1
	v_mov_b32_e32 v4, 0
	v_lshl_add_u32 v2, v94, 2, s20
	v_mul_f32_e32 v3, 0x3c010204, v3
	v_mov_b32_dpp v6, v5 row_half_mirror row_mask:0xf bank_mask:0xf
	s_and_saveexec_b64 s[2:3], s[0:1]
	s_cbranch_execz .LBB0_3275
	v_add_f32_e32 v5, v5, v6
	v_mul_f32_e32 v5, v3, v5
	s_mov_b32 s39, 0x3e6d3388
	v_mul_f32_e32 v6, v5, v5
	s_waitcnt lgkmcnt(0)
	v_fma_f32 v7, |v5|, s39, 1.0
	v_rcp_f32_e32 v7, v7
	v_mov_b32_e32 v10, 0xbf3a00e3
	v_mul_f32_e32 v6, 0xbf38aa3b, v6
	v_exp_f32_e32 v6, v6
	v_fmac_f32_e32 v10, 0x3f07dc22, v7
	v_fmaak_f32 v10, v7, v10, 0x3f35f0e3
	v_fmaak_f32 v10, v7, v10, 0xbe11a98e
	v_fmaak_f32 v10, v7, v10, 0x3e027906
	v_mul_f32_e32 v7, v7, v10
	v_mul_f32_e32 v6, v6, v7
	v_mul_f32_e32 v7, v5, v6
	v_fma_f32 v6, -v5, v6, v5
	v_cmp_gt_f32_e32 vcc, 0, v5
	s_nop 1
	v_cndmask_b32_e32 v5, v6, v7, vcc
	s_waitcnt vmcnt(1)
	v_mul_f32_e32 v5, v5, v40
	s_waitcnt vmcnt(0)
	v_mul_f32_e32 v5, v5, v60
	ds_write_b32 v2, v5
.LBB0_3275:
	s_or_b64 exec, exec, s[2:3]
	v_add_f32_dpp v5, v158, v158 quad_perm:[1,0,3,2] row_mask:0xf bank_mask:0xf bound_ctrl:1
	s_nop 1
	v_add_f32_dpp v5, v5, v5 quad_perm:[2,3,0,1] row_mask:0xf bank_mask:0xf bound_ctrl:1
	s_nop 1
	v_mov_b32_dpp v4, v5 row_half_mirror row_mask:0xf bank_mask:0xf
	s_and_saveexec_b64 s[2:3], s[0:1]
	s_cbranch_execz .LBB0_3277
	v_add_f32_e32 v4, v5, v4
	v_mul_f32_e32 v4, v3, v4
	s_mov_b32 s39, 0x3e6d3388
	v_mul_f32_e32 v5, v4, v4
	s_waitcnt lgkmcnt(0)
	v_fma_f32 v6, |v4|, s39, 1.0
	v_rcp_f32_e32 v6, v6
	v_mov_b32_e32 v9, 0xbf3a00e3
	v_mul_f32_e32 v5, 0xbf38aa3b, v5
	v_exp_f32_e32 v5, v5
	v_fmac_f32_e32 v9, 0x3f07dc22, v6
	v_fmaak_f32 v9, v6, v9, 0x3f35f0e3
	v_fmaak_f32 v9, v6, v9, 0xbe11a98e
	v_fmaak_f32 v9, v6, v9, 0x3e027906
	v_mul_f32_e32 v6, v6, v9
	v_mul_f32_e32 v5, v5, v6
	v_mul_f32_e32 v6, v4, v5
	v_fma_f32 v5, -v4, v5, v4
	v_cmp_gt_f32_e32 vcc, 0, v4
	s_nop 1
	v_cndmask_b32_e32 v4, v5, v6, vcc
	s_waitcnt vmcnt(1)
	v_mul_f32_e32 v4, v4, v41
	s_waitcnt vmcnt(0)
	v_mul_f32_e32 v4, v4, v61
	ds_write_b32 v2, v4 offset:32
; __device__ __forceinline__ float gelu_erf(float v) {
;     const float av = fabsf(v), tt = __builtin_amdgcn_rcpf(av * 0.2316418882f + 1.0f);
;     float q = tt * 0.5307027145f + (-0.7265760135f); q = q * tt + 0.7107068705f; q = q * tt + (-0.142248368f); q = q * tt + 0.127414796f; q = q * tt;
;     const float e = __builtin_amdgcn_exp2f((v * v) * (-0.72134752044f));
;     const float m = v * (q * e); return v < 0.f ? m : v - m;
; }
; __device__ __forceinline__ void p12_peer(Frame& F) {
;     ...
; #pragma unroll
;     for (int i = 0; i < 4; ++i) { const int t = F.gw + i * F.NGW;
; #pragma unroll
;         for (int b = 0; b < 16; ++b) { float d = psum[i][b];
;             d += __builtin_bit_cast(float, __builtin_amdgcn_update_dpp(0, __builtin_bit_cast(int, d), 0xB1, 0xF, 0xF, false));
;             d += __builtin_bit_cast(float, __builtin_amdgcn_update_dpp(0, __builtin_bit_cast(int, d), 0x4E, 0xF, 0xF, false));
;             d += __builtin_bit_cast(float, __builtin_amdgcn_update_dpp(0, __builtin_bit_cast(int, d), 0x141, 0xF, 0xF, false));
;             const int idx = b * 8 + g8; const float w = PGT[(size_t)t * 128 + idx] * gelu_erf(sx[i] * d) * VSC[EL[i * 128 + idx]];
;             if (k8 == 0) WL[i * 128 + idx] = w; } }
.LBB0_3277:
	s_or_b64 exec, exec, s[2:3]
	v_add_f32_dpp v5, v157, v157 quad_perm:[1,0,3,2] row_mask:0xf bank_mask:0xf bound_ctrl:1
	v_mov_b32_e32 v6, 0
	v_mov_b32_e32 v4, 0
	v_add_f32_dpp v5, v5, v5 quad_perm:[2,3,0,1] row_mask:0xf bank_mask:0xf bound_ctrl:1
	s_nop 1
	v_mov_b32_dpp v6, v5 row_half_mirror row_mask:0xf bank_mask:0xf
	s_and_saveexec_b64 s[2:3], s[0:1]
	s_cbranch_execz .LBB0_3279
	v_add_f32_e32 v5, v5, v6
	v_mul_f32_e32 v5, v3, v5
	s_mov_b32 s39, 0x3e6d3388
	v_mul_f32_e32 v6, v5, v5
	s_waitcnt lgkmcnt(0)
	v_fma_f32 v7, |v5|, s39, 1.0
	v_rcp_f32_e32 v7, v7
	v_mov_b32_e32 v10, 0xbf3a00e3
	v_mul_f32_e32 v6, 0xbf38aa3b, v6
	v_exp_f32_e32 v6, v6
	v_fmac_f32_e32 v10, 0x3f07dc22, v7
	v_fmaak_f32 v10, v7, v10, 0x3f35f0e3
	v_fmaak_f32 v10, v7, v10, 0xbe11a98e
	v_fmaak_f32 v10, v7, v10, 0x3e027906
	v_mul_f32_e32 v7, v7, v10
	v_mul_f32_e32 v6, v6, v7
	v_mul_f32_e32 v7, v5, v6
	v_fma_f32 v6, -v5, v6, v5
	v_cmp_gt_f32_e32 vcc, 0, v5
	s_nop 1
	v_cndmask_b32_e32 v5, v6, v7, vcc
	s_waitcnt vmcnt(1)
	v_mul_f32_e32 v5, v5, v42
	s_waitcnt vmcnt(0)
	v_mul_f32_e32 v5, v5, v62
	ds_write_b32 v2, v5 offset:64
.LBB0_3279:
	s_or_b64 exec, exec, s[2:3]
	v_add_f32_dpp v5, v156, v156 quad_perm:[1,0,3,2] row_mask:0xf bank_mask:0xf bound_ctrl:1
	s_nop 1
	v_add_f32_dpp v5, v5, v5 quad_perm:[2,3,0,1] row_mask:0xf bank_mask:0xf bound_ctrl:1
	s_nop 1
	v_mov_b32_dpp v4, v5 row_half_mirror row_mask:0xf bank_mask:0xf
	s_and_saveexec_b64 s[2:3], s[0:1]
	s_cbranch_execz .LBB0_3281
	v_add_f32_e32 v4, v5, v4
	v_mul_f32_e32 v4, v3, v4
	s_mov_b32 s39, 0x3e6d3388
	v_mul_f32_e32 v5, v4, v4
	s_waitcnt lgkmcnt(0)
	v_fma_f32 v6, |v4|, s39, 1.0
	v_rcp_f32_e32 v6, v6
	v_mov_b32_e32 v9, 0xbf3a00e3
	v_mul_f32_e32 v5, 0xbf38aa3b, v5
	v_exp_f32_e32 v5, v5
	v_fmac_f32_e32 v9, 0x3f07dc22, v6
	v_fmaak_f32 v9, v6, v9, 0x3f35f0e3
	v_fmaak_f32 v9, v6, v9, 0xbe11a98e
	v_fmaak_f32 v9, v6, v9, 0x3e027906
	v_mul_f32_e32 v6, v6, v9
	v_mul_f32_e32 v5, v5, v6
	v_mul_f32_e32 v6, v4, v5
	v_fma_f32 v5, -v4, v5, v4
	v_cmp_gt_f32_e32 vcc, 0, v4
	s_nop 1
	v_cndmask_b32_e32 v4, v5, v6, vcc
	s_waitcnt vmcnt(1)
	v_mul_f32_e32 v4, v4, v43
	s_waitcnt vmcnt(0)
	v_mul_f32_e32 v4, v4, v63
	ds_write_b32 v2, v4 offset:96
.LBB0_3281:
	s_or_b64 exec, exec, s[2:3]
	v_add_f32_dpp v5, v155, v155 quad_perm:[1,0,3,2] row_mask:0xf bank_mask:0xf bound_ctrl:1
	v_mov_b32_e32 v6, 0
	v_mov_b32_e32 v4, 0
	v_add_f32_dpp v5, v5, v5 quad_perm:[2,3,0,1] row_mask:0xf bank_mask:0xf bound_ctrl:1
	s_nop 1
	v_mov_b32_dpp v6, v5 row_half_mirror row_mask:0xf bank_mask:0xf
	s_and_saveexec_b64 s[2:3], s[0:1]
	s_cbranch_execz .LBB0_3283
	v_add_f32_e32 v5, v5, v6
	v_mul_f32_e32 v5, v3, v5
	s_mov_b32 s39, 0x3e6d3388
	v_mul_f32_e32 v6, v5, v5
	s_waitcnt lgkmcnt(0)
	v_fma_f32 v7, |v5|, s39, 1.0
	v_rcp_f32_e32 v7, v7
	v_mov_b32_e32 v10, 0xbf3a00e3
	v_mul_f32_e32 v6, 0xbf38aa3b, v6
	v_exp_f32_e32 v6, v6
	v_fmac_f32_e32 v10, 0x3f07dc22, v7
	v_fmaak_f32 v10, v7, v10, 0x3f35f0e3
	v_fmaak_f32 v10, v7, v10, 0xbe11a98e
	v_fmaak_f32 v10, v7, v10, 0x3e027906
	v_mul_f32_e32 v7, v7, v10
	v_mul_f32_e32 v6, v6, v7
	v_mul_f32_e32 v7, v5, v6
	v_fma_f32 v6, -v5, v6, v5
	v_cmp_gt_f32_e32 vcc, 0, v5
	s_nop 1
	v_cndmask_b32_e32 v5, v6, v7, vcc
	s_waitcnt vmcnt(1)
	v_mul_f32_e32 v5, v5, v44
	s_waitcnt vmcnt(0)
	v_mul_f32_e32 v5, v5, v64
	ds_write_b32 v2, v5 offset:128
.LBB0_3283:
	s_or_b64 exec, exec, s[2:3]
	v_add_f32_dpp v5, v154, v154 quad_perm:[1,0,3,2] row_mask:0xf bank_mask:0xf bound_ctrl:1
	s_nop 1
	v_add_f32_dpp v5, v5, v5 quad_perm:[2,3,0,1] row_mask:0xf bank_mask:0xf bound_ctrl:1
	s_nop 1
	v_mov_b32_dpp v4, v5 row_half_mirror row_mask:0xf bank_mask:0xf
	s_and_saveexec_b64 s[2:3], s[0:1]
	s_cbranch_execz .LBB0_3285
	v_add_f32_e32 v4, v5, v4
	v_mul_f32_e32 v4, v3, v4
	s_mov_b32 s39, 0x3e6d3388
	v_mul_f32_e32 v5, v4, v4
	s_waitcnt lgkmcnt(0)
	v_fma_f32 v6, |v4|, s39, 1.0
	v_rcp_f32_e32 v6, v6
	v_mov_b32_e32 v9, 0xbf3a00e3
	v_mul_f32_e32 v5, 0xbf38aa3b, v5
	v_exp_f32_e32 v5, v5
	v_fmac_f32_e32 v9, 0x3f07dc22, v6
	v_fmaak_f32 v9, v6, v9, 0x3f35f0e3
	v_fmaak_f32 v9, v6, v9, 0xbe11a98e
	v_fmaak_f32 v9, v6, v9, 0x3e027906
	v_mul_f32_e32 v6, v6, v9
	v_mul_f32_e32 v5, v5, v6
	v_mul_f32_e32 v6, v4, v5
	v_fma_f32 v5, -v4, v5, v4
	v_cmp_gt_f32_e32 vcc, 0, v4
	s_nop 1
	v_cndmask_b32_e32 v4, v5, v6, vcc
	s_waitcnt vmcnt(1)
	v_mul_f32_e32 v4, v4, v45
	s_waitcnt vmcnt(0)
	v_mul_f32_e32 v4, v4, v65
	ds_write_b32 v2, v4 offset:160
.LBB0_3285:
	s_or_b64 exec, exec, s[2:3]
	v_add_f32_dpp v5, v153, v153 quad_perm:[1,0,3,2] row_mask:0xf bank_mask:0xf bound_ctrl:1
	v_mov_b32_e32 v6, 0
	v_mov_b32_e32 v4, 0
	v_add_f32_dpp v5, v5, v5 quad_perm:[2,3,0,1] row_mask:0xf bank_mask:0xf bound_ctrl:1
	s_nop 1
	v_mov_b32_dpp v6, v5 row_half_mirror row_mask:0xf bank_mask:0xf
	s_and_saveexec_b64 s[2:3], s[0:1]
	s_cbranch_execz .LBB0_3287
	v_add_f32_e32 v5, v5, v6
	v_mul_f32_e32 v5, v3, v5
	s_mov_b32 s39, 0x3e6d3388
	v_mul_f32_e32 v6, v5, v5
	s_waitcnt lgkmcnt(0)
	v_fma_f32 v7, |v5|, s39, 1.0
	v_rcp_f32_e32 v7, v7
	v_mov_b32_e32 v10, 0xbf3a00e3
	v_mul_f32_e32 v6, 0xbf38aa3b, v6
	v_exp_f32_e32 v6, v6
	v_fmac_f32_e32 v10, 0x3f07dc22, v7
	v_fmaak_f32 v10, v7, v10, 0x3f35f0e3
	v_fmaak_f32 v10, v7, v10, 0xbe11a98e
	v_fmaak_f32 v10, v7, v10, 0x3e027906
	v_mul_f32_e32 v7, v7, v10
	v_mul_f32_e32 v6, v6, v7
	v_mul_f32_e32 v7, v5, v6
	v_fma_f32 v6, -v5, v6, v5
	v_cmp_gt_f32_e32 vcc, 0, v5
	s_nop 1
	v_cndmask_b32_e32 v5, v6, v7, vcc
	s_waitcnt vmcnt(1)
	v_mul_f32_e32 v5, v5, v46
	s_waitcnt vmcnt(0)
	v_mul_f32_e32 v5, v5, v66
	ds_write_b32 v2, v5 offset:192
; __device__ __forceinline__ float gelu_erf(float v) {
;     const float av = fabsf(v), tt = __builtin_amdgcn_rcpf(av * 0.2316418882f + 1.0f);
;     float q = tt * 0.5307027145f + (-0.7265760135f); q = q * tt + 0.7107068705f; q = q * tt + (-0.142248368f); q = q * tt + 0.127414796f; q = q * tt;
;     const float e = __builtin_amdgcn_exp2f((v * v) * (-0.72134752044f));
;     const float m = v * (q * e); return v < 0.f ? m : v - m;
; }
; __device__ __forceinline__ void p12_peer(Frame& F) {
;     ...
; #pragma unroll
;     for (int i = 0; i < 4; ++i) { const int t = F.gw + i * F.NGW;
; #pragma unroll
;         for (int b = 0; b < 16; ++b) { float d = psum[i][b];
;             d += __builtin_bit_cast(float, __builtin_amdgcn_update_dpp(0, __builtin_bit_cast(int, d), 0xB1, 0xF, 0xF, false));
;             d += __builtin_bit_cast(float, __builtin_amdgcn_update_dpp(0, __builtin_bit_cast(int, d), 0x4E, 0xF, 0xF, false));
;             d += __builtin_bit_cast(float, __builtin_amdgcn_update_dpp(0, __builtin_bit_cast(int, d), 0x141, 0xF, 0xF, false));
;             const int idx = b * 8 + g8; const float w = PGT[(size_t)t * 128 + idx] * gelu_erf(sx[i] * d) * VSC[EL[i * 128 + idx]];
;             if (k8 == 0) WL[i * 128 + idx] = w; } }
.LBB0_3287:
	s_or_b64 exec, exec, s[2:3]
	v_add_f32_dpp v5, v152, v152 quad_perm:[1,0,3,2] row_mask:0xf bank_mask:0xf bound_ctrl:1
	s_nop 1
	v_add_f32_dpp v5, v5, v5 quad_perm:[2,3,0,1] row_mask:0xf bank_mask:0xf bound_ctrl:1
	s_nop 1
	v_mov_b32_dpp v4, v5 row_half_mirror row_mask:0xf bank_mask:0xf
	s_and_saveexec_b64 s[2:3], s[0:1]
	s_cbranch_execz .LBB0_3289
	v_add_f32_e32 v4, v5, v4
	v_mul_f32_e32 v4, v3, v4
	s_mov_b32 s39, 0x3e6d3388
	v_mul_f32_e32 v5, v4, v4
	s_waitcnt lgkmcnt(0)
	v_fma_f32 v6, |v4|, s39, 1.0
	v_rcp_f32_e32 v6, v6
	v_mov_b32_e32 v9, 0xbf3a00e3
	v_mul_f32_e32 v5, 0xbf38aa3b, v5
	v_exp_f32_e32 v5, v5
	v_fmac_f32_e32 v9, 0x3f07dc22, v6
	v_fmaak_f32 v9, v6, v9, 0x3f35f0e3
	v_fmaak_f32 v9, v6, v9, 0xbe11a98e
	v_fmaak_f32 v9, v6, v9, 0x3e027906
	v_mul_f32_e32 v6, v6, v9
	v_mul_f32_e32 v5, v5, v6
	v_mul_f32_e32 v6, v4, v5
	v_fma_f32 v5, -v4, v5, v4
	v_cmp_gt_f32_e32 vcc, 0, v4
	s_nop 1
	v_cndmask_b32_e32 v4, v5, v6, vcc
	s_waitcnt vmcnt(1)
	v_mul_f32_e32 v4, v4, v47
	s_waitcnt vmcnt(0)
	v_mul_f32_e32 v4, v4, v67
	ds_write_b32 v2, v4 offset:224
.LBB0_3289:
	s_or_b64 exec, exec, s[2:3]
	v_add_f32_dpp v5, v151, v151 quad_perm:[1,0,3,2] row_mask:0xf bank_mask:0xf bound_ctrl:1
	v_mov_b32_e32 v6, 0
	v_mov_b32_e32 v4, 0
	v_add_f32_dpp v5, v5, v5 quad_perm:[2,3,0,1] row_mask:0xf bank_mask:0xf bound_ctrl:1
	s_nop 1
	v_mov_b32_dpp v6, v5 row_half_mirror row_mask:0xf bank_mask:0xf
	s_and_saveexec_b64 s[2:3], s[0:1]
	s_cbranch_execz .LBB0_3291
	v_add_f32_e32 v5, v5, v6
	v_mul_f32_e32 v5, v3, v5
	s_mov_b32 s39, 0x3e6d3388
	v_mul_f32_e32 v6, v5, v5
	s_waitcnt lgkmcnt(0)
	v_fma_f32 v7, |v5|, s39, 1.0
	v_rcp_f32_e32 v7, v7
	v_mov_b32_e32 v10, 0xbf3a00e3
	v_mul_f32_e32 v6, 0xbf38aa3b, v6
	v_exp_f32_e32 v6, v6
	v_fmac_f32_e32 v10, 0x3f07dc22, v7
	v_fmaak_f32 v10, v7, v10, 0x3f35f0e3
	v_fmaak_f32 v10, v7, v10, 0xbe11a98e
	v_fmaak_f32 v10, v7, v10, 0x3e027906
	v_mul_f32_e32 v7, v7, v10
	v_mul_f32_e32 v6, v6, v7
	v_mul_f32_e32 v7, v5, v6
	v_fma_f32 v6, -v5, v6, v5
	v_cmp_gt_f32_e32 vcc, 0, v5
	s_nop 1
	v_cndmask_b32_e32 v5, v6, v7, vcc
	s_waitcnt vmcnt(1)
	v_mul_f32_e32 v5, v5, v48
	s_waitcnt vmcnt(0)
	v_mul_f32_e32 v5, v5, v68
	ds_write_b32 v2, v5 offset:256
.LBB0_3291:
	s_or_b64 exec, exec, s[2:3]
	v_add_f32_dpp v5, v150, v150 quad_perm:[1,0,3,2] row_mask:0xf bank_mask:0xf bound_ctrl:1
	s_nop 1
	v_add_f32_dpp v5, v5, v5 quad_perm:[2,3,0,1] row_mask:0xf bank_mask:0xf bound_ctrl:1
	s_nop 1
	v_mov_b32_dpp v4, v5 row_half_mirror row_mask:0xf bank_mask:0xf
	s_and_saveexec_b64 s[2:3], s[0:1]
	s_cbranch_execz .LBB0_3293
	v_add_f32_e32 v4, v5, v4
	v_mul_f32_e32 v4, v3, v4
	s_mov_b32 s39, 0x3e6d3388
	v_mul_f32_e32 v5, v4, v4
	s_waitcnt lgkmcnt(0)
	v_fma_f32 v6, |v4|, s39, 1.0
	v_rcp_f32_e32 v6, v6
	v_mov_b32_e32 v9, 0xbf3a00e3
	v_mul_f32_e32 v5, 0xbf38aa3b, v5
	v_exp_f32_e32 v5, v5
	v_fmac_f32_e32 v9, 0x3f07dc22, v6
	v_fmaak_f32 v9, v6, v9, 0x3f35f0e3
	v_fmaak_f32 v9, v6, v9, 0xbe11a98e
	v_fmaak_f32 v9, v6, v9, 0x3e027906
	v_mul_f32_e32 v6, v6, v9
	v_mul_f32_e32 v5, v5, v6
	v_mul_f32_e32 v6, v4, v5
	v_fma_f32 v5, -v4, v5, v4
	v_cmp_gt_f32_e32 vcc, 0, v4
	s_nop 1
	v_cndmask_b32_e32 v4, v5, v6, vcc
	s_waitcnt vmcnt(1)
	v_mul_f32_e32 v4, v4, v49
	s_waitcnt vmcnt(0)
	v_mul_f32_e32 v4, v4, v69
	ds_write_b32 v2, v4 offset:288
.LBB0_3293:
	s_or_b64 exec, exec, s[2:3]
	v_add_f32_dpp v5, v149, v149 quad_perm:[1,0,3,2] row_mask:0xf bank_mask:0xf bound_ctrl:1
	v_mov_b32_e32 v6, 0
	v_mov_b32_e32 v4, 0
	v_add_f32_dpp v5, v5, v5 quad_perm:[2,3,0,1] row_mask:0xf bank_mask:0xf bound_ctrl:1
	s_nop 1
	v_mov_b32_dpp v6, v5 row_half_mirror row_mask:0xf bank_mask:0xf
	s_and_saveexec_b64 s[2:3], s[0:1]
	s_cbranch_execz .LBB0_3295
	v_add_f32_e32 v5, v5, v6
	v_mul_f32_e32 v5, v3, v5
	s_mov_b32 s39, 0x3e6d3388
	v_mul_f32_e32 v6, v5, v5
	s_waitcnt lgkmcnt(0)
	v_fma_f32 v7, |v5|, s39, 1.0
	v_rcp_f32_e32 v7, v7
	v_mov_b32_e32 v10, 0xbf3a00e3
	v_mul_f32_e32 v6, 0xbf38aa3b, v6
	v_exp_f32_e32 v6, v6
	v_fmac_f32_e32 v10, 0x3f07dc22, v7
	v_fmaak_f32 v10, v7, v10, 0x3f35f0e3
	v_fmaak_f32 v10, v7, v10, 0xbe11a98e
	v_fmaak_f32 v10, v7, v10, 0x3e027906
	v_mul_f32_e32 v7, v7, v10
	v_mul_f32_e32 v6, v6, v7
	v_mul_f32_e32 v7, v5, v6
	v_fma_f32 v6, -v5, v6, v5
	v_cmp_gt_f32_e32 vcc, 0, v5
	s_nop 1
	v_cndmask_b32_e32 v5, v6, v7, vcc
	s_waitcnt vmcnt(1)
	v_mul_f32_e32 v5, v5, v50
	s_waitcnt vmcnt(0)
	v_mul_f32_e32 v5, v5, v70
	ds_write_b32 v2, v5 offset:320
.LBB0_3295:
	s_or_b64 exec, exec, s[2:3]
	v_add_f32_dpp v5, v148, v148 quad_perm:[1,0,3,2] row_mask:0xf bank_mask:0xf bound_ctrl:1
	s_nop 1
	v_add_f32_dpp v5, v5, v5 quad_perm:[2,3,0,1] row_mask:0xf bank_mask:0xf bound_ctrl:1
	s_nop 1
	v_mov_b32_dpp v4, v5 row_half_mirror row_mask:0xf bank_mask:0xf
	s_and_saveexec_b64 s[2:3], s[0:1]
	s_cbranch_execz .LBB0_3297
	v_add_f32_e32 v4, v5, v4
	v_mul_f32_e32 v4, v3, v4
	s_mov_b32 s39, 0x3e6d3388
	v_mul_f32_e32 v5, v4, v4
	s_waitcnt lgkmcnt(0)
	v_fma_f32 v6, |v4|, s39, 1.0
	v_rcp_f32_e32 v6, v6
	v_mov_b32_e32 v9, 0xbf3a00e3
	v_mul_f32_e32 v5, 0xbf38aa3b, v5
	v_exp_f32_e32 v5, v5
	v_fmac_f32_e32 v9, 0x3f07dc22, v6
	v_fmaak_f32 v9, v6, v9, 0x3f35f0e3
	v_fmaak_f32 v9, v6, v9, 0xbe11a98e
	v_fmaak_f32 v9, v6, v9, 0x3e027906
	v_mul_f32_e32 v6, v6, v9
	v_mul_f32_e32 v5, v5, v6
	v_mul_f32_e32 v6, v4, v5
	v_fma_f32 v5, -v4, v5, v4
	v_cmp_gt_f32_e32 vcc, 0, v4
	s_nop 1
	v_cndmask_b32_e32 v4, v5, v6, vcc
	s_waitcnt vmcnt(1)
	v_mul_f32_e32 v4, v4, v51
	s_waitcnt vmcnt(0)
	v_mul_f32_e32 v4, v4, v71
	ds_write_b32 v2, v4 offset:352
; __device__ __forceinline__ float gelu_erf(float v) {
;     const float av = fabsf(v), tt = __builtin_amdgcn_rcpf(av * 0.2316418882f + 1.0f);
;     float q = tt * 0.5307027145f + (-0.7265760135f); q = q * tt + 0.7107068705f; q = q * tt + (-0.142248368f); q = q * tt + 0.127414796f; q = q * tt;
;     const float e = __builtin_amdgcn_exp2f((v * v) * (-0.72134752044f));
;     const float m = v * (q * e); return v < 0.f ? m : v - m;
; }
; __device__ __forceinline__ void p12_peer(Frame& F) {
;     ...
; #pragma unroll
;     for (int i = 0; i < 4; ++i) { const int t = F.gw + i * F.NGW;
; #pragma unroll
;         for (int b = 0; b < 16; ++b) { float d = psum[i][b];
;             d += __builtin_bit_cast(float, __builtin_amdgcn_update_dpp(0, __builtin_bit_cast(int, d), 0xB1, 0xF, 0xF, false));
;             d += __builtin_bit_cast(float, __builtin_amdgcn_update_dpp(0, __builtin_bit_cast(int, d), 0x4E, 0xF, 0xF, false));
;             d += __builtin_bit_cast(float, __builtin_amdgcn_update_dpp(0, __builtin_bit_cast(int, d), 0x141, 0xF, 0xF, false));
;             const int idx = b * 8 + g8; const float w = PGT[(size_t)t * 128 + idx] * gelu_erf(sx[i] * d) * VSC[EL[i * 128 + idx]];
;             if (k8 == 0) WL[i * 128 + idx] = w; } }
.LBB0_3297:
	s_or_b64 exec, exec, s[2:3]
	v_add_f32_dpp v5, v147, v147 quad_perm:[1,0,3,2] row_mask:0xf bank_mask:0xf bound_ctrl:1
	v_mov_b32_e32 v6, 0
	v_mov_b32_e32 v4, 0
	v_add_f32_dpp v5, v5, v5 quad_perm:[2,3,0,1] row_mask:0xf bank_mask:0xf bound_ctrl:1
	s_nop 1
	v_mov_b32_dpp v6, v5 row_half_mirror row_mask:0xf bank_mask:0xf
	s_and_saveexec_b64 s[2:3], s[0:1]
	s_cbranch_execz .LBB0_3299
	v_add_f32_e32 v5, v5, v6
	v_mul_f32_e32 v5, v3, v5
	s_mov_b32 s39, 0x3e6d3388
	v_mul_f32_e32 v6, v5, v5
	s_waitcnt lgkmcnt(0)
	v_fma_f32 v7, |v5|, s39, 1.0
	v_rcp_f32_e32 v7, v7
	v_mov_b32_e32 v10, 0xbf3a00e3
	v_mul_f32_e32 v6, 0xbf38aa3b, v6
	v_exp_f32_e32 v6, v6
	v_fmac_f32_e32 v10, 0x3f07dc22, v7
	v_fmaak_f32 v10, v7, v10, 0x3f35f0e3
	v_fmaak_f32 v10, v7, v10, 0xbe11a98e
	v_fmaak_f32 v10, v7, v10, 0x3e027906
	v_mul_f32_e32 v7, v7, v10
	v_mul_f32_e32 v6, v6, v7
	v_mul_f32_e32 v7, v5, v6
	v_fma_f32 v6, -v5, v6, v5
	v_cmp_gt_f32_e32 vcc, 0, v5
	s_nop 1
	v_cndmask_b32_e32 v5, v6, v7, vcc
	s_waitcnt vmcnt(1)
	v_mul_f32_e32 v5, v5, v52
	s_waitcnt vmcnt(0)
	v_mul_f32_e32 v5, v5, v72
	ds_write_b32 v2, v5 offset:384
.LBB0_3299:
	s_or_b64 exec, exec, s[2:3]
	v_add_f32_dpp v5, v146, v146 quad_perm:[1,0,3,2] row_mask:0xf bank_mask:0xf bound_ctrl:1
	s_nop 1
	v_add_f32_dpp v5, v5, v5 quad_perm:[2,3,0,1] row_mask:0xf bank_mask:0xf bound_ctrl:1
	s_nop 1
	v_mov_b32_dpp v4, v5 row_half_mirror row_mask:0xf bank_mask:0xf
	s_and_saveexec_b64 s[2:3], s[0:1]
	s_cbranch_execz .LBB0_3301
	v_add_f32_e32 v4, v5, v4
	v_mul_f32_e32 v4, v3, v4
	s_mov_b32 s39, 0x3e6d3388
	v_mul_f32_e32 v5, v4, v4
	s_waitcnt lgkmcnt(0)
	v_fma_f32 v6, |v4|, s39, 1.0
	v_rcp_f32_e32 v6, v6
	v_mov_b32_e32 v9, 0xbf3a00e3
	v_mul_f32_e32 v5, 0xbf38aa3b, v5
	v_exp_f32_e32 v5, v5
	v_fmac_f32_e32 v9, 0x3f07dc22, v6
	v_fmaak_f32 v9, v6, v9, 0x3f35f0e3
	v_fmaak_f32 v9, v6, v9, 0xbe11a98e
	v_fmaak_f32 v9, v6, v9, 0x3e027906
	v_mul_f32_e32 v6, v6, v9
	v_mul_f32_e32 v5, v5, v6
	v_mul_f32_e32 v6, v4, v5
	v_fma_f32 v5, -v4, v5, v4
	v_cmp_gt_f32_e32 vcc, 0, v4
	s_nop 1
	v_cndmask_b32_e32 v4, v5, v6, vcc
	s_waitcnt vmcnt(1)
	v_mul_f32_e32 v4, v4, v53
	s_waitcnt vmcnt(0)
	v_mul_f32_e32 v4, v4, v73
	ds_write_b32 v2, v4 offset:416
.LBB0_3301:
	s_or_b64 exec, exec, s[2:3]
	v_add_f32_dpp v5, v145, v145 quad_perm:[1,0,3,2] row_mask:0xf bank_mask:0xf bound_ctrl:1
	v_mov_b32_e32 v6, 0
	v_mov_b32_e32 v4, 0
	v_add_f32_dpp v5, v5, v5 quad_perm:[2,3,0,1] row_mask:0xf bank_mask:0xf bound_ctrl:1
	s_nop 1
	v_mov_b32_dpp v6, v5 row_half_mirror row_mask:0xf bank_mask:0xf
	s_and_saveexec_b64 s[2:3], s[0:1]
	s_cbranch_execz .LBB0_3303
	v_add_f32_e32 v5, v5, v6
	v_mul_f32_e32 v5, v3, v5
	s_mov_b32 s39, 0x3e6d3388
	v_mul_f32_e32 v6, v5, v5
	s_waitcnt lgkmcnt(0)
	v_fma_f32 v7, |v5|, s39, 1.0
	v_rcp_f32_e32 v7, v7
	v_mov_b32_e32 v10, 0xbf3a00e3
	v_mul_f32_e32 v6, 0xbf38aa3b, v6
	v_exp_f32_e32 v6, v6
	v_fmac_f32_e32 v10, 0x3f07dc22, v7
	v_fmaak_f32 v10, v7, v10, 0x3f35f0e3
	v_fmaak_f32 v10, v7, v10, 0xbe11a98e
	v_fmaak_f32 v10, v7, v10, 0x3e027906
	v_mul_f32_e32 v7, v7, v10
	v_mul_f32_e32 v6, v6, v7
	v_mul_f32_e32 v7, v5, v6
	v_fma_f32 v6, -v5, v6, v5
	v_cmp_gt_f32_e32 vcc, 0, v5
	s_nop 1
	v_cndmask_b32_e32 v5, v6, v7, vcc
	s_waitcnt vmcnt(1)
	v_mul_f32_e32 v5, v5, v54
	s_waitcnt vmcnt(0)
	v_mul_f32_e32 v5, v5, v74
	ds_write_b32 v2, v5 offset:448
.LBB0_3303:
	s_or_b64 exec, exec, s[2:3]
	v_add_f32_dpp v5, v144, v144 quad_perm:[1,0,3,2] row_mask:0xf bank_mask:0xf bound_ctrl:1
	s_nop 1
	v_add_f32_dpp v5, v5, v5 quad_perm:[2,3,0,1] row_mask:0xf bank_mask:0xf bound_ctrl:1
	s_nop 1
	v_mov_b32_dpp v4, v5 row_half_mirror row_mask:0xf bank_mask:0xf
	s_and_saveexec_b64 s[2:3], s[0:1]
	s_cbranch_execz .LBB0_3305
	s_mov_b32 s39, 0x3e6d3388
	s_waitcnt lgkmcnt(0)
	v_add_f32_e32 v0, v5, v4
	v_mul_f32_e32 v0, v3, v0
	v_fma_f32 v3, |v0|, s39, 1.0
	v_rcp_f32_e32 v3, v3
	v_mul_f32_e32 v1, v0, v0
	v_mov_b32_e32 v4, 0xbf3a00e3
	v_mul_f32_e32 v1, 0xbf38aa3b, v1
	v_fmac_f32_e32 v4, 0x3f07dc22, v3
	v_exp_f32_e32 v1, v1
	v_fmaak_f32 v4, v3, v4, 0x3f35f0e3
	v_fmaak_f32 v4, v3, v4, 0xbe11a98e
	v_fmaak_f32 v4, v3, v4, 0x3e027906
	v_mul_f32_e32 v3, v3, v4
	v_mul_f32_e32 v1, v1, v3
	v_mul_f32_e32 v3, v0, v1
	v_fma_f32 v1, -v0, v1, v0
	v_cmp_gt_f32_e32 vcc, 0, v0
	s_nop 1
	v_cndmask_b32_e32 v0, v1, v3, vcc
	s_waitcnt vmcnt(1)
	v_mul_f32_e32 v0, v0, v55
	s_waitcnt vmcnt(0)
	v_mul_f32_e32 v0, v0, v75
	ds_write_b32 v2, v0 offset:480
; __device__ __forceinline__ float gelu_erf(float v) {
;     const float av = fabsf(v), tt = __builtin_amdgcn_rcpf(av * 0.2316418882f + 1.0f);
;     float q = tt * 0.5307027145f + (-0.7265760135f); q = q * tt + 0.7107068705f; q = q * tt + (-0.142248368f); q = q * tt + 0.127414796f; q = q * tt;
;     const float e = __builtin_amdgcn_exp2f((v * v) * (-0.72134752044f));
;     const float m = v * (q * e); return v < 0.f ? m : v - m;
; }
; __device__ __forceinline__ void p12_peer(Frame& F) {
;     ...
; #pragma unroll
;     for (int i = 0; i < 4; ++i) { const int t = F.gw + i * F.NGW;
; #pragma unroll
;         for (int b = 0; b < 16; ++b) { float d = psum[i][b];
;             d += __builtin_bit_cast(float, __builtin_amdgcn_update_dpp(0, __builtin_bit_cast(int, d), 0xB1, 0xF, 0xF, false));
;             d += __builtin_bit_cast(float, __builtin_amdgcn_update_dpp(0, __builtin_bit_cast(int, d), 0x4E, 0xF, 0xF, false));
;             d += __builtin_bit_cast(float, __builtin_amdgcn_update_dpp(0, __builtin_bit_cast(int, d), 0x141, 0xF, 0xF, false));
;             const int idx = b * 8 + g8; const float w = PGT[(size_t)t * 128 + idx] * gelu_erf(sx[i] * d) * VSC[EL[i * 128 + idx]];
;             if (k8 == 0) WL[i * 128 + idx] = w; } }
.LBB0_3305:
	s_or_b64 exec, exec, s[2:3]
	v_mov_b32_e32 v0, s37
	v_mov_b32_e32 v1, s38
	v_add_f32_e32 v0, s35, v0
	v_add_f32_e32 v1, s36, v1
	v_add_f32_e32 v0, v0, v1
	v_mov_b32_e32 v1, 0x358637bd
	v_fmac_f32_e32 v1, 0x39800000, v0
	s_mov_b32 s2, 0xf800000
	v_mul_f32_e32 v0, 0x4f800000, v1
	v_cmp_gt_f32_e32 vcc, s2, v1
	s_nop 1
	v_cndmask_b32_e32 v0, v1, v0, vcc
	v_sqrt_f32_e32 v1, v0
	s_nop 0
	v_add_u32_e32 v3, -1, v1
	v_fma_f32 v4, -v3, v1, v0
	v_cmp_ge_f32_e64 s[2:3], 0, v4
	v_add_u32_e32 v4, 1, v1
	s_nop 0
	v_cndmask_b32_e64 v3, v1, v3, s[2:3]
	v_fma_f32 v1, -v4, v1, v0
	v_cmp_lt_f32_e64 s[2:3], 0, v1
	s_nop 1
	v_cndmask_b32_e64 v1, v3, v4, s[2:3]
	v_mul_f32_e32 v3, 0x37800000, v1
	v_cndmask_b32_e32 v1, v1, v3, vcc
	v_mov_b32_e32 v3, 0x260
	v_cmp_class_f32_e32 vcc, v0, v3
	s_nop 1
	v_cndmask_b32_e32 v0, v1, v0, vcc
	v_div_scale_f32 v1, s[2:3], v0, v0, 1.0
	v_rcp_f32_e32 v3, v1
	s_add_u32 s2, s43, s16
	s_addc_u32 s3, s44, s17
	v_fma_f32 v4, -v1, v3, 1.0
	v_fmac_f32_e32 v3, v4, v3
	v_div_scale_f32 v4, vcc, 1.0, v0, 1.0
	v_mul_f32_e32 v5, v4, v3
	v_fma_f32 v6, -v1, v5, v4
	v_fmac_f32_e32 v5, v6, v3
	v_fma_f32 v1, -v1, v5, v4
	v_div_fmas_f32 v1, v1, v3, v5
	v_div_fixup_f32 v0, v1, v0, 1.0
	v_add_f32_dpp v5, v143, v143 quad_perm:[1,0,3,2] row_mask:0xf bank_mask:0xf bound_ctrl:1
	v_mul_f32_e32 v0, v162, v0
	v_mov_b32_e32 v6, 0
	v_add_f32_dpp v5, v5, v5 quad_perm:[2,3,0,1] row_mask:0xf bank_mask:0xf bound_ctrl:1
	v_mul_f32_e32 v3, 0x3c010204, v0
	v_lshl_add_u64 v[0:1], v[94:95], 2, s[2:3]
	ds_read_u16 v20, v93 offset:16640
	ds_read_u16 v21, v93 offset:16656
	ds_read_u16 v22, v93 offset:16672
	ds_read_u16 v23, v93 offset:16688
	ds_read_u16 v24, v93 offset:16704
	ds_read_u16 v25, v93 offset:16720
	ds_read_u16 v26, v93 offset:16736
	ds_read_u16 v27, v93 offset:16752
	s_waitcnt lgkmcnt(0)
	ds_read_u16 v28, v93 offset:16768
	ds_read_u16 v29, v93 offset:16784
	ds_read_u16 v30, v93 offset:16800
	ds_read_u16 v31, v93 offset:16816
	ds_read_u16 v32, v93 offset:16832
	ds_read_u16 v33, v93 offset:16848
	ds_read_u16 v34, v93 offset:16864
	ds_read_u16 v35, v93 offset:16880
	s_waitcnt lgkmcnt(0)
	v_lshlrev_b32_e32 v20, 2, v20
	v_lshlrev_b32_e32 v21, 2, v21
	v_lshlrev_b32_e32 v22, 2, v22
	v_lshlrev_b32_e32 v23, 2, v23
	v_lshlrev_b32_e32 v24, 2, v24
	v_lshlrev_b32_e32 v25, 2, v25
	v_lshlrev_b32_e32 v26, 2, v26
	v_lshlrev_b32_e32 v27, 2, v27
	v_lshlrev_b32_e32 v28, 2, v28
	v_lshlrev_b32_e32 v29, 2, v29
	v_lshlrev_b32_e32 v30, 2, v30
	v_lshlrev_b32_e32 v31, 2, v31
	v_lshlrev_b32_e32 v32, 2, v32
	v_lshlrev_b32_e32 v33, 2, v33
	v_lshlrev_b32_e32 v34, 2, v34
	v_lshlrev_b32_e32 v35, 2, v35
	global_load_dword v40, v[0:1], off offset:0
	global_load_dword v60, v20, s[18:19]
	global_load_dword v41, v[0:1], off offset:32
	global_load_dword v61, v21, s[18:19]
	global_load_dword v42, v[0:1], off offset:64
	global_load_dword v62, v22, s[18:19]
	global_load_dword v43, v[0:1], off offset:96
	global_load_dword v63, v23, s[18:19]
	global_load_dword v44, v[0:1], off offset:128
	global_load_dword v64, v24, s[18:19]
	global_load_dword v45, v[0:1], off offset:160
	global_load_dword v65, v25, s[18:19]
	global_load_dword v46, v[0:1], off offset:192
	global_load_dword v66, v26, s[18:19]
	global_load_dword v47, v[0:1], off offset:224
	global_load_dword v67, v27, s[18:19]
	global_load_dword v48, v[0:1], off offset:256
	global_load_dword v68, v28, s[18:19]
	global_load_dword v49, v[0:1], off offset:288
	global_load_dword v69, v29, s[18:19]
	global_load_dword v50, v[0:1], off offset:320
	global_load_dword v70, v30, s[18:19]
	global_load_dword v51, v[0:1], off offset:352
	global_load_dword v71, v31, s[18:19]
	global_load_dword v52, v[0:1], off offset:384
	global_load_dword v72, v32, s[18:19]
	global_load_dword v53, v[0:1], off offset:416
	global_load_dword v73, v33, s[18:19]
	global_load_dword v54, v[0:1], off offset:448
	global_load_dword v74, v34, s[18:19]
	global_load_dword v55, v[0:1], off offset:480
	global_load_dword v75, v35, s[18:19]
	s_waitcnt vmcnt(0)
	v_mov_b32_e32 v4, 0
	v_mov_b32_dpp v6, v5 row_half_mirror row_mask:0xf bank_mask:0xf
	s_and_saveexec_b64 s[2:3], s[0:1]
	s_cbranch_execz .LBB0_3307
	v_add_f32_e32 v5, v5, v6
	v_mul_f32_e32 v5, v3, v5
	s_mov_b32 s16, 0x3e6d3388
	v_mul_f32_e32 v6, v5, v5
	s_waitcnt lgkmcnt(0)
	v_fma_f32 v7, |v5|, s16, 1.0
	v_rcp_f32_e32 v7, v7
	v_mov_b32_e32 v10, 0xbf3a00e3
	v_mul_f32_e32 v6, 0xbf38aa3b, v6
	v_exp_f32_e32 v6, v6
	v_fmac_f32_e32 v10, 0x3f07dc22, v7
	v_fmaak_f32 v10, v7, v10, 0x3f35f0e3
	v_fmaak_f32 v10, v7, v10, 0xbe11a98e
	v_fmaak_f32 v10, v7, v10, 0x3e027906
	v_mul_f32_e32 v7, v7, v10
	v_mul_f32_e32 v6, v6, v7
	v_mul_f32_e32 v7, v5, v6
	v_fma_f32 v6, -v5, v6, v5
	v_cmp_gt_f32_e32 vcc, 0, v5
	s_nop 1
	v_cndmask_b32_e32 v5, v6, v7, vcc
	s_waitcnt vmcnt(1)
	v_mul_f32_e32 v5, v5, v40
	s_waitcnt vmcnt(0)
	v_mul_f32_e32 v5, v5, v60
	ds_write_b32 v2, v5 offset:512
.LBB0_3307:
	s_or_b64 exec, exec, s[2:3]
	v_add_f32_dpp v5, v142, v142 quad_perm:[1,0,3,2] row_mask:0xf bank_mask:0xf bound_ctrl:1
	s_nop 1
	v_add_f32_dpp v5, v5, v5 quad_perm:[2,3,0,1] row_mask:0xf bank_mask:0xf bound_ctrl:1
	s_nop 1
	v_mov_b32_dpp v4, v5 row_half_mirror row_mask:0xf bank_mask:0xf
	s_and_saveexec_b64 s[2:3], s[0:1]
	s_cbranch_execz .LBB0_3309
	v_add_f32_e32 v4, v5, v4
	v_mul_f32_e32 v4, v3, v4
	s_mov_b32 s16, 0x3e6d3388
	v_mul_f32_e32 v5, v4, v4
	s_waitcnt lgkmcnt(0)
	v_fma_f32 v6, |v4|, s16, 1.0
	v_rcp_f32_e32 v6, v6
	v_mov_b32_e32 v9, 0xbf3a00e3
	v_mul_f32_e32 v5, 0xbf38aa3b, v5
	v_exp_f32_e32 v5, v5
	v_fmac_f32_e32 v9, 0x3f07dc22, v6
	v_fmaak_f32 v9, v6, v9, 0x3f35f0e3
	v_fmaak_f32 v9, v6, v9, 0xbe11a98e
	v_fmaak_f32 v9, v6, v9, 0x3e027906
	v_mul_f32_e32 v6, v6, v9
	v_mul_f32_e32 v5, v5, v6
	v_mul_f32_e32 v6, v4, v5
	v_fma_f32 v5, -v4, v5, v4
	v_cmp_gt_f32_e32 vcc, 0, v4
	s_nop 1
	v_cndmask_b32_e32 v4, v5, v6, vcc
	s_waitcnt vmcnt(1)
	v_mul_f32_e32 v4, v4, v41
	s_waitcnt vmcnt(0)
	v_mul_f32_e32 v4, v4, v61
	ds_write_b32 v2, v4 offset:544
; __device__ __forceinline__ float gelu_erf(float v) {
;     const float av = fabsf(v), tt = __builtin_amdgcn_rcpf(av * 0.2316418882f + 1.0f);
;     float q = tt * 0.5307027145f + (-0.7265760135f); q = q * tt + 0.7107068705f; q = q * tt + (-0.142248368f); q = q * tt + 0.127414796f; q = q * tt;
;     const float e = __builtin_amdgcn_exp2f((v * v) * (-0.72134752044f));
;     const float m = v * (q * e); return v < 0.f ? m : v - m;
; }
; __device__ __forceinline__ void p12_peer(Frame& F) {
;     ...
; #pragma unroll
;     for (int i = 0; i < 4; ++i) { const int t = F.gw + i * F.NGW;
; #pragma unroll
;         for (int b = 0; b < 16; ++b) { float d = psum[i][b];
;             d += __builtin_bit_cast(float, __builtin_amdgcn_update_dpp(0, __builtin_bit_cast(int, d), 0xB1, 0xF, 0xF, false));
;             d += __builtin_bit_cast(float, __builtin_amdgcn_update_dpp(0, __builtin_bit_cast(int, d), 0x4E, 0xF, 0xF, false));
;             d += __builtin_bit_cast(float, __builtin_amdgcn_update_dpp(0, __builtin_bit_cast(int, d), 0x141, 0xF, 0xF, false));
;             const int idx = b * 8 + g8; const float w = PGT[(size_t)t * 128 + idx] * gelu_erf(sx[i] * d) * VSC[EL[i * 128 + idx]];
;             if (k8 == 0) WL[i * 128 + idx] = w; } }
.LBB0_3309:
	s_or_b64 exec, exec, s[2:3]
	v_add_f32_dpp v5, v141, v141 quad_perm:[1,0,3,2] row_mask:0xf bank_mask:0xf bound_ctrl:1
	v_mov_b32_e32 v6, 0
	v_mov_b32_e32 v4, 0
	v_add_f32_dpp v5, v5, v5 quad_perm:[2,3,0,1] row_mask:0xf bank_mask:0xf bound_ctrl:1
	s_nop 1
	v_mov_b32_dpp v6, v5 row_half_mirror row_mask:0xf bank_mask:0xf
	s_and_saveexec_b64 s[2:3], s[0:1]
	s_cbranch_execz .LBB0_3311
	v_add_f32_e32 v5, v5, v6
	v_mul_f32_e32 v5, v3, v5
	s_mov_b32 s16, 0x3e6d3388
	v_mul_f32_e32 v6, v5, v5
	s_waitcnt lgkmcnt(0)
	v_fma_f32 v7, |v5|, s16, 1.0
	v_rcp_f32_e32 v7, v7
	v_mov_b32_e32 v10, 0xbf3a00e3
	v_mul_f32_e32 v6, 0xbf38aa3b, v6
	v_exp_f32_e32 v6, v6
	v_fmac_f32_e32 v10, 0x3f07dc22, v7
	v_fmaak_f32 v10, v7, v10, 0x3f35f0e3
	v_fmaak_f32 v10, v7, v10, 0xbe11a98e
	v_fmaak_f32 v10, v7, v10, 0x3e027906
	v_mul_f32_e32 v7, v7, v10
	v_mul_f32_e32 v6, v6, v7
	v_mul_f32_e32 v7, v5, v6
	v_fma_f32 v6, -v5, v6, v5
	v_cmp_gt_f32_e32 vcc, 0, v5
	s_nop 1
	v_cndmask_b32_e32 v5, v6, v7, vcc
	s_waitcnt vmcnt(1)
	v_mul_f32_e32 v5, v5, v42
	s_waitcnt vmcnt(0)
	v_mul_f32_e32 v5, v5, v62
	ds_write_b32 v2, v5 offset:576
.LBB0_3311:
	s_or_b64 exec, exec, s[2:3]
	v_add_f32_dpp v5, v140, v140 quad_perm:[1,0,3,2] row_mask:0xf bank_mask:0xf bound_ctrl:1
	s_nop 1
	v_add_f32_dpp v5, v5, v5 quad_perm:[2,3,0,1] row_mask:0xf bank_mask:0xf bound_ctrl:1
	s_nop 1
	v_mov_b32_dpp v4, v5 row_half_mirror row_mask:0xf bank_mask:0xf
	s_and_saveexec_b64 s[2:3], s[0:1]
	s_cbranch_execz .LBB0_3313
	v_add_f32_e32 v4, v5, v4
	v_mul_f32_e32 v4, v3, v4
	s_mov_b32 s16, 0x3e6d3388
	v_mul_f32_e32 v5, v4, v4
	s_waitcnt lgkmcnt(0)
	v_fma_f32 v6, |v4|, s16, 1.0
	v_rcp_f32_e32 v6, v6
	v_mov_b32_e32 v9, 0xbf3a00e3
	v_mul_f32_e32 v5, 0xbf38aa3b, v5
	v_exp_f32_e32 v5, v5
	v_fmac_f32_e32 v9, 0x3f07dc22, v6
	v_fmaak_f32 v9, v6, v9, 0x3f35f0e3
	v_fmaak_f32 v9, v6, v9, 0xbe11a98e
	v_fmaak_f32 v9, v6, v9, 0x3e027906
	v_mul_f32_e32 v6, v6, v9
	v_mul_f32_e32 v5, v5, v6
	v_mul_f32_e32 v6, v4, v5
	v_fma_f32 v5, -v4, v5, v4
	v_cmp_gt_f32_e32 vcc, 0, v4
	s_nop 1
	v_cndmask_b32_e32 v4, v5, v6, vcc
	s_waitcnt vmcnt(1)
	v_mul_f32_e32 v4, v4, v43
	s_waitcnt vmcnt(0)
	v_mul_f32_e32 v4, v4, v63
	ds_write_b32 v2, v4 offset:608
.LBB0_3313:
	s_or_b64 exec, exec, s[2:3]
	v_add_f32_dpp v5, v139, v139 quad_perm:[1,0,3,2] row_mask:0xf bank_mask:0xf bound_ctrl:1
	v_mov_b32_e32 v6, 0
	v_mov_b32_e32 v4, 0
	v_add_f32_dpp v5, v5, v5 quad_perm:[2,3,0,1] row_mask:0xf bank_mask:0xf bound_ctrl:1
	s_nop 1
	v_mov_b32_dpp v6, v5 row_half_mirror row_mask:0xf bank_mask:0xf
	s_and_saveexec_b64 s[2:3], s[0:1]
	s_cbranch_execz .LBB0_3315
	v_add_f32_e32 v5, v5, v6
	v_mul_f32_e32 v5, v3, v5
	s_mov_b32 s16, 0x3e6d3388
	v_mul_f32_e32 v6, v5, v5
	s_waitcnt lgkmcnt(0)
	v_fma_f32 v7, |v5|, s16, 1.0
	v_rcp_f32_e32 v7, v7
	v_mov_b32_e32 v10, 0xbf3a00e3
	v_mul_f32_e32 v6, 0xbf38aa3b, v6
	v_exp_f32_e32 v6, v6
	v_fmac_f32_e32 v10, 0x3f07dc22, v7
	v_fmaak_f32 v10, v7, v10, 0x3f35f0e3
	v_fmaak_f32 v10, v7, v10, 0xbe11a98e
	v_fmaak_f32 v10, v7, v10, 0x3e027906
	v_mul_f32_e32 v7, v7, v10
	v_mul_f32_e32 v6, v6, v7
	v_mul_f32_e32 v7, v5, v6
	v_fma_f32 v6, -v5, v6, v5
	v_cmp_gt_f32_e32 vcc, 0, v5
	s_nop 1
	v_cndmask_b32_e32 v5, v6, v7, vcc
	s_waitcnt vmcnt(1)
	v_mul_f32_e32 v5, v5, v44
	s_waitcnt vmcnt(0)
	v_mul_f32_e32 v5, v5, v64
	ds_write_b32 v2, v5 offset:640
.LBB0_3315:
	s_or_b64 exec, exec, s[2:3]
	v_add_f32_dpp v5, v138, v138 quad_perm:[1,0,3,2] row_mask:0xf bank_mask:0xf bound_ctrl:1
	s_nop 1
	v_add_f32_dpp v5, v5, v5 quad_perm:[2,3,0,1] row_mask:0xf bank_mask:0xf bound_ctrl:1
	s_nop 1
	v_mov_b32_dpp v4, v5 row_half_mirror row_mask:0xf bank_mask:0xf
	s_and_saveexec_b64 s[2:3], s[0:1]
	s_cbranch_execz .LBB0_3317
	v_add_f32_e32 v4, v5, v4
	v_mul_f32_e32 v4, v3, v4
	s_mov_b32 s16, 0x3e6d3388
	v_mul_f32_e32 v5, v4, v4
	s_waitcnt lgkmcnt(0)
	v_fma_f32 v6, |v4|, s16, 1.0
	v_rcp_f32_e32 v6, v6
	v_mov_b32_e32 v9, 0xbf3a00e3
	v_mul_f32_e32 v5, 0xbf38aa3b, v5
	v_exp_f32_e32 v5, v5
	v_fmac_f32_e32 v9, 0x3f07dc22, v6
	v_fmaak_f32 v9, v6, v9, 0x3f35f0e3
	v_fmaak_f32 v9, v6, v9, 0xbe11a98e
	v_fmaak_f32 v9, v6, v9, 0x3e027906
	v_mul_f32_e32 v6, v6, v9
	v_mul_f32_e32 v5, v5, v6
	v_mul_f32_e32 v6, v4, v5
	v_fma_f32 v5, -v4, v5, v4
	v_cmp_gt_f32_e32 vcc, 0, v4
	s_nop 1
	v_cndmask_b32_e32 v4, v5, v6, vcc
	s_waitcnt vmcnt(1)
	v_mul_f32_e32 v4, v4, v45
	s_waitcnt vmcnt(0)
	v_mul_f32_e32 v4, v4, v65
	ds_write_b32 v2, v4 offset:672
.LBB0_3317:
	s_or_b64 exec, exec, s[2:3]
	v_add_f32_dpp v5, v137, v137 quad_perm:[1,0,3,2] row_mask:0xf bank_mask:0xf bound_ctrl:1
	v_mov_b32_e32 v6, 0
	v_mov_b32_e32 v4, 0
	v_add_f32_dpp v5, v5, v5 quad_perm:[2,3,0,1] row_mask:0xf bank_mask:0xf bound_ctrl:1
	s_nop 1
	v_mov_b32_dpp v6, v5 row_half_mirror row_mask:0xf bank_mask:0xf
	s_and_saveexec_b64 s[2:3], s[0:1]
	s_cbranch_execz .LBB0_3319
	v_add_f32_e32 v5, v5, v6
	v_mul_f32_e32 v5, v3, v5
	s_mov_b32 s16, 0x3e6d3388
	v_mul_f32_e32 v6, v5, v5
	s_waitcnt lgkmcnt(0)
	v_fma_f32 v7, |v5|, s16, 1.0
	v_rcp_f32_e32 v7, v7
	v_mov_b32_e32 v10, 0xbf3a00e3
	v_mul_f32_e32 v6, 0xbf38aa3b, v6
	v_exp_f32_e32 v6, v6
	v_fmac_f32_e32 v10, 0x3f07dc22, v7
	v_fmaak_f32 v10, v7, v10, 0x3f35f0e3
	v_fmaak_f32 v10, v7, v10, 0xbe11a98e
	v_fmaak_f32 v10, v7, v10, 0x3e027906
	v_mul_f32_e32 v7, v7, v10
	v_mul_f32_e32 v6, v6, v7
	v_mul_f32_e32 v7, v5, v6
	v_fma_f32 v6, -v5, v6, v5
	v_cmp_gt_f32_e32 vcc, 0, v5
	s_nop 1
	v_cndmask_b32_e32 v5, v6, v7, vcc
	s_waitcnt vmcnt(1)
	v_mul_f32_e32 v5, v5, v46
	s_waitcnt vmcnt(0)
	v_mul_f32_e32 v5, v5, v66
	ds_write_b32 v2, v5 offset:704
; __device__ __forceinline__ float gelu_erf(float v) {
;     const float av = fabsf(v), tt = __builtin_amdgcn_rcpf(av * 0.2316418882f + 1.0f);
;     float q = tt * 0.5307027145f + (-0.7265760135f); q = q * tt + 0.7107068705f; q = q * tt + (-0.142248368f); q = q * tt + 0.127414796f; q = q * tt;
;     const float e = __builtin_amdgcn_exp2f((v * v) * (-0.72134752044f));
;     const float m = v * (q * e); return v < 0.f ? m : v - m;
; }
; __device__ __forceinline__ void p12_peer(Frame& F) {
;     ...
; #pragma unroll
;     for (int i = 0; i < 4; ++i) { const int t = F.gw + i * F.NGW;
; #pragma unroll
;         for (int b = 0; b < 16; ++b) { float d = psum[i][b];
;             d += __builtin_bit_cast(float, __builtin_amdgcn_update_dpp(0, __builtin_bit_cast(int, d), 0xB1, 0xF, 0xF, false));
;             d += __builtin_bit_cast(float, __builtin_amdgcn_update_dpp(0, __builtin_bit_cast(int, d), 0x4E, 0xF, 0xF, false));
;             d += __builtin_bit_cast(float, __builtin_amdgcn_update_dpp(0, __builtin_bit_cast(int, d), 0x141, 0xF, 0xF, false));
;             const int idx = b * 8 + g8; const float w = PGT[(size_t)t * 128 + idx] * gelu_erf(sx[i] * d) * VSC[EL[i * 128 + idx]];
;             if (k8 == 0) WL[i * 128 + idx] = w; } }
.LBB0_3319:
	s_or_b64 exec, exec, s[2:3]
	v_add_f32_dpp v5, v136, v136 quad_perm:[1,0,3,2] row_mask:0xf bank_mask:0xf bound_ctrl:1
	s_nop 1
	v_add_f32_dpp v5, v5, v5 quad_perm:[2,3,0,1] row_mask:0xf bank_mask:0xf bound_ctrl:1
	s_nop 1
	v_mov_b32_dpp v4, v5 row_half_mirror row_mask:0xf bank_mask:0xf
	s_and_saveexec_b64 s[2:3], s[0:1]
	s_cbranch_execz .LBB0_3321
	v_add_f32_e32 v4, v5, v4
	v_mul_f32_e32 v4, v3, v4
	s_mov_b32 s16, 0x3e6d3388
	v_mul_f32_e32 v5, v4, v4
	s_waitcnt lgkmcnt(0)
	v_fma_f32 v6, |v4|, s16, 1.0
	v_rcp_f32_e32 v6, v6
	v_mov_b32_e32 v9, 0xbf3a00e3
	v_mul_f32_e32 v5, 0xbf38aa3b, v5
	v_exp_f32_e32 v5, v5
	v_fmac_f32_e32 v9, 0x3f07dc22, v6
	v_fmaak_f32 v9, v6, v9, 0x3f35f0e3
	v_fmaak_f32 v9, v6, v9, 0xbe11a98e
	v_fmaak_f32 v9, v6, v9, 0x3e027906
	v_mul_f32_e32 v6, v6, v9
	v_mul_f32_e32 v5, v5, v6
	v_mul_f32_e32 v6, v4, v5
	v_fma_f32 v5, -v4, v5, v4
	v_cmp_gt_f32_e32 vcc, 0, v4
	s_nop 1
	v_cndmask_b32_e32 v4, v5, v6, vcc
	s_waitcnt vmcnt(1)
	v_mul_f32_e32 v4, v4, v47
	s_waitcnt vmcnt(0)
	v_mul_f32_e32 v4, v4, v67
	ds_write_b32 v2, v4 offset:736
.LBB0_3321:
	s_or_b64 exec, exec, s[2:3]
	v_add_f32_dpp v5, v135, v135 quad_perm:[1,0,3,2] row_mask:0xf bank_mask:0xf bound_ctrl:1
	v_mov_b32_e32 v6, 0
	v_mov_b32_e32 v4, 0
	v_add_f32_dpp v5, v5, v5 quad_perm:[2,3,0,1] row_mask:0xf bank_mask:0xf bound_ctrl:1
	s_nop 1
	v_mov_b32_dpp v6, v5 row_half_mirror row_mask:0xf bank_mask:0xf
	s_and_saveexec_b64 s[2:3], s[0:1]
	s_cbranch_execz .LBB0_3323
	v_add_f32_e32 v5, v5, v6
	v_mul_f32_e32 v5, v3, v5
	s_mov_b32 s16, 0x3e6d3388
	v_mul_f32_e32 v6, v5, v5
	s_waitcnt lgkmcnt(0)
	v_fma_f32 v7, |v5|, s16, 1.0
	v_rcp_f32_e32 v7, v7
	v_mov_b32_e32 v10, 0xbf3a00e3
	v_mul_f32_e32 v6, 0xbf38aa3b, v6
	v_exp_f32_e32 v6, v6
	v_fmac_f32_e32 v10, 0x3f07dc22, v7
	v_fmaak_f32 v10, v7, v10, 0x3f35f0e3
	v_fmaak_f32 v10, v7, v10, 0xbe11a98e
	v_fmaak_f32 v10, v7, v10, 0x3e027906
	v_mul_f32_e32 v7, v7, v10
	v_mul_f32_e32 v6, v6, v7
	v_mul_f32_e32 v7, v5, v6
	v_fma_f32 v6, -v5, v6, v5
	v_cmp_gt_f32_e32 vcc, 0, v5
	s_nop 1
	v_cndmask_b32_e32 v5, v6, v7, vcc
	s_waitcnt vmcnt(1)
	v_mul_f32_e32 v5, v5, v48
	s_waitcnt vmcnt(0)
	v_mul_f32_e32 v5, v5, v68
	ds_write_b32 v2, v5 offset:768
.LBB0_3323:
	s_or_b64 exec, exec, s[2:3]
	v_add_f32_dpp v5, v134, v134 quad_perm:[1,0,3,2] row_mask:0xf bank_mask:0xf bound_ctrl:1
	s_nop 1
	v_add_f32_dpp v5, v5, v5 quad_perm:[2,3,0,1] row_mask:0xf bank_mask:0xf bound_ctrl:1
	s_nop 1
	v_mov_b32_dpp v4, v5 row_half_mirror row_mask:0xf bank_mask:0xf
	s_and_saveexec_b64 s[2:3], s[0:1]
	s_cbranch_execz .LBB0_3325
	v_add_f32_e32 v4, v5, v4
	v_mul_f32_e32 v4, v3, v4
	s_mov_b32 s16, 0x3e6d3388
	v_mul_f32_e32 v5, v4, v4
	s_waitcnt lgkmcnt(0)
	v_fma_f32 v6, |v4|, s16, 1.0
	v_rcp_f32_e32 v6, v6
	v_mov_b32_e32 v9, 0xbf3a00e3
	v_mul_f32_e32 v5, 0xbf38aa3b, v5
	v_exp_f32_e32 v5, v5
	v_fmac_f32_e32 v9, 0x3f07dc22, v6
	v_fmaak_f32 v9, v6, v9, 0x3f35f0e3
	v_fmaak_f32 v9, v6, v9, 0xbe11a98e
	v_fmaak_f32 v9, v6, v9, 0x3e027906
	v_mul_f32_e32 v6, v6, v9
	v_mul_f32_e32 v5, v5, v6
	v_mul_f32_e32 v6, v4, v5
	v_fma_f32 v5, -v4, v5, v4
	v_cmp_gt_f32_e32 vcc, 0, v4
	s_nop 1
	v_cndmask_b32_e32 v4, v5, v6, vcc
	s_waitcnt vmcnt(1)
	v_mul_f32_e32 v4, v4, v49
	s_waitcnt vmcnt(0)
	v_mul_f32_e32 v4, v4, v69
	ds_write_b32 v2, v4 offset:800
.LBB0_3325:
	s_or_b64 exec, exec, s[2:3]
	v_add_f32_dpp v5, v133, v133 quad_perm:[1,0,3,2] row_mask:0xf bank_mask:0xf bound_ctrl:1
	v_mov_b32_e32 v6, 0
	v_mov_b32_e32 v4, 0
	v_add_f32_dpp v5, v5, v5 quad_perm:[2,3,0,1] row_mask:0xf bank_mask:0xf bound_ctrl:1
	s_nop 1
	v_mov_b32_dpp v6, v5 row_half_mirror row_mask:0xf bank_mask:0xf
	s_and_saveexec_b64 s[2:3], s[0:1]
	s_cbranch_execz .LBB0_3327
	v_add_f32_e32 v5, v5, v6
	v_mul_f32_e32 v5, v3, v5
	s_mov_b32 s16, 0x3e6d3388
	v_mul_f32_e32 v6, v5, v5
	s_waitcnt lgkmcnt(0)
	v_fma_f32 v7, |v5|, s16, 1.0
	v_rcp_f32_e32 v7, v7
	v_mov_b32_e32 v10, 0xbf3a00e3
	v_mul_f32_e32 v6, 0xbf38aa3b, v6
	v_exp_f32_e32 v6, v6
	v_fmac_f32_e32 v10, 0x3f07dc22, v7
	v_fmaak_f32 v10, v7, v10, 0x3f35f0e3
	v_fmaak_f32 v10, v7, v10, 0xbe11a98e
	v_fmaak_f32 v10, v7, v10, 0x3e027906
	v_mul_f32_e32 v7, v7, v10
	v_mul_f32_e32 v6, v6, v7
	v_mul_f32_e32 v7, v5, v6
	v_fma_f32 v6, -v5, v6, v5
	v_cmp_gt_f32_e32 vcc, 0, v5
	s_nop 1
	v_cndmask_b32_e32 v5, v6, v7, vcc
	s_waitcnt vmcnt(1)
	v_mul_f32_e32 v5, v5, v50
	s_waitcnt vmcnt(0)
	v_mul_f32_e32 v5, v5, v70
	ds_write_b32 v2, v5 offset:832
.LBB0_3327:
	s_or_b64 exec, exec, s[2:3]
	v_add_f32_dpp v5, v132, v132 quad_perm:[1,0,3,2] row_mask:0xf bank_mask:0xf bound_ctrl:1
	s_nop 1
	v_add_f32_dpp v5, v5, v5 quad_perm:[2,3,0,1] row_mask:0xf bank_mask:0xf bound_ctrl:1
	s_nop 1
	v_mov_b32_dpp v4, v5 row_half_mirror row_mask:0xf bank_mask:0xf
	s_and_saveexec_b64 s[2:3], s[0:1]
	s_cbranch_execz .LBB0_3329
	v_add_f32_e32 v4, v5, v4
	v_mul_f32_e32 v4, v3, v4
	s_mov_b32 s16, 0x3e6d3388
	v_mul_f32_e32 v5, v4, v4
	s_waitcnt lgkmcnt(0)
	v_fma_f32 v6, |v4|, s16, 1.0
	v_rcp_f32_e32 v6, v6
	v_mov_b32_e32 v9, 0xbf3a00e3
	v_mul_f32_e32 v5, 0xbf38aa3b, v5
	v_exp_f32_e32 v5, v5
	v_fmac_f32_e32 v9, 0x3f07dc22, v6
	v_fmaak_f32 v9, v6, v9, 0x3f35f0e3
	v_fmaak_f32 v9, v6, v9, 0xbe11a98e
	v_fmaak_f32 v9, v6, v9, 0x3e027906
	v_mul_f32_e32 v6, v6, v9
	v_mul_f32_e32 v5, v5, v6
	v_mul_f32_e32 v6, v4, v5
	v_fma_f32 v5, -v4, v5, v4
	v_cmp_gt_f32_e32 vcc, 0, v4
	s_nop 1
	v_cndmask_b32_e32 v4, v5, v6, vcc
	s_waitcnt vmcnt(1)
	v_mul_f32_e32 v4, v4, v51
	s_waitcnt vmcnt(0)
	v_mul_f32_e32 v4, v4, v71
	ds_write_b32 v2, v4 offset:864
; __device__ __forceinline__ float gelu_erf(float v) {
;     const float av = fabsf(v), tt = __builtin_amdgcn_rcpf(av * 0.2316418882f + 1.0f);
;     float q = tt * 0.5307027145f + (-0.7265760135f); q = q * tt + 0.7107068705f; q = q * tt + (-0.142248368f); q = q * tt + 0.127414796f; q = q * tt;
;     const float e = __builtin_amdgcn_exp2f((v * v) * (-0.72134752044f));
;     const float m = v * (q * e); return v < 0.f ? m : v - m;
; }
; __device__ __forceinline__ void p12_peer(Frame& F) {
;     ...
; #pragma unroll
;     for (int i = 0; i < 4; ++i) { const int t = F.gw + i * F.NGW;
; #pragma unroll
;         for (int b = 0; b < 16; ++b) { float d = psum[i][b];
;             d += __builtin_bit_cast(float, __builtin_amdgcn_update_dpp(0, __builtin_bit_cast(int, d), 0xB1, 0xF, 0xF, false));
;             d += __builtin_bit_cast(float, __builtin_amdgcn_update_dpp(0, __builtin_bit_cast(int, d), 0x4E, 0xF, 0xF, false));
;             d += __builtin_bit_cast(float, __builtin_amdgcn_update_dpp(0, __builtin_bit_cast(int, d), 0x141, 0xF, 0xF, false));
;             const int idx = b * 8 + g8; const float w = PGT[(size_t)t * 128 + idx] * gelu_erf(sx[i] * d) * VSC[EL[i * 128 + idx]];
;             if (k8 == 0) WL[i * 128 + idx] = w; } }
.LBB0_3329:
	s_or_b64 exec, exec, s[2:3]
	v_add_f32_dpp v5, v131, v131 quad_perm:[1,0,3,2] row_mask:0xf bank_mask:0xf bound_ctrl:1
	v_mov_b32_e32 v6, 0
	v_mov_b32_e32 v4, 0
	v_add_f32_dpp v5, v5, v5 quad_perm:[2,3,0,1] row_mask:0xf bank_mask:0xf bound_ctrl:1
	s_nop 1
	v_mov_b32_dpp v6, v5 row_half_mirror row_mask:0xf bank_mask:0xf
	s_and_saveexec_b64 s[2:3], s[0:1]
	s_cbranch_execz .LBB0_3331
	v_add_f32_e32 v5, v5, v6
	v_mul_f32_e32 v5, v3, v5
	s_mov_b32 s16, 0x3e6d3388
	v_mul_f32_e32 v6, v5, v5
	s_waitcnt lgkmcnt(0)
	v_fma_f32 v7, |v5|, s16, 1.0
	v_rcp_f32_e32 v7, v7
	v_mov_b32_e32 v10, 0xbf3a00e3
	v_mul_f32_e32 v6, 0xbf38aa3b, v6
	v_exp_f32_e32 v6, v6
	v_fmac_f32_e32 v10, 0x3f07dc22, v7
	v_fmaak_f32 v10, v7, v10, 0x3f35f0e3
	v_fmaak_f32 v10, v7, v10, 0xbe11a98e
	v_fmaak_f32 v10, v7, v10, 0x3e027906
	v_mul_f32_e32 v7, v7, v10
	v_mul_f32_e32 v6, v6, v7
	v_mul_f32_e32 v7, v5, v6
	v_fma_f32 v6, -v5, v6, v5
	v_cmp_gt_f32_e32 vcc, 0, v5
	s_nop 1
	v_cndmask_b32_e32 v5, v6, v7, vcc
	s_waitcnt vmcnt(1)
	v_mul_f32_e32 v5, v5, v52
	s_waitcnt vmcnt(0)
	v_mul_f32_e32 v5, v5, v72
	ds_write_b32 v2, v5 offset:896
.LBB0_3331:
	s_or_b64 exec, exec, s[2:3]
	v_add_f32_dpp v5, v130, v130 quad_perm:[1,0,3,2] row_mask:0xf bank_mask:0xf bound_ctrl:1
	s_nop 1
	v_add_f32_dpp v5, v5, v5 quad_perm:[2,3,0,1] row_mask:0xf bank_mask:0xf bound_ctrl:1
	s_nop 1
	v_mov_b32_dpp v4, v5 row_half_mirror row_mask:0xf bank_mask:0xf
	s_and_saveexec_b64 s[2:3], s[0:1]
	s_cbranch_execz .LBB0_3333
	v_add_f32_e32 v4, v5, v4
	v_mul_f32_e32 v4, v3, v4
	s_mov_b32 s16, 0x3e6d3388
	v_mul_f32_e32 v5, v4, v4
	s_waitcnt lgkmcnt(0)
	v_fma_f32 v6, |v4|, s16, 1.0
	v_rcp_f32_e32 v6, v6
	v_mov_b32_e32 v9, 0xbf3a00e3
	v_mul_f32_e32 v5, 0xbf38aa3b, v5
	v_exp_f32_e32 v5, v5
	v_fmac_f32_e32 v9, 0x3f07dc22, v6
	v_fmaak_f32 v9, v6, v9, 0x3f35f0e3
	v_fmaak_f32 v9, v6, v9, 0xbe11a98e
	v_fmaak_f32 v9, v6, v9, 0x3e027906
	v_mul_f32_e32 v6, v6, v9
	v_mul_f32_e32 v5, v5, v6
	v_mul_f32_e32 v6, v4, v5
	v_fma_f32 v5, -v4, v5, v4
	v_cmp_gt_f32_e32 vcc, 0, v4
	s_nop 1
	v_cndmask_b32_e32 v4, v5, v6, vcc
	s_waitcnt vmcnt(1)
	v_mul_f32_e32 v4, v4, v53
	s_waitcnt vmcnt(0)
	v_mul_f32_e32 v4, v4, v73
	ds_write_b32 v2, v4 offset:928
.LBB0_3333:
	s_or_b64 exec, exec, s[2:3]
	v_add_f32_dpp v5, v129, v129 quad_perm:[1,0,3,2] row_mask:0xf bank_mask:0xf bound_ctrl:1
	v_mov_b32_e32 v6, 0
	v_mov_b32_e32 v4, 0
	v_add_f32_dpp v5, v5, v5 quad_perm:[2,3,0,1] row_mask:0xf bank_mask:0xf bound_ctrl:1
	s_nop 1
	v_mov_b32_dpp v6, v5 row_half_mirror row_mask:0xf bank_mask:0xf
	s_and_saveexec_b64 s[2:3], s[0:1]
	s_cbranch_execz .LBB0_3335
	v_add_f32_e32 v5, v5, v6
	v_mul_f32_e32 v5, v3, v5
	s_mov_b32 s16, 0x3e6d3388
	v_mul_f32_e32 v6, v5, v5
	s_waitcnt lgkmcnt(0)
	v_fma_f32 v7, |v5|, s16, 1.0
	v_rcp_f32_e32 v7, v7
	v_mov_b32_e32 v10, 0xbf3a00e3
	v_mul_f32_e32 v6, 0xbf38aa3b, v6
	v_exp_f32_e32 v6, v6
	v_fmac_f32_e32 v10, 0x3f07dc22, v7
	v_fmaak_f32 v10, v7, v10, 0x3f35f0e3
	v_fmaak_f32 v10, v7, v10, 0xbe11a98e
	v_fmaak_f32 v10, v7, v10, 0x3e027906
	v_mul_f32_e32 v7, v7, v10
	v_mul_f32_e32 v6, v6, v7
	v_mul_f32_e32 v7, v5, v6
	v_fma_f32 v6, -v5, v6, v5
	v_cmp_gt_f32_e32 vcc, 0, v5
	s_nop 1
	v_cndmask_b32_e32 v5, v6, v7, vcc
	s_waitcnt vmcnt(1)
	v_mul_f32_e32 v5, v5, v54
	s_waitcnt vmcnt(0)
	v_mul_f32_e32 v5, v5, v74
	ds_write_b32 v2, v5 offset:960
.LBB0_3335:
	s_or_b64 exec, exec, s[2:3]
	v_add_f32_dpp v5, v128, v128 quad_perm:[1,0,3,2] row_mask:0xf bank_mask:0xf bound_ctrl:1
	s_nop 1
	v_add_f32_dpp v5, v5, v5 quad_perm:[2,3,0,1] row_mask:0xf bank_mask:0xf bound_ctrl:1
	s_nop 1
	v_mov_b32_dpp v4, v5 row_half_mirror row_mask:0xf bank_mask:0xf
	s_and_saveexec_b64 s[2:3], s[0:1]
	s_cbranch_execz .LBB0_3337
	s_mov_b32 s16, 0x3e6d3388
	s_waitcnt lgkmcnt(0)
	v_add_f32_e32 v0, v5, v4
	v_mul_f32_e32 v0, v3, v0
	v_fma_f32 v3, |v0|, s16, 1.0
	v_rcp_f32_e32 v3, v3
	v_mul_f32_e32 v1, v0, v0
	v_mov_b32_e32 v4, 0xbf3a00e3
	v_mul_f32_e32 v1, 0xbf38aa3b, v1
	v_fmac_f32_e32 v4, 0x3f07dc22, v3
	v_exp_f32_e32 v1, v1
	v_fmaak_f32 v4, v3, v4, 0x3f35f0e3
	v_fmaak_f32 v4, v3, v4, 0xbe11a98e
	v_fmaak_f32 v4, v3, v4, 0x3e027906
	v_mul_f32_e32 v3, v3, v4
	v_mul_f32_e32 v1, v1, v3
	v_mul_f32_e32 v3, v0, v1
	v_fma_f32 v1, -v0, v1, v0
	v_cmp_gt_f32_e32 vcc, 0, v0
	s_nop 1
	v_cndmask_b32_e32 v0, v1, v3, vcc
	s_waitcnt vmcnt(1)
	v_mul_f32_e32 v0, v0, v55
	s_waitcnt vmcnt(0)
	v_mul_f32_e32 v0, v0, v75
	ds_write_b32 v2, v0 offset:992
; #define LDS_WAIT() asm volatile("s_waitcnt lgkmcnt(0)" ::: "memory")
; __device__ __forceinline__ float wave_sum(float v) { v = dpp_add16(v); return (rdlane(v, 0) + rdlane(v, 16)) + (rdlane(v, 32) + rdlane(v, 48)); }
; __device__ __forceinline__ void p12_peer(Frame& F) {
;     ...
;         const float rsn = 1.0f / sqrtf(wave_sum(PSQ[(size_t)t * 64 + F.lane]) * (1.f / D_) + 1e-6f);
;         sx[i] = mxa * rsn * (1.0f / 127.0f);
;     ...
;     asm volatile("" ::: "memory"); LDS_WAIT();
; #pragma unroll
;     for (int i = 0; i < 4; ++i) { const int t = F.gw + i * F.NGW;
; #pragma unroll
;         for (int b = 0; b < 16; ++b) { float d = psum[i][b];
;             d += __builtin_bit_cast(float, __builtin_amdgcn_update_dpp(0, __builtin_bit_cast(int, d), 0xB1, 0xF, 0xF, false));
;             d += __builtin_bit_cast(float, __builtin_amdgcn_update_dpp(0, __builtin_bit_cast(int, d), 0x4E, 0xF, 0xF, false));
;             d += __builtin_bit_cast(float, __builtin_amdgcn_update_dpp(0, __builtin_bit_cast(int, d), 0x141, 0xF, 0xF, false));
;             const int idx = b * 8 + g8; const float w = PGT[(size_t)t * 128 + idx] * gelu_erf(sx[i] * d) * VSC[EL[i * 128 + idx]];
;             if (k8 == 0) WL[i * 128 + idx] = w; } }
.LBB0_3337:
	s_or_b64 exec, exec, s[2:3]
	v_mov_b32_e32 v0, s31
	v_mov_b32_e32 v1, s33
	v_add_f32_e32 v0, s29, v0
	v_add_f32_e32 v1, s30, v1
	v_add_f32_e32 v0, v0, v1
	v_mov_b32_e32 v1, 0x358637bd
	v_fmac_f32_e32 v1, 0x39800000, v0
	s_mov_b32 s2, 0xf800000
	v_mul_f32_e32 v0, 0x4f800000, v1
	v_cmp_gt_f32_e32 vcc, s2, v1
	s_nop 1
	v_cndmask_b32_e32 v0, v1, v0, vcc
	v_sqrt_f32_e32 v1, v0
	s_nop 0
	v_add_u32_e32 v3, -1, v1
	v_fma_f32 v4, -v3, v1, v0
	v_cmp_ge_f32_e64 s[2:3], 0, v4
	v_add_u32_e32 v4, 1, v1
	s_nop 0
	v_cndmask_b32_e64 v3, v1, v3, s[2:3]
	v_fma_f32 v1, -v4, v1, v0
	v_cmp_lt_f32_e64 s[2:3], 0, v1
	s_nop 1
	v_cndmask_b32_e64 v1, v3, v4, s[2:3]
	v_mul_f32_e32 v3, 0x37800000, v1
	v_cndmask_b32_e32 v1, v1, v3, vcc
	v_mov_b32_e32 v3, 0x260
	v_cmp_class_f32_e32 vcc, v0, v3
	s_nop 1
	v_cndmask_b32_e32 v0, v1, v0, vcc
	v_div_scale_f32 v1, s[2:3], v0, v0, 1.0
	v_rcp_f32_e32 v3, v1
	s_add_u32 s2, s43, s14
	s_addc_u32 s3, s44, s15
	v_fma_f32 v4, -v1, v3, 1.0
	v_fmac_f32_e32 v3, v4, v3
	v_div_scale_f32 v4, vcc, 1.0, v0, 1.0
	v_mul_f32_e32 v5, v4, v3
	v_fma_f32 v6, -v1, v5, v4
	v_fmac_f32_e32 v5, v6, v3
	v_fma_f32 v1, -v1, v5, v4
	v_div_fmas_f32 v1, v1, v3, v5
	v_div_fixup_f32 v0, v1, v0, 1.0
	v_add_f32_dpp v5, v127, v127 quad_perm:[1,0,3,2] row_mask:0xf bank_mask:0xf bound_ctrl:1
	v_mul_f32_e32 v0, v161, v0
	v_mov_b32_e32 v6, 0
	v_add_f32_dpp v5, v5, v5 quad_perm:[2,3,0,1] row_mask:0xf bank_mask:0xf bound_ctrl:1
	v_mul_f32_e32 v3, 0x3c010204, v0
	v_lshl_add_u64 v[0:1], v[94:95], 2, s[2:3]
	ds_read_u16 v20, v93 offset:16896
	ds_read_u16 v21, v93 offset:16912
	ds_read_u16 v22, v93 offset:16928
	ds_read_u16 v23, v93 offset:16944
	ds_read_u16 v24, v93 offset:16960
	ds_read_u16 v25, v93 offset:16976
	ds_read_u16 v26, v93 offset:16992
	ds_read_u16 v27, v93 offset:17008
	s_waitcnt lgkmcnt(0)
	ds_read_u16 v28, v93 offset:17024
	ds_read_u16 v29, v93 offset:17040
	ds_read_u16 v30, v93 offset:17056
	ds_read_u16 v31, v93 offset:17072
	ds_read_u16 v32, v93 offset:17088
	ds_read_u16 v33, v93 offset:17104
	ds_read_u16 v34, v93 offset:17120
	ds_read_u16 v35, v93 offset:17136
	s_waitcnt lgkmcnt(0)
	v_lshlrev_b32_e32 v20, 2, v20
	v_lshlrev_b32_e32 v21, 2, v21
	v_lshlrev_b32_e32 v22, 2, v22
	v_lshlrev_b32_e32 v23, 2, v23
	v_lshlrev_b32_e32 v24, 2, v24
	v_lshlrev_b32_e32 v25, 2, v25
	v_lshlrev_b32_e32 v26, 2, v26
	v_lshlrev_b32_e32 v27, 2, v27
	v_lshlrev_b32_e32 v28, 2, v28
	v_lshlrev_b32_e32 v29, 2, v29
	v_lshlrev_b32_e32 v30, 2, v30
	v_lshlrev_b32_e32 v31, 2, v31
	v_lshlrev_b32_e32 v32, 2, v32
	v_lshlrev_b32_e32 v33, 2, v33
	v_lshlrev_b32_e32 v34, 2, v34
	v_lshlrev_b32_e32 v35, 2, v35
	global_load_dword v40, v[0:1], off offset:0
	global_load_dword v60, v20, s[18:19]
	global_load_dword v41, v[0:1], off offset:32
	global_load_dword v61, v21, s[18:19]
	global_load_dword v42, v[0:1], off offset:64
	global_load_dword v62, v22, s[18:19]
	global_load_dword v43, v[0:1], off offset:96
	global_load_dword v63, v23, s[18:19]
	global_load_dword v44, v[0:1], off offset:128
	global_load_dword v64, v24, s[18:19]
	global_load_dword v45, v[0:1], off offset:160
	global_load_dword v65, v25, s[18:19]
	global_load_dword v46, v[0:1], off offset:192
	global_load_dword v66, v26, s[18:19]
	global_load_dword v47, v[0:1], off offset:224
	global_load_dword v67, v27, s[18:19]
	global_load_dword v48, v[0:1], off offset:256
	global_load_dword v68, v28, s[18:19]
	global_load_dword v49, v[0:1], off offset:288
	global_load_dword v69, v29, s[18:19]
	global_load_dword v50, v[0:1], off offset:320
	global_load_dword v70, v30, s[18:19]
	global_load_dword v51, v[0:1], off offset:352
	global_load_dword v71, v31, s[18:19]
	global_load_dword v52, v[0:1], off offset:384
	global_load_dword v72, v32, s[18:19]
	global_load_dword v53, v[0:1], off offset:416
	global_load_dword v73, v33, s[18:19]
	global_load_dword v54, v[0:1], off offset:448
	global_load_dword v74, v34, s[18:19]
	global_load_dword v55, v[0:1], off offset:480
	global_load_dword v75, v35, s[18:19]
	s_waitcnt vmcnt(0)
	v_mov_b32_e32 v4, 0
	v_mov_b32_dpp v6, v5 row_half_mirror row_mask:0xf bank_mask:0xf
	s_and_saveexec_b64 s[2:3], s[0:1]
	s_cbranch_execz .LBB0_3339
	v_add_f32_e32 v5, v5, v6
	v_mul_f32_e32 v5, v3, v5
	s_mov_b32 s14, 0x3e6d3388
	v_mul_f32_e32 v6, v5, v5
	s_waitcnt lgkmcnt(0)
	v_fma_f32 v7, |v5|, s14, 1.0
	v_rcp_f32_e32 v7, v7
	v_mov_b32_e32 v10, 0xbf3a00e3
	v_mul_f32_e32 v6, 0xbf38aa3b, v6
	v_exp_f32_e32 v6, v6
	v_fmac_f32_e32 v10, 0x3f07dc22, v7
	v_fmaak_f32 v10, v7, v10, 0x3f35f0e3
	v_fmaak_f32 v10, v7, v10, 0xbe11a98e
	v_fmaak_f32 v10, v7, v10, 0x3e027906
	v_mul_f32_e32 v7, v7, v10
	v_mul_f32_e32 v6, v6, v7
	v_mul_f32_e32 v7, v5, v6
	v_fma_f32 v6, -v5, v6, v5
	v_cmp_gt_f32_e32 vcc, 0, v5
	s_nop 1
	v_cndmask_b32_e32 v5, v6, v7, vcc
	s_waitcnt vmcnt(1)
	v_mul_f32_e32 v5, v5, v40
	s_waitcnt vmcnt(0)
	v_mul_f32_e32 v5, v5, v60
	ds_write_b32 v2, v5 offset:1024
.LBB0_3339:
	s_or_b64 exec, exec, s[2:3]
	v_add_f32_dpp v5, v126, v126 quad_perm:[1,0,3,2] row_mask:0xf bank_mask:0xf bound_ctrl:1
	s_nop 1
	v_add_f32_dpp v5, v5, v5 quad_perm:[2,3,0,1] row_mask:0xf bank_mask:0xf bound_ctrl:1
	s_nop 1
	v_mov_b32_dpp v4, v5 row_half_mirror row_mask:0xf bank_mask:0xf
	s_and_saveexec_b64 s[2:3], s[0:1]
	s_cbranch_execz .LBB0_3341
	v_add_f32_e32 v4, v5, v4
	v_mul_f32_e32 v4, v3, v4
	s_mov_b32 s14, 0x3e6d3388
	v_mul_f32_e32 v5, v4, v4
	s_waitcnt lgkmcnt(0)
	v_fma_f32 v6, |v4|, s14, 1.0
	v_rcp_f32_e32 v6, v6
	v_mov_b32_e32 v9, 0xbf3a00e3
	v_mul_f32_e32 v5, 0xbf38aa3b, v5
	v_exp_f32_e32 v5, v5
	v_fmac_f32_e32 v9, 0x3f07dc22, v6
	v_fmaak_f32 v9, v6, v9, 0x3f35f0e3
	v_fmaak_f32 v9, v6, v9, 0xbe11a98e
	v_fmaak_f32 v9, v6, v9, 0x3e027906
	v_mul_f32_e32 v6, v6, v9
	v_mul_f32_e32 v5, v5, v6
	v_mul_f32_e32 v6, v4, v5
	v_fma_f32 v5, -v4, v5, v4
	v_cmp_gt_f32_e32 vcc, 0, v4
	s_nop 1
	v_cndmask_b32_e32 v4, v5, v6, vcc
	s_waitcnt vmcnt(1)
	v_mul_f32_e32 v4, v4, v41
	s_waitcnt vmcnt(0)
	v_mul_f32_e32 v4, v4, v61
	ds_write_b32 v2, v4 offset:1056
; __device__ __forceinline__ void p12_peer(Frame& F) {
;     ...
;     for (int i = 0; i < 4; ++i) { const int t = F.gw + i * F.NGW;
; #pragma unroll
;         for (int b = 0; b < 16; ++b) { float d = psum[i][b];
;             d += __builtin_bit_cast(float, __builtin_amdgcn_update_dpp(0, __builtin_bit_cast(int, d), 0xB1, 0xF, 0xF, false));
;             d += __builtin_bit_cast(float, __builtin_amdgcn_update_dpp(0, __builtin_bit_cast(int, d), 0x4E, 0xF, 0xF, false));
;             d += __builtin_bit_cast(float, __builtin_amdgcn_update_dpp(0, __builtin_bit_cast(int, d), 0x141, 0xF, 0xF, false));
;             const int idx = b * 8 + g8; const float w = PGT[(size_t)t * 128 + idx] * gelu_erf(sx[i] * d) * VSC[EL[i * 128 + idx]];
;             if (k8 == 0) WL[i * 128 + idx] = w; } }
.LBB0_3341:
	s_or_b64 exec, exec, s[2:3]
	v_add_f32_dpp v5, v125, v125 quad_perm:[1,0,3,2] row_mask:0xf bank_mask:0xf bound_ctrl:1
	v_mov_b32_e32 v6, 0
	v_mov_b32_e32 v4, 0
	v_add_f32_dpp v5, v5, v5 quad_perm:[2,3,0,1] row_mask:0xf bank_mask:0xf bound_ctrl:1
	s_nop 1
	v_mov_b32_dpp v6, v5 row_half_mirror row_mask:0xf bank_mask:0xf
	s_and_saveexec_b64 s[2:3], s[0:1]
	s_cbranch_execz .LBB0_3343
	v_add_f32_e32 v5, v5, v6
	v_mul_f32_e32 v5, v3, v5
	s_mov_b32 s14, 0x3e6d3388
	v_mul_f32_e32 v6, v5, v5
	s_waitcnt lgkmcnt(0)
	v_fma_f32 v7, |v5|, s14, 1.0
	v_rcp_f32_e32 v7, v7
	v_mov_b32_e32 v10, 0xbf3a00e3
	v_mul_f32_e32 v6, 0xbf38aa3b, v6
	v_exp_f32_e32 v6, v6
	v_fmac_f32_e32 v10, 0x3f07dc22, v7
	v_fmaak_f32 v10, v7, v10, 0x3f35f0e3
	v_fmaak_f32 v10, v7, v10, 0xbe11a98e
	v_fmaak_f32 v10, v7, v10, 0x3e027906
	v_mul_f32_e32 v7, v7, v10
	v_mul_f32_e32 v6, v6, v7
	v_mul_f32_e32 v7, v5, v6
	v_fma_f32 v6, -v5, v6, v5
	v_cmp_gt_f32_e32 vcc, 0, v5
	s_nop 1
	v_cndmask_b32_e32 v5, v6, v7, vcc
	s_waitcnt vmcnt(1)
	v_mul_f32_e32 v5, v5, v42
	s_waitcnt vmcnt(0)
	v_mul_f32_e32 v5, v5, v62
	ds_write_b32 v2, v5 offset:1088
.LBB0_3343:
	s_or_b64 exec, exec, s[2:3]
	v_add_f32_dpp v5, v124, v124 quad_perm:[1,0,3,2] row_mask:0xf bank_mask:0xf bound_ctrl:1
	s_nop 1
	v_add_f32_dpp v5, v5, v5 quad_perm:[2,3,0,1] row_mask:0xf bank_mask:0xf bound_ctrl:1
	s_nop 1
	v_mov_b32_dpp v4, v5 row_half_mirror row_mask:0xf bank_mask:0xf
	s_and_saveexec_b64 s[2:3], s[0:1]
	s_cbranch_execz .LBB0_3345
	v_add_f32_e32 v4, v5, v4
	v_mul_f32_e32 v4, v3, v4
	s_mov_b32 s14, 0x3e6d3388
	v_mul_f32_e32 v5, v4, v4
	s_waitcnt lgkmcnt(0)
	v_fma_f32 v6, |v4|, s14, 1.0
	v_rcp_f32_e32 v6, v6
	v_mov_b32_e32 v9, 0xbf3a00e3
	v_mul_f32_e32 v5, 0xbf38aa3b, v5
	v_exp_f32_e32 v5, v5
	v_fmac_f32_e32 v9, 0x3f07dc22, v6
	v_fmaak_f32 v9, v6, v9, 0x3f35f0e3
	v_fmaak_f32 v9, v6, v9, 0xbe11a98e
	v_fmaak_f32 v9, v6, v9, 0x3e027906
	v_mul_f32_e32 v6, v6, v9
	v_mul_f32_e32 v5, v5, v6
	v_mul_f32_e32 v6, v4, v5
	v_fma_f32 v5, -v4, v5, v4
	v_cmp_gt_f32_e32 vcc, 0, v4
	s_nop 1
	v_cndmask_b32_e32 v4, v5, v6, vcc
	s_waitcnt vmcnt(1)
	v_mul_f32_e32 v4, v4, v43
	s_waitcnt vmcnt(0)
	v_mul_f32_e32 v4, v4, v63
	ds_write_b32 v2, v4 offset:1120
.LBB0_3345:
	s_or_b64 exec, exec, s[2:3]
	v_add_f32_dpp v5, v123, v123 quad_perm:[1,0,3,2] row_mask:0xf bank_mask:0xf bound_ctrl:1
	v_mov_b32_e32 v6, 0
	v_mov_b32_e32 v4, 0
	v_add_f32_dpp v5, v5, v5 quad_perm:[2,3,0,1] row_mask:0xf bank_mask:0xf bound_ctrl:1
	s_nop 1
	v_mov_b32_dpp v6, v5 row_half_mirror row_mask:0xf bank_mask:0xf
	s_and_saveexec_b64 s[2:3], s[0:1]
	s_cbranch_execz .LBB0_3347
	v_add_f32_e32 v5, v5, v6
	v_mul_f32_e32 v5, v3, v5
	s_mov_b32 s14, 0x3e6d3388
	v_mul_f32_e32 v6, v5, v5
	s_waitcnt lgkmcnt(0)
	v_fma_f32 v7, |v5|, s14, 1.0
	v_rcp_f32_e32 v7, v7
	v_mov_b32_e32 v10, 0xbf3a00e3
	v_mul_f32_e32 v6, 0xbf38aa3b, v6
	v_exp_f32_e32 v6, v6
	v_fmac_f32_e32 v10, 0x3f07dc22, v7
	v_fmaak_f32 v10, v7, v10, 0x3f35f0e3
	v_fmaak_f32 v10, v7, v10, 0xbe11a98e
	v_fmaak_f32 v10, v7, v10, 0x3e027906
	v_mul_f32_e32 v7, v7, v10
	v_mul_f32_e32 v6, v6, v7
	v_mul_f32_e32 v7, v5, v6
	v_fma_f32 v6, -v5, v6, v5
	v_cmp_gt_f32_e32 vcc, 0, v5
	s_nop 1
	v_cndmask_b32_e32 v5, v6, v7, vcc
	s_waitcnt vmcnt(1)
	v_mul_f32_e32 v5, v5, v44
	s_waitcnt vmcnt(0)
	v_mul_f32_e32 v5, v5, v64
	ds_write_b32 v2, v5 offset:1152
.LBB0_3347:
	s_or_b64 exec, exec, s[2:3]
	v_add_f32_dpp v5, v122, v122 quad_perm:[1,0,3,2] row_mask:0xf bank_mask:0xf bound_ctrl:1
	s_nop 1
	v_add_f32_dpp v5, v5, v5 quad_perm:[2,3,0,1] row_mask:0xf bank_mask:0xf bound_ctrl:1
	s_nop 1
	v_mov_b32_dpp v4, v5 row_half_mirror row_mask:0xf bank_mask:0xf
	s_and_saveexec_b64 s[2:3], s[0:1]
	s_cbranch_execz .LBB0_3349
	v_add_f32_e32 v4, v5, v4
	v_mul_f32_e32 v4, v3, v4
	s_mov_b32 s14, 0x3e6d3388
	v_mul_f32_e32 v5, v4, v4
	s_waitcnt lgkmcnt(0)
	v_fma_f32 v6, |v4|, s14, 1.0
	v_rcp_f32_e32 v6, v6
	v_mov_b32_e32 v9, 0xbf3a00e3
	v_mul_f32_e32 v5, 0xbf38aa3b, v5
	v_exp_f32_e32 v5, v5
	v_fmac_f32_e32 v9, 0x3f07dc22, v6
	v_fmaak_f32 v9, v6, v9, 0x3f35f0e3
	v_fmaak_f32 v9, v6, v9, 0xbe11a98e
	v_fmaak_f32 v9, v6, v9, 0x3e027906
	v_mul_f32_e32 v6, v6, v9
	v_mul_f32_e32 v5, v5, v6
	v_mul_f32_e32 v6, v4, v5
	v_fma_f32 v5, -v4, v5, v4
	v_cmp_gt_f32_e32 vcc, 0, v4
	s_nop 1
	v_cndmask_b32_e32 v4, v5, v6, vcc
	s_waitcnt vmcnt(1)
	v_mul_f32_e32 v4, v4, v45
	s_waitcnt vmcnt(0)
	v_mul_f32_e32 v4, v4, v65
	ds_write_b32 v2, v4 offset:1184
.LBB0_3349:
	s_or_b64 exec, exec, s[2:3]
	v_add_f32_dpp v5, v121, v121 quad_perm:[1,0,3,2] row_mask:0xf bank_mask:0xf bound_ctrl:1
	v_mov_b32_e32 v6, 0
	v_mov_b32_e32 v4, 0
	v_add_f32_dpp v5, v5, v5 quad_perm:[2,3,0,1] row_mask:0xf bank_mask:0xf bound_ctrl:1
	s_nop 1
	v_mov_b32_dpp v6, v5 row_half_mirror row_mask:0xf bank_mask:0xf
	s_and_saveexec_b64 s[2:3], s[0:1]
	s_cbranch_execz .LBB0_3351
	v_add_f32_e32 v5, v5, v6
	v_mul_f32_e32 v5, v3, v5
	s_mov_b32 s14, 0x3e6d3388
	v_mul_f32_e32 v6, v5, v5
	s_waitcnt lgkmcnt(0)
	v_fma_f32 v7, |v5|, s14, 1.0
	v_rcp_f32_e32 v7, v7
	v_mov_b32_e32 v10, 0xbf3a00e3
	v_mul_f32_e32 v6, 0xbf38aa3b, v6
	v_exp_f32_e32 v6, v6
	v_fmac_f32_e32 v10, 0x3f07dc22, v7
	v_fmaak_f32 v10, v7, v10, 0x3f35f0e3
	v_fmaak_f32 v10, v7, v10, 0xbe11a98e
	v_fmaak_f32 v10, v7, v10, 0x3e027906
	v_mul_f32_e32 v7, v7, v10
	v_mul_f32_e32 v6, v6, v7
	v_mul_f32_e32 v7, v5, v6
	v_fma_f32 v6, -v5, v6, v5
	v_cmp_gt_f32_e32 vcc, 0, v5
	s_nop 1
	v_cndmask_b32_e32 v5, v6, v7, vcc
	s_waitcnt vmcnt(1)
	v_mul_f32_e32 v5, v5, v46
	s_waitcnt vmcnt(0)
	v_mul_f32_e32 v5, v5, v66
	ds_write_b32 v2, v5 offset:1216
; __device__ __forceinline__ void p12_peer(Frame& F) {
;     ...
;     for (int i = 0; i < 4; ++i) { const int t = F.gw + i * F.NGW;
; #pragma unroll
;         for (int b = 0; b < 16; ++b) { float d = psum[i][b];
;             d += __builtin_bit_cast(float, __builtin_amdgcn_update_dpp(0, __builtin_bit_cast(int, d), 0xB1, 0xF, 0xF, false));
;             d += __builtin_bit_cast(float, __builtin_amdgcn_update_dpp(0, __builtin_bit_cast(int, d), 0x4E, 0xF, 0xF, false));
;             d += __builtin_bit_cast(float, __builtin_amdgcn_update_dpp(0, __builtin_bit_cast(int, d), 0x141, 0xF, 0xF, false));
;             const int idx = b * 8 + g8; const float w = PGT[(size_t)t * 128 + idx] * gelu_erf(sx[i] * d) * VSC[EL[i * 128 + idx]];
;             if (k8 == 0) WL[i * 128 + idx] = w; } }
.LBB0_3351:
	s_or_b64 exec, exec, s[2:3]
	v_add_f32_dpp v5, v120, v120 quad_perm:[1,0,3,2] row_mask:0xf bank_mask:0xf bound_ctrl:1
	s_nop 1
	v_add_f32_dpp v5, v5, v5 quad_perm:[2,3,0,1] row_mask:0xf bank_mask:0xf bound_ctrl:1
	s_nop 1
	v_mov_b32_dpp v4, v5 row_half_mirror row_mask:0xf bank_mask:0xf
	s_and_saveexec_b64 s[2:3], s[0:1]
	s_cbranch_execz .LBB0_3353
	v_add_f32_e32 v4, v5, v4
	v_mul_f32_e32 v4, v3, v4
	s_mov_b32 s14, 0x3e6d3388
	v_mul_f32_e32 v5, v4, v4
	s_waitcnt lgkmcnt(0)
	v_fma_f32 v6, |v4|, s14, 1.0
	v_rcp_f32_e32 v6, v6
	v_mov_b32_e32 v9, 0xbf3a00e3
	v_mul_f32_e32 v5, 0xbf38aa3b, v5
	v_exp_f32_e32 v5, v5
	v_fmac_f32_e32 v9, 0x3f07dc22, v6
	v_fmaak_f32 v9, v6, v9, 0x3f35f0e3
	v_fmaak_f32 v9, v6, v9, 0xbe11a98e
	v_fmaak_f32 v9, v6, v9, 0x3e027906
	v_mul_f32_e32 v6, v6, v9
	v_mul_f32_e32 v5, v5, v6
	v_mul_f32_e32 v6, v4, v5
	v_fma_f32 v5, -v4, v5, v4
	v_cmp_gt_f32_e32 vcc, 0, v4
	s_nop 1
	v_cndmask_b32_e32 v4, v5, v6, vcc
	s_waitcnt vmcnt(1)
	v_mul_f32_e32 v4, v4, v47
	s_waitcnt vmcnt(0)
	v_mul_f32_e32 v4, v4, v67
	ds_write_b32 v2, v4 offset:1248
.LBB0_3353:
	s_or_b64 exec, exec, s[2:3]
	v_add_f32_dpp v5, v119, v119 quad_perm:[1,0,3,2] row_mask:0xf bank_mask:0xf bound_ctrl:1
	v_mov_b32_e32 v6, 0
	v_mov_b32_e32 v4, 0
	v_add_f32_dpp v5, v5, v5 quad_perm:[2,3,0,1] row_mask:0xf bank_mask:0xf bound_ctrl:1
	s_nop 1
	v_mov_b32_dpp v6, v5 row_half_mirror row_mask:0xf bank_mask:0xf
	s_and_saveexec_b64 s[2:3], s[0:1]
	s_cbranch_execz .LBB0_3355
	v_add_f32_e32 v5, v5, v6
	v_mul_f32_e32 v5, v3, v5
	s_mov_b32 s14, 0x3e6d3388
	v_mul_f32_e32 v6, v5, v5
	s_waitcnt lgkmcnt(0)
	v_fma_f32 v7, |v5|, s14, 1.0
	v_rcp_f32_e32 v7, v7
	v_mov_b32_e32 v10, 0xbf3a00e3
	v_mul_f32_e32 v6, 0xbf38aa3b, v6
	v_exp_f32_e32 v6, v6
	v_fmac_f32_e32 v10, 0x3f07dc22, v7
	v_fmaak_f32 v10, v7, v10, 0x3f35f0e3
	v_fmaak_f32 v10, v7, v10, 0xbe11a98e
	v_fmaak_f32 v10, v7, v10, 0x3e027906
	v_mul_f32_e32 v7, v7, v10
	v_mul_f32_e32 v6, v6, v7
	v_mul_f32_e32 v7, v5, v6
	v_fma_f32 v6, -v5, v6, v5
	v_cmp_gt_f32_e32 vcc, 0, v5
	s_nop 1
	v_cndmask_b32_e32 v5, v6, v7, vcc
	s_waitcnt vmcnt(1)
	v_mul_f32_e32 v5, v5, v48
	s_waitcnt vmcnt(0)
	v_mul_f32_e32 v5, v5, v68
	ds_write_b32 v2, v5 offset:1280
.LBB0_3355:
	s_or_b64 exec, exec, s[2:3]
	v_add_f32_dpp v5, v118, v118 quad_perm:[1,0,3,2] row_mask:0xf bank_mask:0xf bound_ctrl:1
	s_nop 1
	v_add_f32_dpp v5, v5, v5 quad_perm:[2,3,0,1] row_mask:0xf bank_mask:0xf bound_ctrl:1
	s_nop 1
	v_mov_b32_dpp v4, v5 row_half_mirror row_mask:0xf bank_mask:0xf
	s_and_saveexec_b64 s[2:3], s[0:1]
	s_cbranch_execz .LBB0_3357
	v_add_f32_e32 v4, v5, v4
	v_mul_f32_e32 v4, v3, v4
	s_mov_b32 s14, 0x3e6d3388
	v_mul_f32_e32 v5, v4, v4
	s_waitcnt lgkmcnt(0)
	v_fma_f32 v6, |v4|, s14, 1.0
	v_rcp_f32_e32 v6, v6
	v_mov_b32_e32 v9, 0xbf3a00e3
	v_mul_f32_e32 v5, 0xbf38aa3b, v5
	v_exp_f32_e32 v5, v5
	v_fmac_f32_e32 v9, 0x3f07dc22, v6
	v_fmaak_f32 v9, v6, v9, 0x3f35f0e3
	v_fmaak_f32 v9, v6, v9, 0xbe11a98e
	v_fmaak_f32 v9, v6, v9, 0x3e027906
	v_mul_f32_e32 v6, v6, v9
	v_mul_f32_e32 v5, v5, v6
	v_mul_f32_e32 v6, v4, v5
	v_fma_f32 v5, -v4, v5, v4
	v_cmp_gt_f32_e32 vcc, 0, v4
	s_nop 1
	v_cndmask_b32_e32 v4, v5, v6, vcc
	s_waitcnt vmcnt(1)
	v_mul_f32_e32 v4, v4, v49
	s_waitcnt vmcnt(0)
	v_mul_f32_e32 v4, v4, v69
	ds_write_b32 v2, v4 offset:1312
.LBB0_3357:
	s_or_b64 exec, exec, s[2:3]
	v_add_f32_dpp v5, v117, v117 quad_perm:[1,0,3,2] row_mask:0xf bank_mask:0xf bound_ctrl:1
	v_mov_b32_e32 v6, 0
	v_mov_b32_e32 v4, 0
	v_add_f32_dpp v5, v5, v5 quad_perm:[2,3,0,1] row_mask:0xf bank_mask:0xf bound_ctrl:1
	s_nop 1
	v_mov_b32_dpp v6, v5 row_half_mirror row_mask:0xf bank_mask:0xf
	s_and_saveexec_b64 s[2:3], s[0:1]
	s_cbranch_execz .LBB0_3359
	v_add_f32_e32 v5, v5, v6
	v_mul_f32_e32 v5, v3, v5
	s_mov_b32 s14, 0x3e6d3388
	v_mul_f32_e32 v6, v5, v5
	s_waitcnt lgkmcnt(0)
	v_fma_f32 v7, |v5|, s14, 1.0
	v_rcp_f32_e32 v7, v7
	v_mov_b32_e32 v10, 0xbf3a00e3
	v_mul_f32_e32 v6, 0xbf38aa3b, v6
	v_exp_f32_e32 v6, v6
	v_fmac_f32_e32 v10, 0x3f07dc22, v7
	v_fmaak_f32 v10, v7, v10, 0x3f35f0e3
	v_fmaak_f32 v10, v7, v10, 0xbe11a98e
	v_fmaak_f32 v10, v7, v10, 0x3e027906
	v_mul_f32_e32 v7, v7, v10
	v_mul_f32_e32 v6, v6, v7
	v_mul_f32_e32 v7, v5, v6
	v_fma_f32 v6, -v5, v6, v5
	v_cmp_gt_f32_e32 vcc, 0, v5
	s_nop 1
	v_cndmask_b32_e32 v5, v6, v7, vcc
	s_waitcnt vmcnt(1)
	v_mul_f32_e32 v5, v5, v50
	s_waitcnt vmcnt(0)
	v_mul_f32_e32 v5, v5, v70
	ds_write_b32 v2, v5 offset:1344
.LBB0_3359:
	s_or_b64 exec, exec, s[2:3]
	v_add_f32_dpp v5, v116, v116 quad_perm:[1,0,3,2] row_mask:0xf bank_mask:0xf bound_ctrl:1
	s_nop 1
	v_add_f32_dpp v5, v5, v5 quad_perm:[2,3,0,1] row_mask:0xf bank_mask:0xf bound_ctrl:1
	s_nop 1
	v_mov_b32_dpp v4, v5 row_half_mirror row_mask:0xf bank_mask:0xf
	s_and_saveexec_b64 s[2:3], s[0:1]
	s_cbranch_execz .LBB0_3361
	v_add_f32_e32 v4, v5, v4
	v_mul_f32_e32 v4, v3, v4
	s_mov_b32 s14, 0x3e6d3388
	v_mul_f32_e32 v5, v4, v4
	s_waitcnt lgkmcnt(0)
	v_fma_f32 v6, |v4|, s14, 1.0
	v_rcp_f32_e32 v6, v6
	v_mov_b32_e32 v9, 0xbf3a00e3
	v_mul_f32_e32 v5, 0xbf38aa3b, v5
	v_exp_f32_e32 v5, v5
	v_fmac_f32_e32 v9, 0x3f07dc22, v6
	v_fmaak_f32 v9, v6, v9, 0x3f35f0e3
	v_fmaak_f32 v9, v6, v9, 0xbe11a98e
	v_fmaak_f32 v9, v6, v9, 0x3e027906
	v_mul_f32_e32 v6, v6, v9
	v_mul_f32_e32 v5, v5, v6
	v_mul_f32_e32 v6, v4, v5
	v_fma_f32 v5, -v4, v5, v4
	v_cmp_gt_f32_e32 vcc, 0, v4
	s_nop 1
	v_cndmask_b32_e32 v4, v5, v6, vcc
	s_waitcnt vmcnt(1)
	v_mul_f32_e32 v4, v4, v51
	s_waitcnt vmcnt(0)
	v_mul_f32_e32 v4, v4, v71
	ds_write_b32 v2, v4 offset:1376
; __device__ __forceinline__ void p12_peer(Frame& F) {
;     ...
;     for (int i = 0; i < 4; ++i) { const int t = F.gw + i * F.NGW;
; #pragma unroll
;         for (int b = 0; b < 16; ++b) { float d = psum[i][b];
;             d += __builtin_bit_cast(float, __builtin_amdgcn_update_dpp(0, __builtin_bit_cast(int, d), 0xB1, 0xF, 0xF, false));
;             d += __builtin_bit_cast(float, __builtin_amdgcn_update_dpp(0, __builtin_bit_cast(int, d), 0x4E, 0xF, 0xF, false));
;             d += __builtin_bit_cast(float, __builtin_amdgcn_update_dpp(0, __builtin_bit_cast(int, d), 0x141, 0xF, 0xF, false));
;             const int idx = b * 8 + g8; const float w = PGT[(size_t)t * 128 + idx] * gelu_erf(sx[i] * d) * VSC[EL[i * 128 + idx]];
;             if (k8 == 0) WL[i * 128 + idx] = w; } }
.LBB0_3361:
	s_or_b64 exec, exec, s[2:3]
	v_add_f32_dpp v5, v115, v115 quad_perm:[1,0,3,2] row_mask:0xf bank_mask:0xf bound_ctrl:1
	v_mov_b32_e32 v6, 0
	v_mov_b32_e32 v4, 0
	v_add_f32_dpp v5, v5, v5 quad_perm:[2,3,0,1] row_mask:0xf bank_mask:0xf bound_ctrl:1
	s_nop 1
	v_mov_b32_dpp v6, v5 row_half_mirror row_mask:0xf bank_mask:0xf
	s_and_saveexec_b64 s[2:3], s[0:1]
	s_cbranch_execz .LBB0_3363
	v_add_f32_e32 v5, v5, v6
	v_mul_f32_e32 v5, v3, v5
	s_mov_b32 s14, 0x3e6d3388
	v_mul_f32_e32 v6, v5, v5
	s_waitcnt lgkmcnt(0)
	v_fma_f32 v7, |v5|, s14, 1.0
	v_rcp_f32_e32 v7, v7
	v_mov_b32_e32 v10, 0xbf3a00e3
	v_mul_f32_e32 v6, 0xbf38aa3b, v6
	v_exp_f32_e32 v6, v6
	v_fmac_f32_e32 v10, 0x3f07dc22, v7
	v_fmaak_f32 v10, v7, v10, 0x3f35f0e3
	v_fmaak_f32 v10, v7, v10, 0xbe11a98e
	v_fmaak_f32 v10, v7, v10, 0x3e027906
	v_mul_f32_e32 v7, v7, v10
	v_mul_f32_e32 v6, v6, v7
	v_mul_f32_e32 v7, v5, v6
	v_fma_f32 v6, -v5, v6, v5
	v_cmp_gt_f32_e32 vcc, 0, v5
	s_nop 1
	v_cndmask_b32_e32 v5, v6, v7, vcc
	s_waitcnt vmcnt(1)
	v_mul_f32_e32 v5, v5, v52
	s_waitcnt vmcnt(0)
	v_mul_f32_e32 v5, v5, v72
	ds_write_b32 v2, v5 offset:1408
.LBB0_3363:
	s_or_b64 exec, exec, s[2:3]
	v_add_f32_dpp v5, v114, v114 quad_perm:[1,0,3,2] row_mask:0xf bank_mask:0xf bound_ctrl:1
	s_nop 1
	v_add_f32_dpp v5, v5, v5 quad_perm:[2,3,0,1] row_mask:0xf bank_mask:0xf bound_ctrl:1
	s_nop 1
	v_mov_b32_dpp v4, v5 row_half_mirror row_mask:0xf bank_mask:0xf
	s_and_saveexec_b64 s[2:3], s[0:1]
	s_cbranch_execz .LBB0_3365
	v_add_f32_e32 v4, v5, v4
	v_mul_f32_e32 v4, v3, v4
	s_mov_b32 s14, 0x3e6d3388
	v_mul_f32_e32 v5, v4, v4
	s_waitcnt lgkmcnt(0)
	v_fma_f32 v6, |v4|, s14, 1.0
	v_rcp_f32_e32 v6, v6
	v_mov_b32_e32 v9, 0xbf3a00e3
	v_mul_f32_e32 v5, 0xbf38aa3b, v5
	v_exp_f32_e32 v5, v5
	v_fmac_f32_e32 v9, 0x3f07dc22, v6
	v_fmaak_f32 v9, v6, v9, 0x3f35f0e3
	v_fmaak_f32 v9, v6, v9, 0xbe11a98e
	v_fmaak_f32 v9, v6, v9, 0x3e027906
	v_mul_f32_e32 v6, v6, v9
	v_mul_f32_e32 v5, v5, v6
	v_mul_f32_e32 v6, v4, v5
	v_fma_f32 v5, -v4, v5, v4
	v_cmp_gt_f32_e32 vcc, 0, v4
	s_nop 1
	v_cndmask_b32_e32 v4, v5, v6, vcc
	s_waitcnt vmcnt(1)
	v_mul_f32_e32 v4, v4, v53
	s_waitcnt vmcnt(0)
	v_mul_f32_e32 v4, v4, v73
	ds_write_b32 v2, v4 offset:1440
.LBB0_3365:
	s_or_b64 exec, exec, s[2:3]
	v_add_f32_dpp v5, v113, v113 quad_perm:[1,0,3,2] row_mask:0xf bank_mask:0xf bound_ctrl:1
	v_mov_b32_e32 v6, 0
	v_mov_b32_e32 v4, 0
	v_add_f32_dpp v5, v5, v5 quad_perm:[2,3,0,1] row_mask:0xf bank_mask:0xf bound_ctrl:1
	s_nop 1
	v_mov_b32_dpp v6, v5 row_half_mirror row_mask:0xf bank_mask:0xf
	s_and_saveexec_b64 s[2:3], s[0:1]
	s_cbranch_execz .LBB0_3367
	v_add_f32_e32 v5, v5, v6
	v_mul_f32_e32 v5, v3, v5
	s_mov_b32 s14, 0x3e6d3388
	v_mul_f32_e32 v6, v5, v5
	s_waitcnt lgkmcnt(0)
	v_fma_f32 v7, |v5|, s14, 1.0
	v_rcp_f32_e32 v7, v7
	v_mov_b32_e32 v10, 0xbf3a00e3
	v_mul_f32_e32 v6, 0xbf38aa3b, v6
	v_exp_f32_e32 v6, v6
	v_fmac_f32_e32 v10, 0x3f07dc22, v7
	v_fmaak_f32 v10, v7, v10, 0x3f35f0e3
	v_fmaak_f32 v10, v7, v10, 0xbe11a98e
	v_fmaak_f32 v10, v7, v10, 0x3e027906
	v_mul_f32_e32 v7, v7, v10
	v_mul_f32_e32 v6, v6, v7
	v_mul_f32_e32 v7, v5, v6
	v_fma_f32 v6, -v5, v6, v5
	v_cmp_gt_f32_e32 vcc, 0, v5
	s_nop 1
	v_cndmask_b32_e32 v5, v6, v7, vcc
	s_waitcnt vmcnt(1)
	v_mul_f32_e32 v5, v5, v54
	s_waitcnt vmcnt(0)
	v_mul_f32_e32 v5, v5, v74
	ds_write_b32 v2, v5 offset:1472
.LBB0_3367:
	s_or_b64 exec, exec, s[2:3]
	v_add_f32_dpp v5, v112, v112 quad_perm:[1,0,3,2] row_mask:0xf bank_mask:0xf bound_ctrl:1
	s_nop 1
	v_add_f32_dpp v5, v5, v5 quad_perm:[2,3,0,1] row_mask:0xf bank_mask:0xf bound_ctrl:1
	s_nop 1
	v_mov_b32_dpp v4, v5 row_half_mirror row_mask:0xf bank_mask:0xf
	s_and_saveexec_b64 s[2:3], s[0:1]
	s_cbranch_execz .LBB0_3369
	s_mov_b32 s14, 0x3e6d3388
	s_waitcnt lgkmcnt(0)
	v_add_f32_e32 v0, v5, v4
	v_mul_f32_e32 v0, v3, v0
	v_fma_f32 v3, |v0|, s14, 1.0
	v_rcp_f32_e32 v3, v3
	v_mul_f32_e32 v1, v0, v0
	v_mov_b32_e32 v4, 0xbf3a00e3
	v_mul_f32_e32 v1, 0xbf38aa3b, v1
	v_fmac_f32_e32 v4, 0x3f07dc22, v3
	v_exp_f32_e32 v1, v1
	v_fmaak_f32 v4, v3, v4, 0x3f35f0e3
	v_fmaak_f32 v4, v3, v4, 0xbe11a98e
	v_fmaak_f32 v4, v3, v4, 0x3e027906
	v_mul_f32_e32 v3, v3, v4
	v_mul_f32_e32 v1, v1, v3
	v_mul_f32_e32 v3, v0, v1
	v_fma_f32 v1, -v0, v1, v0
	v_cmp_gt_f32_e32 vcc, 0, v0
	s_nop 1
	v_cndmask_b32_e32 v0, v1, v3, vcc
	s_waitcnt vmcnt(1)
	v_mul_f32_e32 v0, v0, v55
	s_waitcnt vmcnt(0)
	v_mul_f32_e32 v0, v0, v75
	ds_write_b32 v2, v0 offset:1504
; #define LDS_WAIT() asm volatile("s_waitcnt lgkmcnt(0)" ::: "memory")
; __device__ __forceinline__ float wave_sum(float v) { v = dpp_add16(v); return (rdlane(v, 0) + rdlane(v, 16)) + (rdlane(v, 32) + rdlane(v, 48)); }
; __device__ __forceinline__ void p12_peer(Frame& F) {
;     ...
;         const float rsn = 1.0f / sqrtf(wave_sum(PSQ[(size_t)t * 64 + F.lane]) * (1.f / D_) + 1e-6f);
;         sx[i] = mxa * rsn * (1.0f / 127.0f);
;     ...
;     asm volatile("" ::: "memory"); LDS_WAIT();
; #pragma unroll
;     for (int i = 0; i < 4; ++i) { const int t = F.gw + i * F.NGW;
; #pragma unroll
;         for (int b = 0; b < 16; ++b) { float d = psum[i][b];
;             d += __builtin_bit_cast(float, __builtin_amdgcn_update_dpp(0, __builtin_bit_cast(int, d), 0xB1, 0xF, 0xF, false));
;             d += __builtin_bit_cast(float, __builtin_amdgcn_update_dpp(0, __builtin_bit_cast(int, d), 0x4E, 0xF, 0xF, false));
;             d += __builtin_bit_cast(float, __builtin_amdgcn_update_dpp(0, __builtin_bit_cast(int, d), 0x141, 0xF, 0xF, false));
;             const int idx = b * 8 + g8; const float w = PGT[(size_t)t * 128 + idx] * gelu_erf(sx[i] * d) * VSC[EL[i * 128 + idx]];
;             if (k8 == 0) WL[i * 128 + idx] = w; } }
.LBB0_3369:
	s_or_b64 exec, exec, s[2:3]
	v_mov_b32_e32 v0, s23
	v_mov_b32_e32 v1, s28
	v_add_f32_e32 v0, s21, v0
	v_add_f32_e32 v1, s22, v1
	v_add_f32_e32 v0, v0, v1
	v_mov_b32_e32 v1, 0x358637bd
	v_fmac_f32_e32 v1, 0x39800000, v0
	s_mov_b32 s2, 0xf800000
	v_mul_f32_e32 v0, 0x4f800000, v1
	v_cmp_gt_f32_e32 vcc, s2, v1
	s_nop 1
	v_cndmask_b32_e32 v0, v1, v0, vcc
	v_sqrt_f32_e32 v1, v0
	s_nop 0
	v_add_u32_e32 v3, -1, v1
	v_fma_f32 v4, -v3, v1, v0
	v_cmp_ge_f32_e64 s[2:3], 0, v4
	v_add_u32_e32 v4, 1, v1
	s_nop 0
	v_cndmask_b32_e64 v3, v1, v3, s[2:3]
	v_fma_f32 v1, -v4, v1, v0
	v_cmp_lt_f32_e64 s[2:3], 0, v1
	s_nop 1
	v_cndmask_b32_e64 v1, v3, v4, s[2:3]
	v_mul_f32_e32 v3, 0x37800000, v1
	v_cndmask_b32_e32 v1, v1, v3, vcc
	v_mov_b32_e32 v3, 0x260
	v_cmp_class_f32_e32 vcc, v0, v3
	s_nop 1
	v_cndmask_b32_e32 v0, v1, v0, vcc
	v_div_scale_f32 v1, s[2:3], v0, v0, 1.0
	v_rcp_f32_e32 v3, v1
	s_add_u32 s2, s43, s12
	s_addc_u32 s3, s44, s13
	v_fma_f32 v4, -v1, v3, 1.0
	v_fmac_f32_e32 v3, v4, v3
	v_div_scale_f32 v4, vcc, 1.0, v0, 1.0
	v_mul_f32_e32 v5, v4, v3
	v_fma_f32 v6, -v1, v5, v4
	v_fmac_f32_e32 v5, v6, v3
	v_fma_f32 v1, -v1, v5, v4
	v_div_fmas_f32 v1, v1, v3, v5
	v_div_fixup_f32 v0, v1, v0, 1.0
	v_add_f32_dpp v5, v111, v111 quad_perm:[1,0,3,2] row_mask:0xf bank_mask:0xf bound_ctrl:1
	v_mul_f32_e32 v0, v160, v0
	v_mov_b32_e32 v6, 0
	v_add_f32_dpp v5, v5, v5 quad_perm:[2,3,0,1] row_mask:0xf bank_mask:0xf bound_ctrl:1
	v_mul_f32_e32 v3, 0x3c010204, v0
	v_lshl_add_u64 v[0:1], v[94:95], 2, s[2:3]
	ds_read_u16 v20, v93 offset:17152
	ds_read_u16 v21, v93 offset:17168
	ds_read_u16 v22, v93 offset:17184
	ds_read_u16 v23, v93 offset:17200
	ds_read_u16 v24, v93 offset:17216
	ds_read_u16 v25, v93 offset:17232
	ds_read_u16 v26, v93 offset:17248
	ds_read_u16 v27, v93 offset:17264
	s_waitcnt lgkmcnt(0)
	ds_read_u16 v28, v93 offset:17280
	ds_read_u16 v29, v93 offset:17296
	ds_read_u16 v30, v93 offset:17312
	ds_read_u16 v31, v93 offset:17328
	ds_read_u16 v32, v93 offset:17344
	ds_read_u16 v33, v93 offset:17360
	ds_read_u16 v34, v93 offset:17376
	ds_read_u16 v35, v93 offset:17392
	s_waitcnt lgkmcnt(0)
	v_lshlrev_b32_e32 v20, 2, v20
	v_lshlrev_b32_e32 v21, 2, v21
	v_lshlrev_b32_e32 v22, 2, v22
	v_lshlrev_b32_e32 v23, 2, v23
	v_lshlrev_b32_e32 v24, 2, v24
	v_lshlrev_b32_e32 v25, 2, v25
	v_lshlrev_b32_e32 v26, 2, v26
	v_lshlrev_b32_e32 v27, 2, v27
	v_lshlrev_b32_e32 v28, 2, v28
	v_lshlrev_b32_e32 v29, 2, v29
	v_lshlrev_b32_e32 v30, 2, v30
	v_lshlrev_b32_e32 v31, 2, v31
	v_lshlrev_b32_e32 v32, 2, v32
	v_lshlrev_b32_e32 v33, 2, v33
	v_lshlrev_b32_e32 v34, 2, v34
	v_lshlrev_b32_e32 v35, 2, v35
	global_load_dword v40, v[0:1], off offset:0
	global_load_dword v60, v20, s[18:19]
	global_load_dword v41, v[0:1], off offset:32
	global_load_dword v61, v21, s[18:19]
	global_load_dword v42, v[0:1], off offset:64
	global_load_dword v62, v22, s[18:19]
	global_load_dword v43, v[0:1], off offset:96
	global_load_dword v63, v23, s[18:19]
	global_load_dword v44, v[0:1], off offset:128
	global_load_dword v64, v24, s[18:19]
	global_load_dword v45, v[0:1], off offset:160
	global_load_dword v65, v25, s[18:19]
	global_load_dword v46, v[0:1], off offset:192
	global_load_dword v66, v26, s[18:19]
	global_load_dword v47, v[0:1], off offset:224
	global_load_dword v67, v27, s[18:19]
	global_load_dword v48, v[0:1], off offset:256
	global_load_dword v68, v28, s[18:19]
	global_load_dword v49, v[0:1], off offset:288
	global_load_dword v69, v29, s[18:19]
	global_load_dword v50, v[0:1], off offset:320
	global_load_dword v70, v30, s[18:19]
	global_load_dword v51, v[0:1], off offset:352
	global_load_dword v71, v31, s[18:19]
	global_load_dword v52, v[0:1], off offset:384
	global_load_dword v72, v32, s[18:19]
	global_load_dword v53, v[0:1], off offset:416
	global_load_dword v73, v33, s[18:19]
	global_load_dword v54, v[0:1], off offset:448
	global_load_dword v74, v34, s[18:19]
	global_load_dword v55, v[0:1], off offset:480
	global_load_dword v75, v35, s[18:19]
	s_waitcnt vmcnt(0)
	v_mov_b32_e32 v4, 0
	v_mov_b32_dpp v6, v5 row_half_mirror row_mask:0xf bank_mask:0xf
	s_and_saveexec_b64 s[2:3], s[0:1]
	s_cbranch_execz .LBB0_3371
	v_add_f32_e32 v5, v5, v6
	v_mul_f32_e32 v5, v3, v5
	s_mov_b32 s12, 0x3e6d3388
	v_mul_f32_e32 v6, v5, v5
	s_waitcnt lgkmcnt(0)
	v_fma_f32 v7, |v5|, s12, 1.0
	v_rcp_f32_e32 v7, v7
	v_mov_b32_e32 v10, 0xbf3a00e3
	v_mul_f32_e32 v6, 0xbf38aa3b, v6
	v_exp_f32_e32 v6, v6
	v_fmac_f32_e32 v10, 0x3f07dc22, v7
	v_fmaak_f32 v10, v7, v10, 0x3f35f0e3
	v_fmaak_f32 v10, v7, v10, 0xbe11a98e
	v_fmaak_f32 v10, v7, v10, 0x3e027906
	v_mul_f32_e32 v7, v7, v10
	v_mul_f32_e32 v6, v6, v7
	v_mul_f32_e32 v7, v5, v6
	v_fma_f32 v6, -v5, v6, v5
	v_cmp_gt_f32_e32 vcc, 0, v5
	s_nop 1
	v_cndmask_b32_e32 v5, v6, v7, vcc
	s_waitcnt vmcnt(1)
	v_mul_f32_e32 v5, v5, v40
	s_waitcnt vmcnt(0)
	v_mul_f32_e32 v5, v5, v60
	ds_write_b32 v2, v5 offset:1536
.LBB0_3371:
	s_or_b64 exec, exec, s[2:3]
	v_add_f32_dpp v5, v110, v110 quad_perm:[1,0,3,2] row_mask:0xf bank_mask:0xf bound_ctrl:1
	s_nop 1
	v_add_f32_dpp v5, v5, v5 quad_perm:[2,3,0,1] row_mask:0xf bank_mask:0xf bound_ctrl:1
	s_nop 1
	v_mov_b32_dpp v4, v5 row_half_mirror row_mask:0xf bank_mask:0xf
	s_and_saveexec_b64 s[2:3], s[0:1]
	s_cbranch_execz .LBB0_3373
	v_add_f32_e32 v4, v5, v4
	v_mul_f32_e32 v4, v3, v4
	s_mov_b32 s12, 0x3e6d3388
	v_mul_f32_e32 v5, v4, v4
	s_waitcnt lgkmcnt(0)
	v_fma_f32 v6, |v4|, s12, 1.0
	v_rcp_f32_e32 v6, v6
	v_mov_b32_e32 v9, 0xbf3a00e3
	v_mul_f32_e32 v5, 0xbf38aa3b, v5
	v_exp_f32_e32 v5, v5
	v_fmac_f32_e32 v9, 0x3f07dc22, v6
	v_fmaak_f32 v9, v6, v9, 0x3f35f0e3
	v_fmaak_f32 v9, v6, v9, 0xbe11a98e
	v_fmaak_f32 v9, v6, v9, 0x3e027906
	v_mul_f32_e32 v6, v6, v9
	v_mul_f32_e32 v5, v5, v6
	v_mul_f32_e32 v6, v4, v5
	v_fma_f32 v5, -v4, v5, v4
	v_cmp_gt_f32_e32 vcc, 0, v4
	s_nop 1
	v_cndmask_b32_e32 v4, v5, v6, vcc
	s_waitcnt vmcnt(1)
	v_mul_f32_e32 v4, v4, v41
	s_waitcnt vmcnt(0)
	v_mul_f32_e32 v4, v4, v61
	ds_write_b32 v2, v4 offset:1568
; __device__ __forceinline__ void p12_peer(Frame& F) {
;     ...
;     for (int i = 0; i < 4; ++i) { const int t = F.gw + i * F.NGW;
; #pragma unroll
;         for (int b = 0; b < 16; ++b) { float d = psum[i][b];
;             d += __builtin_bit_cast(float, __builtin_amdgcn_update_dpp(0, __builtin_bit_cast(int, d), 0xB1, 0xF, 0xF, false));
;             d += __builtin_bit_cast(float, __builtin_amdgcn_update_dpp(0, __builtin_bit_cast(int, d), 0x4E, 0xF, 0xF, false));
;             d += __builtin_bit_cast(float, __builtin_amdgcn_update_dpp(0, __builtin_bit_cast(int, d), 0x141, 0xF, 0xF, false));
;             const int idx = b * 8 + g8; const float w = PGT[(size_t)t * 128 + idx] * gelu_erf(sx[i] * d) * VSC[EL[i * 128 + idx]];
;             if (k8 == 0) WL[i * 128 + idx] = w; } }
.LBB0_3373:
	s_or_b64 exec, exec, s[2:3]
	v_add_f32_dpp v5, v109, v109 quad_perm:[1,0,3,2] row_mask:0xf bank_mask:0xf bound_ctrl:1
	v_mov_b32_e32 v6, 0
	v_mov_b32_e32 v4, 0
	v_add_f32_dpp v5, v5, v5 quad_perm:[2,3,0,1] row_mask:0xf bank_mask:0xf bound_ctrl:1
	s_nop 1
	v_mov_b32_dpp v6, v5 row_half_mirror row_mask:0xf bank_mask:0xf
	s_and_saveexec_b64 s[2:3], s[0:1]
	s_cbranch_execz .LBB0_3375
	v_add_f32_e32 v5, v5, v6
	v_mul_f32_e32 v5, v3, v5
	s_mov_b32 s12, 0x3e6d3388
	v_mul_f32_e32 v6, v5, v5
	s_waitcnt lgkmcnt(0)
	v_fma_f32 v7, |v5|, s12, 1.0
	v_rcp_f32_e32 v7, v7
	v_mov_b32_e32 v10, 0xbf3a00e3
	v_mul_f32_e32 v6, 0xbf38aa3b, v6
	v_exp_f32_e32 v6, v6
	v_fmac_f32_e32 v10, 0x3f07dc22, v7
	v_fmaak_f32 v10, v7, v10, 0x3f35f0e3
	v_fmaak_f32 v10, v7, v10, 0xbe11a98e
	v_fmaak_f32 v10, v7, v10, 0x3e027906
	v_mul_f32_e32 v7, v7, v10
	v_mul_f32_e32 v6, v6, v7
	v_mul_f32_e32 v7, v5, v6
	v_fma_f32 v6, -v5, v6, v5
	v_cmp_gt_f32_e32 vcc, 0, v5
	s_nop 1
	v_cndmask_b32_e32 v5, v6, v7, vcc
	s_waitcnt vmcnt(1)
	v_mul_f32_e32 v5, v5, v42
	s_waitcnt vmcnt(0)
	v_mul_f32_e32 v5, v5, v62
	ds_write_b32 v2, v5 offset:1600
.LBB0_3375:
	s_or_b64 exec, exec, s[2:3]
	v_add_f32_dpp v5, v108, v108 quad_perm:[1,0,3,2] row_mask:0xf bank_mask:0xf bound_ctrl:1
	s_nop 1
	v_add_f32_dpp v5, v5, v5 quad_perm:[2,3,0,1] row_mask:0xf bank_mask:0xf bound_ctrl:1
	s_nop 1
	v_mov_b32_dpp v4, v5 row_half_mirror row_mask:0xf bank_mask:0xf
	s_and_saveexec_b64 s[2:3], s[0:1]
	s_cbranch_execz .LBB0_3377
	v_add_f32_e32 v4, v5, v4
	v_mul_f32_e32 v4, v3, v4
	s_mov_b32 s12, 0x3e6d3388
	v_mul_f32_e32 v5, v4, v4
	s_waitcnt lgkmcnt(0)
	v_fma_f32 v6, |v4|, s12, 1.0
	v_rcp_f32_e32 v6, v6
	v_mov_b32_e32 v9, 0xbf3a00e3
	v_mul_f32_e32 v5, 0xbf38aa3b, v5
	v_exp_f32_e32 v5, v5
	v_fmac_f32_e32 v9, 0x3f07dc22, v6
	v_fmaak_f32 v9, v6, v9, 0x3f35f0e3
	v_fmaak_f32 v9, v6, v9, 0xbe11a98e
	v_fmaak_f32 v9, v6, v9, 0x3e027906
	v_mul_f32_e32 v6, v6, v9
	v_mul_f32_e32 v5, v5, v6
	v_mul_f32_e32 v6, v4, v5
	v_fma_f32 v5, -v4, v5, v4
	v_cmp_gt_f32_e32 vcc, 0, v4
	s_nop 1
	v_cndmask_b32_e32 v4, v5, v6, vcc
	s_waitcnt vmcnt(1)
	v_mul_f32_e32 v4, v4, v43
	s_waitcnt vmcnt(0)
	v_mul_f32_e32 v4, v4, v63
	ds_write_b32 v2, v4 offset:1632
.LBB0_3377:
	s_or_b64 exec, exec, s[2:3]
	v_add_f32_dpp v5, v106, v106 quad_perm:[1,0,3,2] row_mask:0xf bank_mask:0xf bound_ctrl:1
	v_mov_b32_e32 v6, 0
	v_mov_b32_e32 v4, 0
	v_add_f32_dpp v5, v5, v5 quad_perm:[2,3,0,1] row_mask:0xf bank_mask:0xf bound_ctrl:1
	s_nop 1
	v_mov_b32_dpp v6, v5 row_half_mirror row_mask:0xf bank_mask:0xf
	s_and_saveexec_b64 s[2:3], s[0:1]
	s_cbranch_execz .LBB0_3379
	v_add_f32_e32 v5, v5, v6
	v_mul_f32_e32 v5, v3, v5
	s_mov_b32 s12, 0x3e6d3388
	v_mul_f32_e32 v6, v5, v5
	s_waitcnt lgkmcnt(0)
	v_fma_f32 v7, |v5|, s12, 1.0
	v_rcp_f32_e32 v7, v7
	v_mov_b32_e32 v10, 0xbf3a00e3
	v_mul_f32_e32 v6, 0xbf38aa3b, v6
	v_exp_f32_e32 v6, v6
	v_fmac_f32_e32 v10, 0x3f07dc22, v7
	v_fmaak_f32 v10, v7, v10, 0x3f35f0e3
	v_fmaak_f32 v10, v7, v10, 0xbe11a98e
	v_fmaak_f32 v10, v7, v10, 0x3e027906
	v_mul_f32_e32 v7, v7, v10
	v_mul_f32_e32 v6, v6, v7
	v_mul_f32_e32 v7, v5, v6
	v_fma_f32 v6, -v5, v6, v5
	v_cmp_gt_f32_e32 vcc, 0, v5
	s_nop 1
	v_cndmask_b32_e32 v5, v6, v7, vcc
	s_waitcnt vmcnt(1)
	v_mul_f32_e32 v5, v5, v44
	s_waitcnt vmcnt(0)
	v_mul_f32_e32 v5, v5, v64
	ds_write_b32 v2, v5 offset:1664
.LBB0_3379:
	s_or_b64 exec, exec, s[2:3]
	v_add_f32_dpp v5, v107, v107 quad_perm:[1,0,3,2] row_mask:0xf bank_mask:0xf bound_ctrl:1
	s_nop 1
	v_add_f32_dpp v5, v5, v5 quad_perm:[2,3,0,1] row_mask:0xf bank_mask:0xf bound_ctrl:1
	s_nop 1
	v_mov_b32_dpp v4, v5 row_half_mirror row_mask:0xf bank_mask:0xf
	s_and_saveexec_b64 s[2:3], s[0:1]
	s_cbranch_execz .LBB0_3381
	v_add_f32_e32 v4, v5, v4
	v_mul_f32_e32 v4, v3, v4
	s_mov_b32 s12, 0x3e6d3388
	v_mul_f32_e32 v5, v4, v4
	s_waitcnt lgkmcnt(0)
	v_fma_f32 v6, |v4|, s12, 1.0
	v_rcp_f32_e32 v6, v6
	v_mov_b32_e32 v9, 0xbf3a00e3
	v_mul_f32_e32 v5, 0xbf38aa3b, v5
	v_exp_f32_e32 v5, v5
	v_fmac_f32_e32 v9, 0x3f07dc22, v6
	v_fmaak_f32 v9, v6, v9, 0x3f35f0e3
	v_fmaak_f32 v9, v6, v9, 0xbe11a98e
	v_fmaak_f32 v9, v6, v9, 0x3e027906
	v_mul_f32_e32 v6, v6, v9
	v_mul_f32_e32 v5, v5, v6
	v_mul_f32_e32 v6, v4, v5
	v_fma_f32 v5, -v4, v5, v4
	v_cmp_gt_f32_e32 vcc, 0, v4
	s_nop 1
	v_cndmask_b32_e32 v4, v5, v6, vcc
	s_waitcnt vmcnt(1)
	v_mul_f32_e32 v4, v4, v45
	s_waitcnt vmcnt(0)
	v_mul_f32_e32 v4, v4, v65
	ds_write_b32 v2, v4 offset:1696
.LBB0_3381:
	s_or_b64 exec, exec, s[2:3]
	v_add_f32_dpp v5, v104, v104 quad_perm:[1,0,3,2] row_mask:0xf bank_mask:0xf bound_ctrl:1
	v_mov_b32_e32 v6, 0
	v_mov_b32_e32 v4, 0
	v_add_f32_dpp v5, v5, v5 quad_perm:[2,3,0,1] row_mask:0xf bank_mask:0xf bound_ctrl:1
	s_nop 1
	v_mov_b32_dpp v6, v5 row_half_mirror row_mask:0xf bank_mask:0xf
	s_and_saveexec_b64 s[2:3], s[0:1]
	s_cbranch_execz .LBB0_3383
	v_add_f32_e32 v5, v5, v6
	v_mul_f32_e32 v5, v3, v5
	s_mov_b32 s12, 0x3e6d3388
	v_mul_f32_e32 v6, v5, v5
	s_waitcnt lgkmcnt(0)
	v_fma_f32 v7, |v5|, s12, 1.0
	v_rcp_f32_e32 v7, v7
	v_mov_b32_e32 v10, 0xbf3a00e3
	v_mul_f32_e32 v6, 0xbf38aa3b, v6
	v_exp_f32_e32 v6, v6
	v_fmac_f32_e32 v10, 0x3f07dc22, v7
	v_fmaak_f32 v10, v7, v10, 0x3f35f0e3
	v_fmaak_f32 v10, v7, v10, 0xbe11a98e
	v_fmaak_f32 v10, v7, v10, 0x3e027906
	v_mul_f32_e32 v7, v7, v10
	v_mul_f32_e32 v6, v6, v7
	v_mul_f32_e32 v7, v5, v6
	v_fma_f32 v6, -v5, v6, v5
	v_cmp_gt_f32_e32 vcc, 0, v5
	s_nop 1
	v_cndmask_b32_e32 v5, v6, v7, vcc
	s_waitcnt vmcnt(1)
	v_mul_f32_e32 v5, v5, v46
	s_waitcnt vmcnt(0)
	v_mul_f32_e32 v5, v5, v66
	ds_write_b32 v2, v5 offset:1728
; __device__ __forceinline__ void p12_peer(Frame& F) {
;     ...
;     for (int i = 0; i < 4; ++i) { const int t = F.gw + i * F.NGW;
; #pragma unroll
;         for (int b = 0; b < 16; ++b) { float d = psum[i][b];
;             d += __builtin_bit_cast(float, __builtin_amdgcn_update_dpp(0, __builtin_bit_cast(int, d), 0xB1, 0xF, 0xF, false));
;             d += __builtin_bit_cast(float, __builtin_amdgcn_update_dpp(0, __builtin_bit_cast(int, d), 0x4E, 0xF, 0xF, false));
;             d += __builtin_bit_cast(float, __builtin_amdgcn_update_dpp(0, __builtin_bit_cast(int, d), 0x141, 0xF, 0xF, false));
;             const int idx = b * 8 + g8; const float w = PGT[(size_t)t * 128 + idx] * gelu_erf(sx[i] * d) * VSC[EL[i * 128 + idx]];
;             if (k8 == 0) WL[i * 128 + idx] = w; } }
.LBB0_3383:
	s_or_b64 exec, exec, s[2:3]
	v_add_f32_dpp v5, v105, v105 quad_perm:[1,0,3,2] row_mask:0xf bank_mask:0xf bound_ctrl:1
	s_nop 1
	v_add_f32_dpp v5, v5, v5 quad_perm:[2,3,0,1] row_mask:0xf bank_mask:0xf bound_ctrl:1
	s_nop 1
	v_mov_b32_dpp v4, v5 row_half_mirror row_mask:0xf bank_mask:0xf
	s_and_saveexec_b64 s[2:3], s[0:1]
	s_cbranch_execz .LBB0_3385
	v_add_f32_e32 v4, v5, v4
	v_mul_f32_e32 v4, v3, v4
	s_mov_b32 s12, 0x3e6d3388
	v_mul_f32_e32 v5, v4, v4
	s_waitcnt lgkmcnt(0)
	v_fma_f32 v6, |v4|, s12, 1.0
	v_rcp_f32_e32 v6, v6
	v_mov_b32_e32 v9, 0xbf3a00e3
	v_mul_f32_e32 v5, 0xbf38aa3b, v5
	v_exp_f32_e32 v5, v5
	v_fmac_f32_e32 v9, 0x3f07dc22, v6
	v_fmaak_f32 v9, v6, v9, 0x3f35f0e3
	v_fmaak_f32 v9, v6, v9, 0xbe11a98e
	v_fmaak_f32 v9, v6, v9, 0x3e027906
	v_mul_f32_e32 v6, v6, v9
	v_mul_f32_e32 v5, v5, v6
	v_mul_f32_e32 v6, v4, v5
	v_fma_f32 v5, -v4, v5, v4
	v_cmp_gt_f32_e32 vcc, 0, v4
	s_nop 1
	v_cndmask_b32_e32 v4, v5, v6, vcc
	s_waitcnt vmcnt(1)
	v_mul_f32_e32 v4, v4, v47
	s_waitcnt vmcnt(0)
	v_mul_f32_e32 v4, v4, v67
	ds_write_b32 v2, v4 offset:1760
.LBB0_3385:
	s_or_b64 exec, exec, s[2:3]
	v_add_f32_dpp v5, v102, v102 quad_perm:[1,0,3,2] row_mask:0xf bank_mask:0xf bound_ctrl:1
	v_mov_b32_e32 v6, 0
	v_mov_b32_e32 v4, 0
	v_add_f32_dpp v5, v5, v5 quad_perm:[2,3,0,1] row_mask:0xf bank_mask:0xf bound_ctrl:1
	s_nop 1
	v_mov_b32_dpp v6, v5 row_half_mirror row_mask:0xf bank_mask:0xf
	s_and_saveexec_b64 s[2:3], s[0:1]
	s_cbranch_execz .LBB0_3387
	v_add_f32_e32 v5, v5, v6
	v_mul_f32_e32 v5, v3, v5
	s_mov_b32 s12, 0x3e6d3388
	v_mul_f32_e32 v6, v5, v5
	s_waitcnt lgkmcnt(0)
	v_fma_f32 v7, |v5|, s12, 1.0
	v_rcp_f32_e32 v7, v7
	v_mov_b32_e32 v10, 0xbf3a00e3
	v_mul_f32_e32 v6, 0xbf38aa3b, v6
	v_exp_f32_e32 v6, v6
	v_fmac_f32_e32 v10, 0x3f07dc22, v7
	v_fmaak_f32 v10, v7, v10, 0x3f35f0e3
	v_fmaak_f32 v10, v7, v10, 0xbe11a98e
	v_fmaak_f32 v10, v7, v10, 0x3e027906
	v_mul_f32_e32 v7, v7, v10
	v_mul_f32_e32 v6, v6, v7
	v_mul_f32_e32 v7, v5, v6
	v_fma_f32 v6, -v5, v6, v5
	v_cmp_gt_f32_e32 vcc, 0, v5
	s_nop 1
	v_cndmask_b32_e32 v5, v6, v7, vcc
	s_waitcnt vmcnt(1)
	v_mul_f32_e32 v5, v5, v48
	s_waitcnt vmcnt(0)
	v_mul_f32_e32 v5, v5, v68
	ds_write_b32 v2, v5 offset:1792
.LBB0_3387:
	s_or_b64 exec, exec, s[2:3]
	v_add_f32_dpp v5, v103, v103 quad_perm:[1,0,3,2] row_mask:0xf bank_mask:0xf bound_ctrl:1
	s_nop 1
	v_add_f32_dpp v5, v5, v5 quad_perm:[2,3,0,1] row_mask:0xf bank_mask:0xf bound_ctrl:1
	s_nop 1
	v_mov_b32_dpp v4, v5 row_half_mirror row_mask:0xf bank_mask:0xf
	s_and_saveexec_b64 s[2:3], s[0:1]
	s_cbranch_execz .LBB0_3389
	v_add_f32_e32 v4, v5, v4
	v_mul_f32_e32 v4, v3, v4
	s_mov_b32 s12, 0x3e6d3388
	v_mul_f32_e32 v5, v4, v4
	s_waitcnt lgkmcnt(0)
	v_fma_f32 v6, |v4|, s12, 1.0
	v_rcp_f32_e32 v6, v6
	v_mov_b32_e32 v9, 0xbf3a00e3
	v_mul_f32_e32 v5, 0xbf38aa3b, v5
	v_exp_f32_e32 v5, v5
	v_fmac_f32_e32 v9, 0x3f07dc22, v6
	v_fmaak_f32 v9, v6, v9, 0x3f35f0e3
	v_fmaak_f32 v9, v6, v9, 0xbe11a98e
	v_fmaak_f32 v9, v6, v9, 0x3e027906
	v_mul_f32_e32 v6, v6, v9
	v_mul_f32_e32 v5, v5, v6
	v_mul_f32_e32 v6, v4, v5
	v_fma_f32 v5, -v4, v5, v4
	v_cmp_gt_f32_e32 vcc, 0, v4
	s_nop 1
	v_cndmask_b32_e32 v4, v5, v6, vcc
	s_waitcnt vmcnt(1)
	v_mul_f32_e32 v4, v4, v49
	s_waitcnt vmcnt(0)
	v_mul_f32_e32 v4, v4, v69
	ds_write_b32 v2, v4 offset:1824
.LBB0_3389:
	s_or_b64 exec, exec, s[2:3]
	v_add_f32_dpp v5, v100, v100 quad_perm:[1,0,3,2] row_mask:0xf bank_mask:0xf bound_ctrl:1
	v_mov_b32_e32 v6, 0
	v_mov_b32_e32 v4, 0
	v_add_f32_dpp v5, v5, v5 quad_perm:[2,3,0,1] row_mask:0xf bank_mask:0xf bound_ctrl:1
	s_nop 1
	v_mov_b32_dpp v6, v5 row_half_mirror row_mask:0xf bank_mask:0xf
	s_and_saveexec_b64 s[2:3], s[0:1]
	s_cbranch_execz .LBB0_3391
	v_add_f32_e32 v5, v5, v6
	v_mul_f32_e32 v5, v3, v5
	s_mov_b32 s12, 0x3e6d3388
	v_mul_f32_e32 v6, v5, v5
	s_waitcnt lgkmcnt(0)
	v_fma_f32 v7, |v5|, s12, 1.0
	v_rcp_f32_e32 v7, v7
	v_mov_b32_e32 v10, 0xbf3a00e3
	v_mul_f32_e32 v6, 0xbf38aa3b, v6
	v_exp_f32_e32 v6, v6
	v_fmac_f32_e32 v10, 0x3f07dc22, v7
	v_fmaak_f32 v10, v7, v10, 0x3f35f0e3
	v_fmaak_f32 v10, v7, v10, 0xbe11a98e
	v_fmaak_f32 v10, v7, v10, 0x3e027906
	v_mul_f32_e32 v7, v7, v10
	v_mul_f32_e32 v6, v6, v7
	v_mul_f32_e32 v7, v5, v6
	v_fma_f32 v6, -v5, v6, v5
	v_cmp_gt_f32_e32 vcc, 0, v5
	s_nop 1
	v_cndmask_b32_e32 v5, v6, v7, vcc
	s_waitcnt vmcnt(1)
	v_mul_f32_e32 v5, v5, v50
	s_waitcnt vmcnt(0)
	v_mul_f32_e32 v5, v5, v70
	ds_write_b32 v2, v5 offset:1856
; __device__ __forceinline__ void p12_peer(Frame& F) {
;     ...
;     for (int i = 0; i < 4; ++i) { const int t = F.gw + i * F.NGW;
; #pragma unroll
;         for (int b = 0; b < 16; ++b) { float d = psum[i][b];
;             d += __builtin_bit_cast(float, __builtin_amdgcn_update_dpp(0, __builtin_bit_cast(int, d), 0xB1, 0xF, 0xF, false));
;             d += __builtin_bit_cast(float, __builtin_amdgcn_update_dpp(0, __builtin_bit_cast(int, d), 0x4E, 0xF, 0xF, false));
;             d += __builtin_bit_cast(float, __builtin_amdgcn_update_dpp(0, __builtin_bit_cast(int, d), 0x141, 0xF, 0xF, false));
;             const int idx = b * 8 + g8; const float w = PGT[(size_t)t * 128 + idx] * gelu_erf(sx[i] * d) * VSC[EL[i * 128 + idx]];
;             if (k8 == 0) WL[i * 128 + idx] = w; } }
.LBB0_3391:
	s_or_b64 exec, exec, s[2:3]
	v_add_f32_dpp v5, v101, v101 quad_perm:[1,0,3,2] row_mask:0xf bank_mask:0xf bound_ctrl:1
	s_nop 1
	v_add_f32_dpp v5, v5, v5 quad_perm:[2,3,0,1] row_mask:0xf bank_mask:0xf bound_ctrl:1
	s_nop 1
	v_mov_b32_dpp v4, v5 row_half_mirror row_mask:0xf bank_mask:0xf
	s_and_saveexec_b64 s[2:3], s[0:1]
	s_cbranch_execz .LBB0_3393
	v_add_f32_e32 v4, v5, v4
	v_mul_f32_e32 v4, v3, v4
	s_mov_b32 s12, 0x3e6d3388
	v_mul_f32_e32 v5, v4, v4
	s_waitcnt lgkmcnt(0)
	v_fma_f32 v6, |v4|, s12, 1.0
	v_rcp_f32_e32 v6, v6
	v_mov_b32_e32 v9, 0xbf3a00e3
	v_mul_f32_e32 v5, 0xbf38aa3b, v5
	v_exp_f32_e32 v5, v5
	v_fmac_f32_e32 v9, 0x3f07dc22, v6
	v_fmaak_f32 v9, v6, v9, 0x3f35f0e3
	v_fmaak_f32 v9, v6, v9, 0xbe11a98e
	v_fmaak_f32 v9, v6, v9, 0x3e027906
	v_mul_f32_e32 v6, v6, v9
	v_mul_f32_e32 v5, v5, v6
	v_mul_f32_e32 v6, v4, v5
	v_fma_f32 v5, -v4, v5, v4
	v_cmp_gt_f32_e32 vcc, 0, v4
	s_nop 1
	v_cndmask_b32_e32 v4, v5, v6, vcc
	s_waitcnt vmcnt(1)
	v_mul_f32_e32 v4, v4, v51
	s_waitcnt vmcnt(0)
	v_mul_f32_e32 v4, v4, v71
	ds_write_b32 v2, v4 offset:1888
.LBB0_3393:
	s_or_b64 exec, exec, s[2:3]
	v_add_f32_dpp v5, v98, v98 quad_perm:[1,0,3,2] row_mask:0xf bank_mask:0xf bound_ctrl:1
	v_mov_b32_e32 v6, 0
	v_mov_b32_e32 v4, 0
	v_add_f32_dpp v5, v5, v5 quad_perm:[2,3,0,1] row_mask:0xf bank_mask:0xf bound_ctrl:1
	s_nop 1
	v_mov_b32_dpp v6, v5 row_half_mirror row_mask:0xf bank_mask:0xf
	s_and_saveexec_b64 s[2:3], s[0:1]
	s_cbranch_execz .LBB0_3395
	v_add_f32_e32 v5, v5, v6
	v_mul_f32_e32 v5, v3, v5
	s_mov_b32 s12, 0x3e6d3388
	v_mul_f32_e32 v6, v5, v5
	s_waitcnt lgkmcnt(0)
	v_fma_f32 v7, |v5|, s12, 1.0
	v_rcp_f32_e32 v7, v7
	v_mov_b32_e32 v10, 0xbf3a00e3
	v_mul_f32_e32 v6, 0xbf38aa3b, v6
	v_exp_f32_e32 v6, v6
	v_fmac_f32_e32 v10, 0x3f07dc22, v7
	v_fmaak_f32 v10, v7, v10, 0x3f35f0e3
	v_fmaak_f32 v10, v7, v10, 0xbe11a98e
	v_fmaak_f32 v10, v7, v10, 0x3e027906
	v_mul_f32_e32 v7, v7, v10
	v_mul_f32_e32 v6, v6, v7
	v_mul_f32_e32 v7, v5, v6
	v_fma_f32 v6, -v5, v6, v5
	v_cmp_gt_f32_e32 vcc, 0, v5
	s_nop 1
	v_cndmask_b32_e32 v5, v6, v7, vcc
	s_waitcnt vmcnt(1)
	v_mul_f32_e32 v5, v5, v52
	s_waitcnt vmcnt(0)
	v_mul_f32_e32 v5, v5, v72
	ds_write_b32 v2, v5 offset:1920
.LBB0_3395:
	s_or_b64 exec, exec, s[2:3]
	v_add_f32_dpp v5, v99, v99 quad_perm:[1,0,3,2] row_mask:0xf bank_mask:0xf bound_ctrl:1
	s_nop 1
	v_add_f32_dpp v5, v5, v5 quad_perm:[2,3,0,1] row_mask:0xf bank_mask:0xf bound_ctrl:1
	s_nop 1
	v_mov_b32_dpp v4, v5 row_half_mirror row_mask:0xf bank_mask:0xf
	s_and_saveexec_b64 s[2:3], s[0:1]
	s_cbranch_execz .LBB0_3397
	v_add_f32_e32 v4, v5, v4
	v_mul_f32_e32 v4, v3, v4
	s_mov_b32 s12, 0x3e6d3388
	v_mul_f32_e32 v5, v4, v4
	s_waitcnt lgkmcnt(0)
	v_fma_f32 v6, |v4|, s12, 1.0
	v_rcp_f32_e32 v6, v6
	v_mov_b32_e32 v9, 0xbf3a00e3
	v_mul_f32_e32 v5, 0xbf38aa3b, v5
	v_exp_f32_e32 v5, v5
	v_fmac_f32_e32 v9, 0x3f07dc22, v6
	v_fmaak_f32 v9, v6, v9, 0x3f35f0e3
	v_fmaak_f32 v9, v6, v9, 0xbe11a98e
	v_fmaak_f32 v9, v6, v9, 0x3e027906
	v_mul_f32_e32 v6, v6, v9
	v_mul_f32_e32 v5, v5, v6
	v_mul_f32_e32 v6, v4, v5
	v_fma_f32 v5, -v4, v5, v4
	v_cmp_gt_f32_e32 vcc, 0, v4
	s_nop 1
	v_cndmask_b32_e32 v4, v5, v6, vcc
	s_waitcnt vmcnt(1)
	v_mul_f32_e32 v4, v4, v53
	s_waitcnt vmcnt(0)
	v_mul_f32_e32 v4, v4, v73
	ds_write_b32 v2, v4 offset:1952
.LBB0_3397:
	s_or_b64 exec, exec, s[2:3]
	v_add_f32_dpp v5, v96, v96 quad_perm:[1,0,3,2] row_mask:0xf bank_mask:0xf bound_ctrl:1
	v_mov_b32_e32 v6, 0
	v_mov_b32_e32 v4, 0
	v_add_f32_dpp v5, v5, v5 quad_perm:[2,3,0,1] row_mask:0xf bank_mask:0xf bound_ctrl:1
	s_nop 1
	v_mov_b32_dpp v6, v5 row_half_mirror row_mask:0xf bank_mask:0xf
	s_and_saveexec_b64 s[2:3], s[0:1]
	s_cbranch_execz .LBB0_3399
	v_add_f32_e32 v5, v5, v6
	v_mul_f32_e32 v5, v3, v5
	s_mov_b32 s12, 0x3e6d3388
	v_mul_f32_e32 v6, v5, v5
	s_waitcnt lgkmcnt(0)
	v_fma_f32 v7, |v5|, s12, 1.0
	v_rcp_f32_e32 v7, v7
	v_mov_b32_e32 v10, 0xbf3a00e3
	v_mul_f32_e32 v6, 0xbf38aa3b, v6
	v_exp_f32_e32 v6, v6
	v_fmac_f32_e32 v10, 0x3f07dc22, v7
	v_fmaak_f32 v10, v7, v10, 0x3f35f0e3
	v_fmaak_f32 v10, v7, v10, 0xbe11a98e
	v_fmaak_f32 v10, v7, v10, 0x3e027906
	v_mul_f32_e32 v7, v7, v10
	v_mul_f32_e32 v6, v6, v7
	v_mul_f32_e32 v7, v5, v6
	v_fma_f32 v6, -v5, v6, v5
	v_cmp_gt_f32_e32 vcc, 0, v5
	s_nop 1
	v_cndmask_b32_e32 v5, v6, v7, vcc
	s_waitcnt vmcnt(1)
	v_mul_f32_e32 v5, v5, v54
	s_waitcnt vmcnt(0)
	v_mul_f32_e32 v5, v5, v74
	ds_write_b32 v2, v5 offset:1984
.LBB0_3399:
	s_or_b64 exec, exec, s[2:3]
	v_add_f32_dpp v5, v97, v97 quad_perm:[1,0,3,2] row_mask:0xf bank_mask:0xf bound_ctrl:1
	s_nop 1
	v_add_f32_dpp v5, v5, v5 quad_perm:[2,3,0,1] row_mask:0xf bank_mask:0xf bound_ctrl:1
	s_nop 1
	v_mov_b32_dpp v4, v5 row_half_mirror row_mask:0xf bank_mask:0xf
	s_and_saveexec_b64 s[2:3], s[0:1]
	s_cbranch_execz .LBB0_3401
	s_mov_b32 s0, 0x3e6d3388
	s_waitcnt lgkmcnt(0)
	v_add_f32_e32 v0, v5, v4
	v_mul_f32_e32 v0, v3, v0
	v_fma_f32 v3, |v0|, s0, 1.0
	v_rcp_f32_e32 v3, v3
	v_mul_f32_e32 v1, v0, v0
	v_mov_b32_e32 v4, 0xbf3a00e3
	v_mul_f32_e32 v1, 0xbf38aa3b, v1
	v_fmac_f32_e32 v4, 0x3f07dc22, v3
	v_exp_f32_e32 v1, v1
	v_fmaak_f32 v4, v3, v4, 0x3f35f0e3
	v_fmaak_f32 v4, v3, v4, 0xbe11a98e
	v_fmaak_f32 v4, v3, v4, 0x3e027906
	v_mul_f32_e32 v3, v3, v4
	v_mul_f32_e32 v1, v1, v3
	v_mul_f32_e32 v3, v0, v1
	v_fma_f32 v1, -v0, v1, v0
	v_cmp_gt_f32_e32 vcc, 0, v0
	s_nop 1
	v_cndmask_b32_e32 v0, v1, v3, vcc
	s_waitcnt vmcnt(1)
	v_mul_f32_e32 v0, v0, v55
	s_waitcnt vmcnt(0)
	v_mul_f32_e32 v0, v0, v75
	ds_write_b32 v2, v0 offset:2016
